# v16 + nt on once-read loads in P5 (retention unit PROJ reads, gate_a), P6 (gate_b, tmp) and P8 (LN2 x1 rows)
# baseline (speedup 1.0000x reference)
.LBB0_937:
	s_or_b64 exec, exec, s[94:95]
	s_add_i32 s0, 0, 0x23800
	v_add_u32_e32 v66, s0, v122
	s_waitcnt lgkmcnt(0)
	s_barrier
	ds_read_b64 v[66:67], v66
	s_lshl_b32 s94, s84, 2
	v_lshl_add_u64 v[138:139], v[138:139], 0, s[88:89]
	s_waitcnt lgkmcnt(0)
	v_sub_f32_e32 v42, v42, v66
	v_sub_f32_e32 v43, v43, v66
	v_sub_f32_e32 v58, v58, v66
	v_sub_f32_e32 v59, v59, v66
	v_mul_f32_e32 v42, v67, v42
	v_mul_f32_e32 v43, v67, v43
	v_mul_f32_e32 v58, v67, v58
	v_mul_f32_e32 v59, v67, v59
	v_cvt_pk_bf16_f32 v42, v42, v43
	v_sub_f32_e32 v43, v44, v66
	v_sub_f32_e32 v44, v45, v66
	v_cvt_pk_bf16_f32 v58, v58, v59
	v_sub_f32_e32 v59, v60, v66
	v_mul_f32_e32 v43, v67, v43
	v_mul_f32_e32 v44, v67, v44
	v_mul_f32_e32 v59, v67, v59
	v_sub_f32_e32 v60, v61, v66
	v_cvt_pk_bf16_f32 v43, v43, v44
	v_add_u32_e32 v44, 0x8800, v206
	v_mul_f32_e32 v60, v67, v60
	v_cvt_pk_bf16_f32 v59, v59, v60
	ds_write2_b64 v44, v[58:59], v[42:43] offset1:4
	v_add_u32_e32 v42, s0, v182
	ds_read_b64 v[42:43], v42
	s_waitcnt lgkmcnt(0)
	v_sub_f32_e32 v14, v14, v42
	v_sub_f32_e32 v15, v15, v42
	v_sub_f32_e32 v30, v30, v42
	v_sub_f32_e32 v31, v31, v42
	v_mul_f32_e32 v14, v43, v14
	v_mul_f32_e32 v15, v43, v15
	v_mul_f32_e32 v30, v43, v30
	v_mul_f32_e32 v31, v43, v31
	v_cvt_pk_bf16_f32 v14, v14, v15
	v_sub_f32_e32 v15, v16, v42
	v_sub_f32_e32 v16, v17, v42
	v_cvt_pk_bf16_f32 v30, v30, v31
	v_sub_f32_e32 v31, v32, v42
	v_mul_f32_e32 v15, v43, v15
	v_mul_f32_e32 v16, v43, v16
	v_mul_f32_e32 v31, v43, v31
	v_sub_f32_e32 v32, v33, v42
	v_cvt_pk_bf16_f32 v15, v15, v16
	v_add_u32_e32 v16, 0xa800, v206
	v_mul_f32_e32 v32, v43, v32
	v_cvt_pk_bf16_f32 v31, v31, v32
	ds_write2_b64 v16, v[30:31], v[14:15] offset0:32 offset1:36
	v_add_u32_e32 v14, s0, v183
	ds_read_b64 v[14:15], v14
	s_waitcnt lgkmcnt(0)
	v_sub_f32_e32 v16, v62, v14
	v_sub_f32_e32 v17, v63, v14
	v_mul_f32_e32 v16, v15, v16
	v_mul_f32_e32 v17, v15, v17
	v_cvt_pk_bf16_f32 v16, v16, v17
	v_sub_f32_e32 v17, v64, v14
	v_sub_f32_e32 v30, v65, v14
	v_mul_f32_e32 v17, v15, v17
	v_mul_f32_e32 v30, v15, v30
	v_cvt_pk_bf16_f32 v17, v17, v30
	v_sub_f32_e32 v30, v46, v14
	v_sub_f32_e32 v31, v47, v14
	v_mul_f32_e32 v30, v15, v30
	v_mul_f32_e32 v31, v15, v31
	v_cvt_pk_bf16_f32 v30, v30, v31
	v_sub_f32_e32 v31, v48, v14
	v_sub_f32_e32 v14, v49, v14
	v_mul_f32_e32 v31, v15, v31
	v_mul_f32_e32 v14, v15, v14
	v_cvt_pk_bf16_f32 v31, v31, v14
	v_add_u32_e32 v14, 0xc800, v206
	ds_write2_b64 v14, v[16:17], v[30:31] offset0:64 offset1:68
	v_add_u32_e32 v14, s0, v184
	ds_read_b64 v[14:15], v14
	s_waitcnt lgkmcnt(0)
	v_sub_f32_e32 v16, v34, v14
	v_sub_f32_e32 v17, v35, v14
	v_sub_f32_e32 v18, v18, v14
	v_sub_f32_e32 v19, v19, v14
	v_mul_f32_e32 v16, v15, v16
	v_mul_f32_e32 v17, v15, v17
	v_mul_f32_e32 v18, v15, v18
	v_mul_f32_e32 v19, v15, v19
	v_cvt_pk_bf16_f32 v16, v16, v17
	v_sub_f32_e32 v17, v36, v14
	v_sub_f32_e32 v30, v37, v14
	v_cvt_pk_bf16_f32 v18, v18, v19
	v_sub_f32_e32 v19, v20, v14
	v_sub_f32_e32 v14, v21, v14
	v_mul_f32_e32 v19, v15, v19
	v_mul_f32_e32 v14, v15, v14
	v_mul_f32_e32 v17, v15, v17
	v_cvt_pk_bf16_f32 v19, v19, v14
	v_add_u32_e32 v14, 0xe800, v206
	v_mul_f32_e32 v30, v15, v30
	v_cvt_pk_bf16_f32 v17, v17, v30
	ds_write2_b64 v14, v[16:17], v[18:19] offset0:96 offset1:100
	v_add_u32_e32 v14, s0, v185
	ds_read_b64 v[14:15], v14
	s_waitcnt lgkmcnt(0)
	v_sub_f32_e32 v16, v54, v14
	v_sub_f32_e32 v17, v55, v14
	v_mul_f32_e32 v16, v15, v16
	v_mul_f32_e32 v17, v15, v17
	v_cvt_pk_bf16_f32 v16, v16, v17
	v_sub_f32_e32 v17, v56, v14
	v_sub_f32_e32 v18, v57, v14
	v_mul_f32_e32 v17, v15, v17
	v_mul_f32_e32 v18, v15, v18
	v_cvt_pk_bf16_f32 v17, v17, v18
	v_sub_f32_e32 v18, v38, v14
	v_sub_f32_e32 v19, v39, v14
	v_mul_f32_e32 v18, v15, v18
	v_mul_f32_e32 v19, v15, v19
	v_cvt_pk_bf16_f32 v18, v18, v19
	v_sub_f32_e32 v19, v40, v14
	v_sub_f32_e32 v14, v41, v14
	v_mul_f32_e32 v19, v15, v19
	v_mul_f32_e32 v14, v15, v14
	v_cvt_pk_bf16_f32 v19, v19, v14
	v_add_u32_e32 v14, 0x8800, v207
	ds_write2_b64 v14, v[16:17], v[18:19] offset1:4
	v_add_u32_e32 v14, s0, v186
	ds_read_b64 v[14:15], v14
	v_or_b32_e32 v38, s11, v167
	v_mul_lo_u32 v124, v38, s96
	s_waitcnt lgkmcnt(0)
	v_sub_f32_e32 v6, v6, v14
	v_sub_f32_e32 v7, v7, v14
	v_sub_f32_e32 v16, v22, v14
	v_sub_f32_e32 v17, v23, v14
	v_mul_f32_e32 v6, v15, v6
	v_mul_f32_e32 v7, v15, v7
	v_mul_f32_e32 v16, v15, v16
	v_mul_f32_e32 v17, v15, v17
	v_cvt_pk_bf16_f32 v6, v6, v7
	v_sub_f32_e32 v7, v8, v14
	v_sub_f32_e32 v8, v9, v14
	v_cvt_pk_bf16_f32 v16, v16, v17
	v_sub_f32_e32 v17, v24, v14
	v_mul_f32_e32 v7, v15, v7
	v_mul_f32_e32 v8, v15, v8
	v_mul_f32_e32 v17, v15, v17
	v_sub_f32_e32 v18, v25, v14
	v_cvt_pk_bf16_f32 v7, v7, v8
	v_add_u32_e32 v8, 0xa800, v207
	v_mul_f32_e32 v18, v15, v18
	v_cvt_pk_bf16_f32 v17, v17, v18
	ds_write2_b64 v8, v[16:17], v[6:7] offset0:32 offset1:36
	v_add_u32_e32 v6, s0, v187
	ds_read_b64 v[6:7], v6
	s_waitcnt lgkmcnt(0)
	v_sub_f32_e32 v8, v26, v6
	v_sub_f32_e32 v9, v27, v6
	v_sub_f32_e32 v10, v10, v6
	v_sub_f32_e32 v11, v11, v6
	v_mul_f32_e32 v8, v7, v8
	v_mul_f32_e32 v9, v7, v9
	v_mul_f32_e32 v10, v7, v10
	v_mul_f32_e32 v11, v7, v11
	v_cvt_pk_bf16_f32 v8, v8, v9
	v_sub_f32_e32 v9, v28, v6
	v_sub_f32_e32 v14, v29, v6
	v_cvt_pk_bf16_f32 v10, v10, v11
	v_sub_f32_e32 v11, v12, v6
	v_sub_f32_e32 v6, v13, v6
	v_mul_f32_e32 v11, v7, v11
	v_mul_f32_e32 v6, v7, v6
	v_mul_f32_e32 v9, v7, v9
	v_cvt_pk_bf16_f32 v11, v11, v6
	v_add_u32_e32 v6, 0xc800, v207
	v_mul_f32_e32 v14, v7, v14
	v_cvt_pk_bf16_f32 v9, v9, v14
	ds_write2_b64 v6, v[8:9], v[10:11] offset0:64 offset1:68
	v_add_u32_e32 v6, s0, v188
	ds_read_b64 v[6:7], v6
	s_waitcnt lgkmcnt(0)
	v_sub_f32_e32 v2, v2, v6
	v_sub_f32_e32 v3, v3, v6
	v_mul_f32_e32 v2, v7, v2
	v_mul_f32_e32 v3, v7, v3
	v_cvt_pk_bf16_f32 v2, v2, v3
	v_sub_f32_e32 v3, v4, v6
	v_sub_f32_e32 v4, v5, v6
	v_mul_f32_e32 v3, v7, v3
	v_mul_f32_e32 v4, v7, v4
	v_cvt_pk_bf16_f32 v3, v3, v4
	v_sub_f32_e32 v4, v50, v6
	v_sub_f32_e32 v5, v51, v6
	v_mul_f32_e32 v4, v7, v4
	v_mul_f32_e32 v5, v7, v5
	v_cvt_pk_bf16_f32 v4, v4, v5
	v_sub_f32_e32 v5, v52, v6
	v_sub_f32_e32 v6, v53, v6
	v_mul_f32_e32 v5, v7, v5
	v_mul_f32_e32 v6, v7, v6
	v_cvt_pk_bf16_f32 v5, v5, v6
	v_add_u32_e32 v6, 0xe800, v207
	ds_write2_b64 v6, v[2:3], v[4:5] offset0:96 offset1:100
	v_mov_b32_e32 v2, s80
	s_waitcnt lgkmcnt(0)
	s_barrier
	ds_read_b64 v[2:3], v2
	v_lshlrev_b32_e32 v4, 1, v136
	v_mov_b32_e32 v5, v125
	s_waitcnt lgkmcnt(0)
	v_readfirstlane_b32 s0, v2
	v_readfirstlane_b32 s1, v3
	s_add_u32 s0, s0, s94
	s_addc_u32 s1, s1, 0
	v_lshlrev_b32_e32 v2, 2, v136
	s_nop 1
	global_load_dwordx4 v[34:37], v2, s[0:1] offset:16 nt
	global_load_dwordx4 v[40:43], v2, s[0:1] nt
	v_lshl_add_u64 v[2:3], v[124:125], 1, s[82:83]
	s_lshl_b32 s0, s84, 1
	s_mov_b32 s1, s85
	v_lshl_add_u64 v[2:3], v[2:3], 0, s[0:1]
	v_lshl_add_u64 v[2:3], v[2:3], 0, v[4:5]
	v_add_co_u32_e32 v2, vcc, s8, v2
	s_add_i32 s10, s10, s52
	s_nop 0
	v_addc_co_u32_e32 v3, vcc, 0, v3, vcc
	global_load_dwordx4 v[30:33], v[2:3], off offset:2048 nt
	v_add_u32_e32 v2, 0x4c000, v124
	v_mov_b32_e32 v3, v125
	v_lshl_add_u64 v[2:3], v[2:3], 1, s[82:83]
	v_lshl_add_u64 v[2:3], v[2:3], 0, s[0:1]
	v_lshl_add_u64 v[2:3], v[2:3], 0, v[4:5]
	v_add_co_u32_e32 v2, vcc, s8, v2
	s_add_i32 s81, s81, s33
	s_nop 0
	v_addc_co_u32_e32 v3, vcc, 0, v3, vcc
	global_load_dwordx4 v[26:29], v[2:3], off offset:2048 nt
	v_add_u32_e32 v2, 0x98000, v124
	v_mov_b32_e32 v3, v125
	v_lshl_add_u64 v[2:3], v[2:3], 1, s[82:83]
	v_lshl_add_u64 v[2:3], v[2:3], 0, s[0:1]
	v_lshl_add_u64 v[2:3], v[2:3], 0, v[4:5]
	v_add_co_u32_e32 v2, vcc, s8, v2
	s_cmpk_lt_i32 s10, 0x200
	s_nop 0
	v_addc_co_u32_e32 v3, vcc, 0, v3, vcc
	global_load_dwordx4 v[22:25], v[2:3], off offset:2048 nt
	v_add_u32_e32 v2, 0xe4000, v124
	v_mov_b32_e32 v3, v125
	v_lshl_add_u64 v[2:3], v[2:3], 1, s[82:83]
	v_lshl_add_u64 v[2:3], v[2:3], 0, s[0:1]
	v_lshl_add_u64 v[2:3], v[2:3], 0, v[4:5]
	v_add_co_u32_e32 v2, vcc, s8, v2
	s_waitcnt vmcnt(3)
	v_mul_f32_e32 v47, 0x41800000, v40
	v_addc_co_u32_e32 v3, vcc, 0, v3, vcc
	global_load_dwordx4 v[18:21], v[2:3], off offset:2048 nt
	v_add_u32_e32 v2, 0x130000, v124
	v_mov_b32_e32 v3, v125
	v_lshl_add_u64 v[2:3], v[2:3], 1, s[82:83]
	v_lshl_add_u64 v[2:3], v[2:3], 0, s[0:1]
	v_lshl_add_u64 v[2:3], v[2:3], 0, v[4:5]
	v_add_co_u32_e32 v2, vcc, s8, v2
	s_waitcnt vmcnt(3)
	v_lshlrev_b32_e32 v48, 16, v30
	v_addc_co_u32_e32 v3, vcc, 0, v3, vcc
	global_load_dwordx4 v[14:17], v[2:3], off offset:2048 nt
	v_add_u32_e32 v2, 0x17c000, v124
	v_mov_b32_e32 v3, v125
	v_lshl_add_u64 v[2:3], v[2:3], 1, s[82:83]
	v_lshl_add_u64 v[2:3], v[2:3], 0, s[0:1]
	v_lshl_add_u64 v[2:3], v[2:3], 0, v[4:5]
	v_add_co_u32_e32 v2, vcc, s8, v2
	v_mul_f32_e32 v49, 0xbfb8aa3b, v48
	s_nop 0
	v_addc_co_u32_e32 v3, vcc, 0, v3, vcc
	global_load_dwordx4 v[10:13], v[2:3], off offset:2048 nt
	v_add_u32_e32 v2, 0x1c8000, v124
	v_mov_b32_e32 v3, v125
	v_lshl_add_u64 v[2:3], v[2:3], 1, s[82:83]
	v_lshl_add_u64 v[2:3], v[2:3], 0, s[0:1]
	v_exp_f32_e32 v49, v49
	v_lshl_add_u64 v[2:3], v[2:3], 0, v[4:5]
	v_add_co_u32_e32 v2, vcc, s8, v2
	v_add_u32_e32 v124, 0x214000, v124
	s_nop 0
	v_addc_co_u32_e32 v3, vcc, 0, v3, vcc
	global_load_dwordx4 v[6:9], v[2:3], off offset:2048 nt
	v_lshl_add_u64 v[2:3], v[124:125], 1, s[82:83]
	v_add_f32_e32 v49, 1.0, v49
	v_lshl_add_u64 v[2:3], v[2:3], 0, s[0:1]
	v_lshl_add_u64 v[2:3], v[2:3], 0, v[4:5]
	v_add_co_u32_e32 v2, vcc, s8, v2
	s_nop 0
	s_nop 0
	v_addc_co_u32_e32 v3, vcc, 0, v3, vcc
	v_mul_f32_e32 v46, 0x41800000, v41
	v_mul_f32_e32 v45, 0x41800000, v42
	v_mul_f32_e32 v44, 0x41800000, v43
	v_mul_f32_e32 v43, 0x41800000, v34
	v_mul_f32_e32 v42, 0x41800000, v35
	v_mul_f32_e32 v41, 0x41800000, v36
	v_mul_f32_e32 v40, 0x41800000, v37
	ds_read_b128 v[34:37], v208 offset:34816
	s_waitcnt lgkmcnt(0)
	v_lshlrev_b32_e32 v39, 16, v34
	v_mul_f32_e32 v39, v47, v39
	v_rcp_f32_e32 v50, v49
	s_nop 0
	v_mul_f32_e32 v48, v48, v50
	v_and_b32_e32 v30, 0xffff0000, v30
	v_mul_f32_e32 v39, v48, v39
	v_mul_f32_e32 v48, 0xbfb8aa3b, v30
	v_exp_f32_e32 v48, v48
	v_and_b32_e32 v34, 0xffff0000, v34
	v_mul_f32_e32 v34, v46, v34
	global_load_dwordx4 v[2:5], v[2:3], off offset:2048 nt
	v_add_f32_e32 v48, 1.0, v48
	v_or_b32_e32 v124, s11, v189
	v_rcp_f32_e32 v49, v48
	s_nop 0
	v_mul_f32_e32 v30, v30, v49
	v_lshlrev_b32_e32 v48, 16, v31
	v_mul_f32_e32 v49, 0xbfb8aa3b, v48
	v_exp_f32_e32 v49, v49
	v_mul_f32_e32 v30, v30, v34
	v_lshlrev_b32_e32 v34, 16, v35
	v_mul_f32_e32 v34, v45, v34
	v_add_f32_e32 v49, 1.0, v49
	v_and_b32_e32 v31, 0xffff0000, v31
	v_and_b32_e32 v35, 0xffff0000, v35
	v_mul_f32_e32 v35, v44, v35
	v_rcp_f32_e32 v50, v49
	s_nop 0
	v_mul_f32_e32 v48, v48, v50
	v_mul_f32_e32 v34, v48, v34
	v_mul_f32_e32 v48, 0xbfb8aa3b, v31
	v_exp_f32_e32 v48, v48
	v_med3_f32 v34, v34, s9, v214
	v_add_f32_e32 v48, 1.0, v48
	s_nop 0
	v_rcp_f32_e32 v49, v48
	s_nop 0
	v_mul_f32_e32 v31, v31, v49
	v_mul_f32_e32 v31, v31, v35
	v_med3_f32 v35, v39, s9, v214
	v_med3_f32 v39, v30, s9, v214
	v_mov_b32_e32 v30, v125
	v_cvt_pk_fp8_f32 v30, v35, v39
	v_med3_f32 v31, v31, s9, v214
	v_cvt_pk_fp8_f32 v30, v34, v31 op_sel:[0,0,1]
	v_lshlrev_b32_e32 v34, 16, v32
	v_mul_f32_e32 v35, 0xbfb8aa3b, v34
	v_exp_f32_e32 v35, v35
	v_and_b32_e32 v32, 0xffff0000, v32
	v_lshlrev_b32_e32 v31, 16, v36
	v_mul_f32_e32 v31, v43, v31
	v_add_f32_e32 v35, 1.0, v35
	s_nop 0
	v_rcp_f32_e32 v39, v35
	s_nop 0
	v_mul_f32_e32 v34, v34, v39
	v_mul_f32_e32 v35, 0xbfb8aa3b, v32
	v_exp_f32_e32 v35, v35
	v_mul_f32_e32 v31, v34, v31
	v_and_b32_e32 v34, 0xffff0000, v36
	v_mul_f32_e32 v34, v42, v34
	v_add_f32_e32 v35, 1.0, v35
	s_nop 0
	v_rcp_f32_e32 v36, v35
	s_nop 0
	v_mul_f32_e32 v32, v32, v36
	v_lshlrev_b32_e32 v35, 16, v33
	v_mul_f32_e32 v36, 0xbfb8aa3b, v35
	v_exp_f32_e32 v36, v36
	v_and_b32_e32 v33, 0xffff0000, v33
	v_mul_f32_e32 v32, v32, v34
	v_lshlrev_b32_e32 v34, 16, v37
	v_add_f32_e32 v36, 1.0, v36
	v_mul_f32_e32 v34, v41, v34
	v_med3_f32 v32, v32, s9, v214
	v_rcp_f32_e32 v39, v36
	s_nop 0
	v_mul_f32_e32 v35, v35, v39
	v_mul_f32_e32 v36, 0xbfb8aa3b, v33
	v_exp_f32_e32 v36, v36
	v_mul_f32_e32 v34, v35, v34
	v_and_b32_e32 v35, 0xffff0000, v37
	v_mul_f32_e32 v35, v40, v35
	v_add_f32_e32 v36, 1.0, v36
	v_med3_f32 v34, v34, s9, v214
	v_rcp_f32_e32 v37, v36
	s_nop 0
	v_mul_f32_e32 v33, v33, v37
	v_mul_f32_e32 v33, v33, v35
	v_med3_f32 v35, v31, s9, v214
	v_mov_b32_e32 v31, v125
	v_cvt_pk_fp8_f32 v31, v35, v32
	s_waitcnt vmcnt(6)
	v_lshlrev_b32_e32 v35, 16, v26
	v_mul_f32_e32 v36, 0xbfb8aa3b, v35
	v_exp_f32_e32 v36, v36
	v_med3_f32 v33, v33, s9, v214
	v_mov_b32_e32 v39, v125
	v_cvt_pk_fp8_f32 v31, v34, v33 op_sel:[0,0,1]
	v_add_f32_e32 v36, 1.0, v36
	v_lshlrev_b64 v[32:33], 11, v[38:39]
	v_lshl_add_u64 v[32:33], s[86:87], 0, v[32:33]
	v_lshl_add_u64 v[32:33], v[32:33], 0, s[84:85]
	v_lshl_add_u64 v[32:33], v[32:33], 0, v[136:137]
	global_store_dwordx2 v[32:33], v[30:31], off
	ds_read_b128 v[30:33], v208 offset:43264
	s_waitcnt lgkmcnt(0)
	v_lshlrev_b32_e32 v34, 16, v30
	v_mul_f32_e32 v34, v47, v34
	v_rcp_f32_e32 v37, v36
	s_nop 0
	v_mul_f32_e32 v35, v35, v37
	v_and_b32_e32 v26, 0xffff0000, v26
	v_mul_f32_e32 v34, v35, v34
	v_mul_f32_e32 v35, 0xbfb8aa3b, v26
	v_exp_f32_e32 v35, v35
	v_and_b32_e32 v30, 0xffff0000, v30
	v_mul_f32_e32 v30, v46, v30
	v_add_f32_e32 v35, 1.0, v35
	s_nop 0
	v_rcp_f32_e32 v36, v35
	s_nop 0
	v_mul_f32_e32 v26, v26, v36
	v_lshlrev_b32_e32 v35, 16, v27
	v_mul_f32_e32 v36, 0xbfb8aa3b, v35
	v_exp_f32_e32 v36, v36
	v_mul_f32_e32 v26, v26, v30
	v_lshlrev_b32_e32 v30, 16, v31
	v_mul_f32_e32 v30, v45, v30
	v_add_f32_e32 v36, 1.0, v36
	v_and_b32_e32 v27, 0xffff0000, v27
	v_and_b32_e32 v31, 0xffff0000, v31
	v_mul_f32_e32 v31, v44, v31
	v_rcp_f32_e32 v37, v36
	s_nop 0
	v_mul_f32_e32 v35, v35, v37
	v_mul_f32_e32 v30, v35, v30
	v_mul_f32_e32 v35, 0xbfb8aa3b, v27
	v_exp_f32_e32 v35, v35
	v_med3_f32 v30, v30, s9, v214
	v_add_f32_e32 v35, 1.0, v35
	s_nop 0
	v_rcp_f32_e32 v36, v35
	s_nop 0
	v_mul_f32_e32 v27, v27, v36
	v_mul_f32_e32 v27, v27, v31
	v_med3_f32 v31, v34, s9, v214
	v_med3_f32 v34, v26, s9, v214
	v_mov_b32_e32 v26, v125
	v_cvt_pk_fp8_f32 v26, v31, v34
	v_med3_f32 v27, v27, s9, v214
	v_cvt_pk_fp8_f32 v26, v30, v27 op_sel:[0,0,1]
	v_lshlrev_b32_e32 v30, 16, v28
	v_mul_f32_e32 v31, 0xbfb8aa3b, v30
	v_exp_f32_e32 v31, v31
	v_and_b32_e32 v28, 0xffff0000, v28
	v_lshlrev_b32_e32 v27, 16, v32
	v_mul_f32_e32 v27, v43, v27
	v_add_f32_e32 v31, 1.0, v31
	s_nop 0
	v_rcp_f32_e32 v34, v31
	s_nop 0
	v_mul_f32_e32 v30, v30, v34
	v_mul_f32_e32 v31, 0xbfb8aa3b, v28
	v_exp_f32_e32 v31, v31
	v_mul_f32_e32 v27, v30, v27
	v_and_b32_e32 v30, 0xffff0000, v32
	v_mul_f32_e32 v30, v42, v30
	v_add_f32_e32 v31, 1.0, v31
	s_nop 0
	v_rcp_f32_e32 v32, v31
	s_nop 0
	v_mul_f32_e32 v28, v28, v32
	v_lshlrev_b32_e32 v31, 16, v29
	v_mul_f32_e32 v32, 0xbfb8aa3b, v31
	v_exp_f32_e32 v32, v32
	v_and_b32_e32 v29, 0xffff0000, v29
	v_mul_f32_e32 v28, v28, v30
	v_lshlrev_b32_e32 v30, 16, v33
	v_add_f32_e32 v32, 1.0, v32
	v_mul_f32_e32 v30, v41, v30
	v_med3_f32 v28, v28, s9, v214
	v_rcp_f32_e32 v34, v32
	s_nop 0
	v_mul_f32_e32 v31, v31, v34
	v_mul_f32_e32 v32, 0xbfb8aa3b, v29
	v_exp_f32_e32 v32, v32
	v_mul_f32_e32 v30, v31, v30
	v_and_b32_e32 v31, 0xffff0000, v33
	v_mul_f32_e32 v31, v40, v31
	v_add_f32_e32 v32, 1.0, v32
	v_med3_f32 v30, v30, s9, v214
	v_rcp_f32_e32 v33, v32
	s_nop 0
	v_mul_f32_e32 v29, v29, v33
	v_mul_f32_e32 v29, v29, v31
	v_med3_f32 v31, v27, s9, v214
	v_mov_b32_e32 v27, v125
	v_cvt_pk_fp8_f32 v27, v31, v28
	s_waitcnt vmcnt(6)
	v_lshlrev_b32_e32 v31, 16, v22
	v_mul_f32_e32 v32, 0xbfb8aa3b, v31
	v_exp_f32_e32 v32, v32
	v_med3_f32 v29, v29, s9, v214
	v_cvt_pk_fp8_f32 v27, v30, v29 op_sel:[0,0,1]
	v_lshlrev_b64 v[28:29], 11, v[124:125]
	v_add_f32_e32 v32, 1.0, v32
	v_lshl_add_u64 v[28:29], s[86:87], 0, v[28:29]
	v_lshl_add_u64 v[28:29], v[28:29], 0, s[84:85]
	v_lshl_add_u64 v[28:29], v[28:29], 0, v[136:137]
	global_store_dwordx2 v[28:29], v[26:27], off
	ds_read_b128 v[26:29], v208 offset:51712
	s_waitcnt lgkmcnt(0)
	v_lshlrev_b32_e32 v30, 16, v26
	v_mul_f32_e32 v30, v47, v30
	v_rcp_f32_e32 v33, v32
	s_nop 0
	v_mul_f32_e32 v31, v31, v33
	v_and_b32_e32 v22, 0xffff0000, v22
	v_mul_f32_e32 v30, v31, v30
	v_mul_f32_e32 v31, 0xbfb8aa3b, v22
	v_exp_f32_e32 v31, v31
	v_and_b32_e32 v26, 0xffff0000, v26
	v_mul_f32_e32 v26, v46, v26
	v_or_b32_e32 v124, s11, v190
	v_add_f32_e32 v31, 1.0, v31
	s_nop 0
	v_rcp_f32_e32 v32, v31
	s_nop 0
	v_mul_f32_e32 v22, v22, v32
	v_lshlrev_b32_e32 v31, 16, v23
	v_mul_f32_e32 v32, 0xbfb8aa3b, v31
	v_exp_f32_e32 v32, v32
	v_mul_f32_e32 v22, v22, v26
	v_lshlrev_b32_e32 v26, 16, v27
	v_mul_f32_e32 v26, v45, v26
	v_add_f32_e32 v32, 1.0, v32
	v_and_b32_e32 v23, 0xffff0000, v23
	v_and_b32_e32 v27, 0xffff0000, v27
	v_mul_f32_e32 v27, v44, v27
	v_rcp_f32_e32 v33, v32
	s_nop 0
	v_mul_f32_e32 v31, v31, v33
	v_mul_f32_e32 v26, v31, v26
	v_mul_f32_e32 v31, 0xbfb8aa3b, v23
	v_exp_f32_e32 v31, v31
	v_med3_f32 v26, v26, s9, v214
	v_add_f32_e32 v31, 1.0, v31
	s_nop 0
	v_rcp_f32_e32 v32, v31
	s_nop 0
	v_mul_f32_e32 v23, v23, v32
	v_mul_f32_e32 v23, v23, v27
	v_med3_f32 v27, v30, s9, v214
	v_med3_f32 v30, v22, s9, v214
	v_mov_b32_e32 v22, v125
	v_cvt_pk_fp8_f32 v22, v27, v30
	v_med3_f32 v23, v23, s9, v214
	v_cvt_pk_fp8_f32 v22, v26, v23 op_sel:[0,0,1]
	v_lshlrev_b32_e32 v26, 16, v24
	v_mul_f32_e32 v27, 0xbfb8aa3b, v26
	v_exp_f32_e32 v27, v27
	v_and_b32_e32 v24, 0xffff0000, v24
	v_lshlrev_b32_e32 v23, 16, v28
	v_mul_f32_e32 v23, v43, v23
	v_add_f32_e32 v27, 1.0, v27
	s_nop 0
	v_rcp_f32_e32 v30, v27
	s_nop 0
	v_mul_f32_e32 v26, v26, v30
	v_mul_f32_e32 v27, 0xbfb8aa3b, v24
	v_exp_f32_e32 v27, v27
	v_mul_f32_e32 v23, v26, v23
	v_and_b32_e32 v26, 0xffff0000, v28
	v_mul_f32_e32 v26, v42, v26
	v_add_f32_e32 v27, 1.0, v27
	s_nop 0
	v_rcp_f32_e32 v28, v27
	s_nop 0
	v_mul_f32_e32 v24, v24, v28
	v_lshlrev_b32_e32 v27, 16, v25
	v_mul_f32_e32 v28, 0xbfb8aa3b, v27
	v_exp_f32_e32 v28, v28
	v_and_b32_e32 v25, 0xffff0000, v25
	v_mul_f32_e32 v24, v24, v26
	v_lshlrev_b32_e32 v26, 16, v29
	v_add_f32_e32 v28, 1.0, v28
	v_mul_f32_e32 v26, v41, v26
	v_med3_f32 v24, v24, s9, v214
	v_rcp_f32_e32 v30, v28
	s_nop 0
	v_mul_f32_e32 v27, v27, v30
	v_mul_f32_e32 v28, 0xbfb8aa3b, v25
	v_exp_f32_e32 v28, v28
	v_mul_f32_e32 v26, v27, v26
	v_and_b32_e32 v27, 0xffff0000, v29
	v_mul_f32_e32 v27, v40, v27
	v_add_f32_e32 v28, 1.0, v28
	v_med3_f32 v26, v26, s9, v214
	v_rcp_f32_e32 v29, v28
	s_nop 0
	v_mul_f32_e32 v25, v25, v29
	v_mul_f32_e32 v25, v25, v27
	v_med3_f32 v27, v23, s9, v214
	v_mov_b32_e32 v23, v125
	v_cvt_pk_fp8_f32 v23, v27, v24
	s_waitcnt vmcnt(6)
	v_lshlrev_b32_e32 v27, 16, v18
	v_mul_f32_e32 v28, 0xbfb8aa3b, v27
	v_exp_f32_e32 v28, v28
	v_med3_f32 v25, v25, s9, v214
	v_cvt_pk_fp8_f32 v23, v26, v25 op_sel:[0,0,1]
	v_lshlrev_b64 v[24:25], 11, v[124:125]
	v_add_f32_e32 v28, 1.0, v28
	v_lshl_add_u64 v[24:25], s[86:87], 0, v[24:25]
	v_lshl_add_u64 v[24:25], v[24:25], 0, s[84:85]
	v_lshl_add_u64 v[24:25], v[24:25], 0, v[136:137]
	global_store_dwordx2 v[24:25], v[22:23], off
	ds_read_b128 v[22:25], v208 offset:60160
	s_waitcnt lgkmcnt(0)
	v_lshlrev_b32_e32 v26, 16, v22
	v_mul_f32_e32 v26, v47, v26
	v_rcp_f32_e32 v29, v28
	s_nop 0
	v_mul_f32_e32 v27, v27, v29
	v_and_b32_e32 v18, 0xffff0000, v18
	v_mul_f32_e32 v26, v27, v26
	v_mul_f32_e32 v27, 0xbfb8aa3b, v18
	v_exp_f32_e32 v27, v27
	v_and_b32_e32 v22, 0xffff0000, v22
	v_mul_f32_e32 v22, v46, v22
	v_or_b32_e32 v124, s11, v191
	v_add_f32_e32 v27, 1.0, v27
	s_nop 0
	v_rcp_f32_e32 v28, v27
	s_nop 0
	v_mul_f32_e32 v18, v18, v28
	v_lshlrev_b32_e32 v27, 16, v19
	v_mul_f32_e32 v28, 0xbfb8aa3b, v27
	v_exp_f32_e32 v28, v28
	v_mul_f32_e32 v18, v18, v22
	v_lshlrev_b32_e32 v22, 16, v23
	v_mul_f32_e32 v22, v45, v22
	v_add_f32_e32 v28, 1.0, v28
	v_and_b32_e32 v19, 0xffff0000, v19
	v_and_b32_e32 v23, 0xffff0000, v23
	v_mul_f32_e32 v23, v44, v23
	v_rcp_f32_e32 v29, v28
	s_nop 0
	v_mul_f32_e32 v27, v27, v29
	v_mul_f32_e32 v22, v27, v22
	v_mul_f32_e32 v27, 0xbfb8aa3b, v19
	v_exp_f32_e32 v27, v27
	v_med3_f32 v22, v22, s9, v214
	v_add_f32_e32 v27, 1.0, v27
	s_nop 0
	v_rcp_f32_e32 v28, v27
	s_nop 0
	v_mul_f32_e32 v19, v19, v28
	v_mul_f32_e32 v19, v19, v23
	v_med3_f32 v23, v26, s9, v214
	v_med3_f32 v26, v18, s9, v214
	v_mov_b32_e32 v18, v125
	v_cvt_pk_fp8_f32 v18, v23, v26
	v_med3_f32 v19, v19, s9, v214
	v_cvt_pk_fp8_f32 v18, v22, v19 op_sel:[0,0,1]
	v_lshlrev_b32_e32 v22, 16, v20
	v_mul_f32_e32 v23, 0xbfb8aa3b, v22
	v_exp_f32_e32 v23, v23
	v_and_b32_e32 v20, 0xffff0000, v20
	v_lshlrev_b32_e32 v19, 16, v24
	v_mul_f32_e32 v19, v43, v19
	v_add_f32_e32 v23, 1.0, v23
	s_nop 0
	v_rcp_f32_e32 v26, v23
	s_nop 0
	v_mul_f32_e32 v22, v22, v26
	v_mul_f32_e32 v23, 0xbfb8aa3b, v20
	v_exp_f32_e32 v23, v23
	v_mul_f32_e32 v19, v22, v19
	v_and_b32_e32 v22, 0xffff0000, v24
	v_mul_f32_e32 v22, v42, v22
	v_add_f32_e32 v23, 1.0, v23
	s_nop 0
	v_rcp_f32_e32 v24, v23
	s_nop 0
	v_mul_f32_e32 v20, v20, v24
	v_lshlrev_b32_e32 v23, 16, v21
	v_mul_f32_e32 v24, 0xbfb8aa3b, v23
	v_exp_f32_e32 v24, v24
	v_and_b32_e32 v21, 0xffff0000, v21
	v_mul_f32_e32 v20, v20, v22
	v_lshlrev_b32_e32 v22, 16, v25
	v_add_f32_e32 v24, 1.0, v24
	v_mul_f32_e32 v22, v41, v22
	v_med3_f32 v20, v20, s9, v214
	v_rcp_f32_e32 v26, v24
	s_nop 0
	v_mul_f32_e32 v23, v23, v26
	v_mul_f32_e32 v24, 0xbfb8aa3b, v21
	v_exp_f32_e32 v24, v24
	v_mul_f32_e32 v22, v23, v22
	v_and_b32_e32 v23, 0xffff0000, v25
	v_mul_f32_e32 v23, v40, v23
	v_add_f32_e32 v24, 1.0, v24
	v_med3_f32 v22, v22, s9, v214
	v_rcp_f32_e32 v25, v24
	s_nop 0
	v_mul_f32_e32 v21, v21, v25
	v_mul_f32_e32 v21, v21, v23
	v_med3_f32 v23, v19, s9, v214
	v_mov_b32_e32 v19, v125
	v_cvt_pk_fp8_f32 v19, v23, v20
	s_waitcnt vmcnt(6)
	v_lshlrev_b32_e32 v23, 16, v14
	v_mul_f32_e32 v24, 0xbfb8aa3b, v23
	v_exp_f32_e32 v24, v24
	v_med3_f32 v21, v21, s9, v214
	v_cvt_pk_fp8_f32 v19, v22, v21 op_sel:[0,0,1]
	v_lshlrev_b64 v[20:21], 11, v[124:125]
	v_add_f32_e32 v24, 1.0, v24
	v_lshl_add_u64 v[20:21], s[86:87], 0, v[20:21]
	v_lshl_add_u64 v[20:21], v[20:21], 0, s[84:85]
	v_lshl_add_u64 v[20:21], v[20:21], 0, v[136:137]
	global_store_dwordx2 v[20:21], v[18:19], off
	ds_read_b128 v[18:21], v209 offset:34816
	s_waitcnt lgkmcnt(0)
	v_lshlrev_b32_e32 v22, 16, v18
	v_mul_f32_e32 v22, v47, v22
	v_rcp_f32_e32 v25, v24
	s_nop 0
	v_mul_f32_e32 v23, v23, v25
	v_and_b32_e32 v14, 0xffff0000, v14
	v_mul_f32_e32 v22, v23, v22
	v_mul_f32_e32 v23, 0xbfb8aa3b, v14
	v_exp_f32_e32 v23, v23
	v_and_b32_e32 v18, 0xffff0000, v18
	v_mul_f32_e32 v18, v46, v18
	v_or_b32_e32 v124, s11, v192
	v_add_f32_e32 v23, 1.0, v23
	s_nop 0
	v_rcp_f32_e32 v24, v23
	s_nop 0
	v_mul_f32_e32 v14, v14, v24
	v_lshlrev_b32_e32 v23, 16, v15
	v_mul_f32_e32 v24, 0xbfb8aa3b, v23
	v_exp_f32_e32 v24, v24
	v_mul_f32_e32 v14, v14, v18
	v_lshlrev_b32_e32 v18, 16, v19
	v_mul_f32_e32 v18, v45, v18
	v_add_f32_e32 v24, 1.0, v24
	v_and_b32_e32 v15, 0xffff0000, v15
	v_and_b32_e32 v19, 0xffff0000, v19
	v_mul_f32_e32 v19, v44, v19
	v_rcp_f32_e32 v25, v24
	s_nop 0
	v_mul_f32_e32 v23, v23, v25
	v_mul_f32_e32 v18, v23, v18
	v_mul_f32_e32 v23, 0xbfb8aa3b, v15
	v_exp_f32_e32 v23, v23
	v_med3_f32 v18, v18, s9, v214
	v_add_f32_e32 v23, 1.0, v23
	s_nop 0
	v_rcp_f32_e32 v24, v23
	s_nop 0
	v_mul_f32_e32 v15, v15, v24
	v_mul_f32_e32 v15, v15, v19
	v_med3_f32 v19, v22, s9, v214
	v_med3_f32 v22, v14, s9, v214
	v_mov_b32_e32 v14, v125
	v_cvt_pk_fp8_f32 v14, v19, v22
	v_med3_f32 v15, v15, s9, v214
	v_cvt_pk_fp8_f32 v14, v18, v15 op_sel:[0,0,1]
	v_lshlrev_b32_e32 v18, 16, v16
	v_mul_f32_e32 v19, 0xbfb8aa3b, v18
	v_exp_f32_e32 v19, v19
	v_and_b32_e32 v16, 0xffff0000, v16
	v_lshlrev_b32_e32 v15, 16, v20
	v_mul_f32_e32 v15, v43, v15
	v_add_f32_e32 v19, 1.0, v19
	s_nop 0
	v_rcp_f32_e32 v22, v19
	s_nop 0
	v_mul_f32_e32 v18, v18, v22
	v_mul_f32_e32 v19, 0xbfb8aa3b, v16
	v_exp_f32_e32 v19, v19
	v_mul_f32_e32 v15, v18, v15
	v_and_b32_e32 v18, 0xffff0000, v20
	v_mul_f32_e32 v18, v42, v18
	v_add_f32_e32 v19, 1.0, v19
	s_nop 0
	v_rcp_f32_e32 v20, v19
	s_nop 0
	v_mul_f32_e32 v16, v16, v20
	v_lshlrev_b32_e32 v19, 16, v17
	v_mul_f32_e32 v20, 0xbfb8aa3b, v19
	v_exp_f32_e32 v20, v20
	v_and_b32_e32 v17, 0xffff0000, v17
	v_mul_f32_e32 v16, v16, v18
	v_lshlrev_b32_e32 v18, 16, v21
	v_add_f32_e32 v20, 1.0, v20
	v_mul_f32_e32 v18, v41, v18
	v_med3_f32 v16, v16, s9, v214
	v_rcp_f32_e32 v22, v20
	s_nop 0
	v_mul_f32_e32 v19, v19, v22
	v_mul_f32_e32 v20, 0xbfb8aa3b, v17
	v_exp_f32_e32 v20, v20
	v_mul_f32_e32 v18, v19, v18
	v_and_b32_e32 v19, 0xffff0000, v21
	v_mul_f32_e32 v19, v40, v19
	v_add_f32_e32 v20, 1.0, v20
	v_med3_f32 v18, v18, s9, v214
	v_rcp_f32_e32 v21, v20
	s_nop 0
	v_mul_f32_e32 v17, v17, v21
	v_mul_f32_e32 v17, v17, v19
	v_med3_f32 v19, v15, s9, v214
	v_mov_b32_e32 v15, v125
	v_cvt_pk_fp8_f32 v15, v19, v16
	s_waitcnt vmcnt(6)
	v_lshlrev_b32_e32 v19, 16, v10
	v_mul_f32_e32 v20, 0xbfb8aa3b, v19
	v_exp_f32_e32 v20, v20
	v_med3_f32 v17, v17, s9, v214
	v_cvt_pk_fp8_f32 v15, v18, v17 op_sel:[0,0,1]
	v_lshlrev_b64 v[16:17], 11, v[124:125]
	v_add_f32_e32 v20, 1.0, v20
	v_lshl_add_u64 v[16:17], s[86:87], 0, v[16:17]
	v_lshl_add_u64 v[16:17], v[16:17], 0, s[84:85]
	v_lshl_add_u64 v[16:17], v[16:17], 0, v[136:137]
	global_store_dwordx2 v[16:17], v[14:15], off
	ds_read_b128 v[14:17], v209 offset:43264
	s_waitcnt lgkmcnt(0)
	v_lshlrev_b32_e32 v18, 16, v14
	v_mul_f32_e32 v18, v47, v18
	v_rcp_f32_e32 v21, v20
	s_nop 0
	v_mul_f32_e32 v19, v19, v21
	v_and_b32_e32 v10, 0xffff0000, v10
	v_mul_f32_e32 v18, v19, v18
	v_mul_f32_e32 v19, 0xbfb8aa3b, v10
	v_exp_f32_e32 v19, v19
	v_and_b32_e32 v14, 0xffff0000, v14
	v_mul_f32_e32 v14, v46, v14
	v_or_b32_e32 v124, s11, v193
	v_add_f32_e32 v19, 1.0, v19
	s_nop 0
	v_rcp_f32_e32 v20, v19
	s_nop 0
	v_mul_f32_e32 v10, v10, v20
	v_lshlrev_b32_e32 v19, 16, v11
	v_mul_f32_e32 v20, 0xbfb8aa3b, v19
	v_exp_f32_e32 v20, v20
	v_mul_f32_e32 v10, v10, v14
	v_lshlrev_b32_e32 v14, 16, v15
	v_mul_f32_e32 v14, v45, v14
	v_add_f32_e32 v20, 1.0, v20
	v_and_b32_e32 v11, 0xffff0000, v11
	v_and_b32_e32 v15, 0xffff0000, v15
	v_mul_f32_e32 v15, v44, v15
	v_rcp_f32_e32 v21, v20
	s_nop 0
	v_mul_f32_e32 v19, v19, v21
	v_mul_f32_e32 v14, v19, v14
	v_mul_f32_e32 v19, 0xbfb8aa3b, v11
	v_exp_f32_e32 v19, v19
	v_med3_f32 v14, v14, s9, v214
	v_add_f32_e32 v19, 1.0, v19
	s_nop 0
	v_rcp_f32_e32 v20, v19
	s_nop 0
	v_mul_f32_e32 v11, v11, v20
	v_mul_f32_e32 v11, v11, v15
	v_med3_f32 v15, v18, s9, v214
	v_med3_f32 v18, v10, s9, v214
	v_mov_b32_e32 v10, v125
	v_cvt_pk_fp8_f32 v10, v15, v18
	v_med3_f32 v11, v11, s9, v214
	v_cvt_pk_fp8_f32 v10, v14, v11 op_sel:[0,0,1]
	v_lshlrev_b32_e32 v14, 16, v12
	v_mul_f32_e32 v15, 0xbfb8aa3b, v14
	v_exp_f32_e32 v15, v15
	v_and_b32_e32 v12, 0xffff0000, v12
	v_lshlrev_b32_e32 v11, 16, v16
	v_mul_f32_e32 v11, v43, v11
	v_add_f32_e32 v15, 1.0, v15
	s_nop 0
	v_rcp_f32_e32 v18, v15
	s_nop 0
	v_mul_f32_e32 v14, v14, v18
	v_mul_f32_e32 v15, 0xbfb8aa3b, v12
	v_exp_f32_e32 v15, v15
	v_mul_f32_e32 v11, v14, v11
	v_and_b32_e32 v14, 0xffff0000, v16
	v_mul_f32_e32 v14, v42, v14
	v_add_f32_e32 v15, 1.0, v15
	s_nop 0
	v_rcp_f32_e32 v16, v15
	s_nop 0
	v_mul_f32_e32 v12, v12, v16
	v_lshlrev_b32_e32 v15, 16, v13
	v_mul_f32_e32 v16, 0xbfb8aa3b, v15
	v_exp_f32_e32 v16, v16
	v_and_b32_e32 v13, 0xffff0000, v13
	v_mul_f32_e32 v12, v12, v14
	v_lshlrev_b32_e32 v14, 16, v17
	v_add_f32_e32 v16, 1.0, v16
	v_mul_f32_e32 v14, v41, v14
	v_med3_f32 v12, v12, s9, v214
	v_rcp_f32_e32 v18, v16
	s_nop 0
	v_mul_f32_e32 v15, v15, v18
	v_mul_f32_e32 v16, 0xbfb8aa3b, v13
	v_exp_f32_e32 v16, v16
	v_mul_f32_e32 v14, v15, v14
	v_and_b32_e32 v15, 0xffff0000, v17
	v_mul_f32_e32 v15, v40, v15
	v_add_f32_e32 v16, 1.0, v16
	v_med3_f32 v14, v14, s9, v214
	v_rcp_f32_e32 v17, v16
	s_nop 0
	v_mul_f32_e32 v13, v13, v17
	v_mul_f32_e32 v13, v13, v15
	v_med3_f32 v15, v11, s9, v214
	v_mov_b32_e32 v11, v125
	v_cvt_pk_fp8_f32 v11, v15, v12
	s_waitcnt vmcnt(6)
	v_lshlrev_b32_e32 v15, 16, v6
	v_mul_f32_e32 v16, 0xbfb8aa3b, v15
	v_exp_f32_e32 v16, v16
	v_med3_f32 v13, v13, s9, v214
	v_cvt_pk_fp8_f32 v11, v14, v13 op_sel:[0,0,1]
	v_lshlrev_b64 v[12:13], 11, v[124:125]
	v_add_f32_e32 v16, 1.0, v16
	v_lshl_add_u64 v[12:13], s[86:87], 0, v[12:13]
	v_lshl_add_u64 v[12:13], v[12:13], 0, s[84:85]
	v_lshl_add_u64 v[12:13], v[12:13], 0, v[136:137]
	global_store_dwordx2 v[12:13], v[10:11], off
	ds_read_b128 v[10:13], v209 offset:51712
	s_waitcnt lgkmcnt(0)
	v_lshlrev_b32_e32 v14, 16, v10
	v_mul_f32_e32 v14, v47, v14
	v_rcp_f32_e32 v17, v16
	s_nop 0
	v_mul_f32_e32 v15, v15, v17
	v_and_b32_e32 v6, 0xffff0000, v6
	v_mul_f32_e32 v14, v15, v14
	v_mul_f32_e32 v15, 0xbfb8aa3b, v6
	v_exp_f32_e32 v15, v15
	v_and_b32_e32 v10, 0xffff0000, v10
	v_mul_f32_e32 v10, v46, v10
	v_or_b32_e32 v124, s11, v195
	v_add_f32_e32 v15, 1.0, v15
	s_nop 0
	v_rcp_f32_e32 v16, v15
	s_nop 0
	v_mul_f32_e32 v6, v6, v16
	v_lshlrev_b32_e32 v15, 16, v7
	v_mul_f32_e32 v16, 0xbfb8aa3b, v15
	v_exp_f32_e32 v16, v16
	v_mul_f32_e32 v6, v6, v10
	v_lshlrev_b32_e32 v10, 16, v11
	v_mul_f32_e32 v10, v45, v10
	v_add_f32_e32 v16, 1.0, v16
	v_and_b32_e32 v7, 0xffff0000, v7
	v_and_b32_e32 v11, 0xffff0000, v11
	v_mul_f32_e32 v11, v44, v11
	v_rcp_f32_e32 v17, v16
	s_nop 0
	v_mul_f32_e32 v15, v15, v17
	v_mul_f32_e32 v10, v15, v10
	v_mul_f32_e32 v15, 0xbfb8aa3b, v7
	v_exp_f32_e32 v15, v15
	v_med3_f32 v10, v10, s9, v214
	v_add_f32_e32 v15, 1.0, v15
	s_nop 0
	v_rcp_f32_e32 v16, v15
	s_nop 0
	v_mul_f32_e32 v7, v7, v16
	v_mul_f32_e32 v7, v7, v11
	v_med3_f32 v11, v14, s9, v214
	v_med3_f32 v14, v6, s9, v214
	v_mov_b32_e32 v6, v125
	v_cvt_pk_fp8_f32 v6, v11, v14
	v_med3_f32 v7, v7, s9, v214
	v_cvt_pk_fp8_f32 v6, v10, v7 op_sel:[0,0,1]
	v_lshlrev_b32_e32 v10, 16, v8
	v_mul_f32_e32 v11, 0xbfb8aa3b, v10
	v_exp_f32_e32 v11, v11
	v_and_b32_e32 v8, 0xffff0000, v8
	v_lshlrev_b32_e32 v7, 16, v12
	v_mul_f32_e32 v7, v43, v7
	v_add_f32_e32 v11, 1.0, v11
	s_nop 0
	v_rcp_f32_e32 v14, v11
	s_nop 0
	v_mul_f32_e32 v10, v10, v14
	v_mul_f32_e32 v11, 0xbfb8aa3b, v8
	v_exp_f32_e32 v11, v11
	v_mul_f32_e32 v7, v10, v7
	v_and_b32_e32 v10, 0xffff0000, v12
	v_mul_f32_e32 v10, v42, v10
	v_add_f32_e32 v11, 1.0, v11
	s_nop 0
	v_rcp_f32_e32 v12, v11
	s_nop 0
	v_mul_f32_e32 v8, v8, v12
	v_lshlrev_b32_e32 v11, 16, v9
	v_mul_f32_e32 v12, 0xbfb8aa3b, v11
	v_exp_f32_e32 v12, v12
	v_and_b32_e32 v9, 0xffff0000, v9
	v_mul_f32_e32 v8, v8, v10
	v_lshlrev_b32_e32 v10, 16, v13
	v_add_f32_e32 v12, 1.0, v12
	v_mul_f32_e32 v10, v41, v10
	v_med3_f32 v8, v8, s9, v214
	v_rcp_f32_e32 v14, v12
	s_nop 0
	v_mul_f32_e32 v11, v11, v14
	v_mul_f32_e32 v12, 0xbfb8aa3b, v9
	v_exp_f32_e32 v12, v12
	v_mul_f32_e32 v10, v11, v10
	v_and_b32_e32 v11, 0xffff0000, v13
	v_mul_f32_e32 v11, v40, v11
	v_add_f32_e32 v12, 1.0, v12
	v_med3_f32 v10, v10, s9, v214
	v_rcp_f32_e32 v13, v12
	s_nop 0
	v_mul_f32_e32 v9, v9, v13
	v_mul_f32_e32 v9, v9, v11
	v_med3_f32 v11, v7, s9, v214
	v_mov_b32_e32 v7, v125
	v_cvt_pk_fp8_f32 v7, v11, v8
	s_waitcnt vmcnt(6)
	v_lshlrev_b32_e32 v11, 16, v2
	v_mul_f32_e32 v12, 0xbfb8aa3b, v11
	v_exp_f32_e32 v12, v12
	v_med3_f32 v9, v9, s9, v214
	v_cvt_pk_fp8_f32 v7, v10, v9 op_sel:[0,0,1]
	v_lshlrev_b64 v[8:9], 11, v[124:125]
	v_add_f32_e32 v12, 1.0, v12
	v_lshl_add_u64 v[8:9], s[86:87], 0, v[8:9]
	v_lshl_add_u64 v[8:9], v[8:9], 0, s[84:85]
	v_lshl_add_u64 v[8:9], v[8:9], 0, v[136:137]
	global_store_dwordx2 v[8:9], v[6:7], off
	ds_read_b128 v[6:9], v209 offset:60160
	s_waitcnt lgkmcnt(0)
	v_lshlrev_b32_e32 v10, 16, v6
	v_mul_f32_e32 v10, v47, v10
	v_rcp_f32_e32 v13, v12
	s_nop 0
	v_mul_f32_e32 v11, v11, v13
	v_and_b32_e32 v2, 0xffff0000, v2
	v_mul_f32_e32 v10, v11, v10
	v_mul_f32_e32 v11, 0xbfb8aa3b, v2
	v_exp_f32_e32 v11, v11
	v_and_b32_e32 v6, 0xffff0000, v6
	v_mul_f32_e32 v6, v46, v6
	v_add_u32_e32 v124, s11, v197
	v_add_f32_e32 v11, 1.0, v11
	s_nop 0
	v_rcp_f32_e32 v12, v11
	s_nop 0
	v_mul_f32_e32 v2, v2, v12
	v_lshlrev_b32_e32 v11, 16, v3
	v_mul_f32_e32 v12, 0xbfb8aa3b, v11
	v_exp_f32_e32 v12, v12
	v_mul_f32_e32 v2, v2, v6
	v_lshlrev_b32_e32 v6, 16, v7
	v_mul_f32_e32 v6, v45, v6
	v_add_f32_e32 v12, 1.0, v12
	v_and_b32_e32 v3, 0xffff0000, v3
	v_and_b32_e32 v7, 0xffff0000, v7
	v_mul_f32_e32 v7, v44, v7
	v_rcp_f32_e32 v13, v12
	s_nop 0
	v_mul_f32_e32 v11, v11, v13
	v_mul_f32_e32 v6, v11, v6
	v_mul_f32_e32 v11, 0xbfb8aa3b, v3
	v_exp_f32_e32 v11, v11
	v_med3_f32 v6, v6, s9, v214
	v_add_f32_e32 v11, 1.0, v11
	s_nop 0
	v_rcp_f32_e32 v12, v11
	s_nop 0
	v_mul_f32_e32 v3, v3, v12
	v_mul_f32_e32 v3, v3, v7
	v_med3_f32 v7, v10, s9, v214
	v_med3_f32 v10, v2, s9, v214
	v_mov_b32_e32 v2, v125
	v_cvt_pk_fp8_f32 v2, v7, v10
	v_med3_f32 v3, v3, s9, v214
	v_cvt_pk_fp8_f32 v2, v6, v3 op_sel:[0,0,1]
	v_lshlrev_b32_e32 v6, 16, v4
	v_mul_f32_e32 v7, 0xbfb8aa3b, v6
	v_exp_f32_e32 v7, v7
	v_and_b32_e32 v4, 0xffff0000, v4
	v_lshlrev_b32_e32 v3, 16, v8
	v_mul_f32_e32 v3, v43, v3
	v_add_f32_e32 v7, 1.0, v7
	s_nop 0
	v_rcp_f32_e32 v10, v7
	s_nop 0
	v_mul_f32_e32 v6, v6, v10
	v_mul_f32_e32 v7, 0xbfb8aa3b, v4
	v_exp_f32_e32 v7, v7
	v_mul_f32_e32 v3, v6, v3
	v_and_b32_e32 v6, 0xffff0000, v8
	v_mul_f32_e32 v6, v42, v6
	v_add_f32_e32 v7, 1.0, v7
	s_nop 0
	v_rcp_f32_e32 v8, v7
	s_nop 0
	v_mul_f32_e32 v4, v4, v8
	v_lshlrev_b32_e32 v7, 16, v5
	v_mul_f32_e32 v8, 0xbfb8aa3b, v7
	v_exp_f32_e32 v8, v8
	v_and_b32_e32 v5, 0xffff0000, v5
	v_mul_f32_e32 v4, v4, v6
	v_lshlrev_b32_e32 v6, 16, v9
	v_add_f32_e32 v8, 1.0, v8
	v_mul_f32_e32 v6, v41, v6
	v_med3_f32 v4, v4, s9, v214
	v_rcp_f32_e32 v10, v8
	s_nop 0
	v_mul_f32_e32 v7, v7, v10
	v_mul_f32_e32 v8, 0xbfb8aa3b, v5
	v_exp_f32_e32 v8, v8
	v_mul_f32_e32 v6, v7, v6
	v_and_b32_e32 v7, 0xffff0000, v9
	v_mul_f32_e32 v7, v40, v7
	v_add_f32_e32 v8, 1.0, v8
	v_med3_f32 v6, v6, s9, v214
	v_rcp_f32_e32 v9, v8
	s_nop 0
	v_mul_f32_e32 v5, v5, v9
	v_mul_f32_e32 v5, v5, v7
	v_med3_f32 v7, v3, s9, v214
	v_mov_b32_e32 v3, v125
	v_cvt_pk_fp8_f32 v3, v7, v4
	v_med3_f32 v5, v5, s9, v214
	v_cvt_pk_fp8_f32 v3, v6, v5 op_sel:[0,0,1]
	v_lshlrev_b64 v[4:5], 11, v[124:125]
	v_lshl_add_u64 v[4:5], s[86:87], 0, v[4:5]
	v_lshl_add_u64 v[4:5], v[4:5], 0, s[84:85]
	v_lshl_add_u64 v[4:5], v[4:5], 0, v[136:137]
	global_store_dwordx2 v[4:5], v[2:3], off
	s_barrier
	s_cbranch_scc0 .LBB0_956
.LBB0_938:
	s_and_b32 s94, s10, 7
	v_cvt_f32_ubyte0_e32 v2, s94
	v_sub_f32_e32 v2, 0xc0a00000, v2
	v_cmp_gt_f32_e32 vcc, s53, v2
	s_and_b64 s[0:1], vcc, exec
	s_cselect_b32 s0, 0xffffffc0, 0
	v_cndmask_b32_e32 v3, 0, v210, vcc
	v_add_f32_e32 v2, v2, v3
	v_exp_f32_e32 v2, v2
	v_mov_b32_e32 v141, v125
	v_mov_b32_e32 v143, v125
	v_mov_b32_e32 v27, v125
	v_ldexp_f32 v2, v2, s0
	v_sub_f32_e32 v2, 1.0, v2
	s_mov_b32 s0, 0x800000
	v_cmp_gt_f32_e32 vcc, s0, v2
	s_and_b64 s[0:1], vcc, exec
	s_cselect_b32 s0, 32, 0
	v_ldexp_f32 v2, v2, s0
	v_log_f32_e32 v2, v2
	s_and_b32 s11, s81, 0xffffff80
	v_or_b32_e32 v8, s11, v123
	v_cndmask_b32_e32 v3, 0, v211, vcc
	v_mul_lo_u32 v124, v8, s96
	v_sub_f32_e32 v215, v2, v3
	s_lshl_b32 s84, s94, 8
	v_lshl_add_u64 v[2:3], v[124:125], 1, s[82:83]
	v_lshl_add_u64 v[4:5], v[2:3], 0, s[84:85]
	v_lshl_add_u64 v[4:5], v[4:5], 0, s[90:91]
	v_lshl_add_u64 v[6:7], v[4:5], 0, v[140:141]
	v_lshl_add_u64 v[4:5], v[4:5], 0, v[142:143]
	v_lshlrev_b32_e32 v26, 6, v8
	global_load_dwordx4 v[216:219], v[6:7], off nt
	global_load_dwordx4 v[220:223], v[4:5], off nt
	v_lshlrev_b64 v[4:5], 2, v[26:27]
	v_lshl_add_u64 v[6:7], v[126:127], 0, v[4:5]
	v_lshl_add_u64 v[4:5], v[128:129], 0, v[4:5]
	global_load_dwordx4 v[98:101], v[6:7], off offset:16 nt
	global_load_dwordx4 v[114:117], v[6:7], off nt
	global_load_dwordx4 v[102:105], v[4:5], off offset:16 nt
	global_load_dwordx4 v[118:121], v[4:5], off nt
	s_lshl_b32 s0, s94, 9
	s_mov_b32 s1, s85
	v_add_u32_e32 v10, 0x98000, v124
	v_mov_b32_e32 v11, v125
	v_lshl_add_u64 v[2:3], v[2:3], 0, s[0:1]
	v_lshl_add_u64 v[10:11], v[10:11], 1, s[82:83]
	v_lshl_add_u64 v[2:3], v[2:3], 0, v[140:141]
	v_lshl_add_u64 v[12:13], v[10:11], 0, s[84:85]
	v_lshl_add_u64 v[6:7], v[2:3], 0, s[92:93]
	v_add_co_u32_e32 v2, vcc, s97, v2
	v_lshl_add_u64 v[12:13], v[12:13], 0, s[90:91]
	s_nop 0
	v_addc_co_u32_e32 v3, vcc, 0, v3, vcc
	v_lshl_add_u64 v[14:15], v[12:13], 0, v[140:141]
	v_lshl_add_u64 v[12:13], v[12:13], 0, v[142:143]
	global_load_dwordx4 v[2:5], v[2:3], off offset:2048 nt
	s_nop 0
	global_load_dwordx4 v[6:9], v[6:7], off offset:256 nt
	s_nop 0
	global_load_dwordx4 v[106:109], v[14:15], off nt
	global_load_dwordx4 v[110:113], v[12:13], off nt
	v_or_b32_e32 v12, 0x800, v26
	v_mov_b32_e32 v13, v125
	v_lshlrev_b64 v[12:13], 2, v[12:13]
	v_lshl_add_u64 v[14:15], v[126:127], 0, v[12:13]
	v_lshl_add_u64 v[12:13], v[128:129], 0, v[12:13]
	global_load_dwordx4 v[74:77], v[14:15], off offset:16 nt
	global_load_dwordx4 v[90:93], v[14:15], off nt
	global_load_dwordx4 v[78:81], v[12:13], off offset:16 nt
	global_load_dwordx4 v[94:97], v[12:13], off nt
	v_add_u32_e32 v18, 0x130000, v124
	v_mov_b32_e32 v19, v125
	v_lshl_add_u64 v[10:11], v[10:11], 0, s[0:1]
	v_lshl_add_u64 v[18:19], v[18:19], 1, s[82:83]
	v_lshl_add_u64 v[10:11], v[10:11], 0, v[140:141]
	v_lshl_add_u64 v[20:21], v[18:19], 0, s[84:85]
	v_lshl_add_u64 v[14:15], v[10:11], 0, s[92:93]
	v_add_co_u32_e32 v10, vcc, s97, v10
	v_lshl_add_u64 v[20:21], v[20:21], 0, s[90:91]
	s_nop 0
	v_addc_co_u32_e32 v11, vcc, 0, v11, vcc
	v_lshl_add_u64 v[22:23], v[20:21], 0, v[140:141]
	v_lshl_add_u64 v[20:21], v[20:21], 0, v[142:143]
	global_load_dwordx4 v[10:13], v[10:11], off offset:2048 nt
	s_nop 0
	global_load_dwordx4 v[14:17], v[14:15], off offset:256 nt
	s_nop 0
	global_load_dwordx4 v[82:85], v[22:23], off nt
	global_load_dwordx4 v[86:89], v[20:21], off nt
	v_or_b32_e32 v20, 0x1000, v26
	v_mov_b32_e32 v21, v125
	v_lshlrev_b64 v[20:21], 2, v[20:21]
	v_lshl_add_u64 v[22:23], v[126:127], 0, v[20:21]
	v_lshl_add_u64 v[20:21], v[128:129], 0, v[20:21]
	global_load_dwordx4 v[58:61], v[22:23], off offset:16 nt
	global_load_dwordx4 v[66:69], v[22:23], off nt
	global_load_dwordx4 v[62:65], v[20:21], off offset:16 nt
	global_load_dwordx4 v[70:73], v[20:21], off nt
	v_add_u32_e32 v124, 0x1c8000, v124
	v_lshl_add_u64 v[28:29], v[124:125], 1, s[82:83]
	v_or_b32_e32 v124, 0x1800, v26
	v_lshl_add_u64 v[18:19], v[18:19], 0, s[0:1]
	v_lshlrev_b64 v[26:27], 2, v[124:125]
	v_lshl_add_u64 v[18:19], v[18:19], 0, v[140:141]
	v_lshl_add_u64 v[30:31], v[28:29], 0, s[84:85]
	v_lshl_add_u64 v[22:23], v[18:19], 0, s[92:93]
	v_add_co_u32_e32 v18, vcc, s97, v18
	v_lshl_add_u64 v[30:31], v[30:31], 0, s[90:91]
	s_nop 0
	v_addc_co_u32_e32 v19, vcc, 0, v19, vcc
	v_lshl_add_u64 v[32:33], v[30:31], 0, v[140:141]
	global_load_dwordx4 v[18:21], v[18:19], off offset:2048 nt
	s_nop 0
	global_load_dwordx4 v[22:25], v[22:23], off offset:256 nt
	v_lshl_add_u64 v[30:31], v[30:31], 0, v[142:143]
	global_load_dwordx4 v[50:53], v[32:33], off nt
	global_load_dwordx4 v[54:57], v[30:31], off nt
	v_lshl_add_u64 v[30:31], v[126:127], 0, v[26:27]
	v_lshl_add_u64 v[26:27], v[128:129], 0, v[26:27]
	global_load_dwordx4 v[34:37], v[30:31], off offset:16 nt
	global_load_dwordx4 v[42:45], v[30:31], off nt
	global_load_dwordx4 v[38:41], v[26:27], off offset:16 nt
	global_load_dwordx4 v[46:49], v[26:27], off nt
	v_lshl_add_u64 v[26:27], v[28:29], 0, s[0:1]
	v_lshl_add_u64 v[26:27], v[26:27], 0, v[140:141]
	v_lshl_add_u64 v[28:29], v[26:27], 0, s[92:93]
	v_add_co_u32_e32 v26, vcc, s97, v26
	s_mov_b64 s[0:1], 0x4800
	s_nop 0
	v_addc_co_u32_e32 v27, vcc, 0, v27, vcc
	s_waitcnt vmcnt(29)
	v_lshlrev_b32_e32 v224, 16, v216
	s_waitcnt vmcnt(28)
	v_lshlrev_b32_e32 v225, 16, v220
	v_and_b32_e32 v227, 0xffff0000, v220
	v_and_b32_e32 v226, 0xffff0000, v216
	v_lshlrev_b32_e32 v228, 16, v217
	v_and_b32_e32 v220, 0xffff0000, v217
	v_lshlrev_b32_e32 v217, 16, v222
	v_lshlrev_b32_e32 v216, 16, v218
	v_and_b32_e32 v231, 0xffff0000, v222
	v_and_b32_e32 v230, 0xffff0000, v218
	v_lshlrev_b32_e32 v232, 16, v219
	v_and_b32_e32 v222, 0xffff0000, v219
	s_waitcnt vmcnt(26)
	v_mov_b32_e32 v218, v114
	s_waitcnt vmcnt(24)
	v_mov_b32_e32 v219, v118
	v_pk_mul_f32 v[218:219], v[218:219], v[224:225]
	v_lshlrev_b32_e32 v229, 16, v221
	v_sub_f32_e32 v114, v218, v219
	v_add_f32_e32 v118, v218, v219
	v_cndmask_b32_e64 v114, v118, v114, s[6:7]
	v_mov_b32_e32 v118, v115
	v_mul_f32_e32 v124, 0x3db504f3, v114
	v_pk_mul_f32 v[114:115], v[118:119], v[226:227]
	v_and_b32_e32 v221, 0xffff0000, v221
	v_sub_f32_e32 v118, v114, v115
	v_add_f32_e32 v114, v114, v115
	v_cndmask_b32_e64 v114, v114, v118, s[6:7]
	v_mul_f32_e32 v118, 0x3db504f3, v114
	v_mov_b32_e32 v114, v116
	v_mov_b32_e32 v115, v120
	v_pk_mul_f32 v[114:115], v[114:115], v[228:229]
	v_mov_b32_e32 v120, v117
	v_sub_f32_e32 v116, v114, v115
	v_add_f32_e32 v114, v114, v115
	v_cndmask_b32_e64 v114, v114, v116, s[6:7]
	v_mul_f32_e32 v116, 0x3db504f3, v114
	v_pk_mul_f32 v[114:115], v[120:121], v[220:221]
	v_lshlrev_b32_e32 v233, 16, v223
	v_sub_f32_e32 v117, v114, v115
	v_add_f32_e32 v114, v114, v115
	v_cndmask_b32_e64 v114, v114, v117, s[6:7]
	v_mul_f32_e32 v117, 0x3db504f3, v114
	v_mov_b32_e32 v114, v98
	v_mov_b32_e32 v115, v102
	v_pk_mul_f32 v[114:115], v[114:115], v[216:217]
	v_and_b32_e32 v223, 0xffff0000, v223
	v_sub_f32_e32 v98, v114, v115
	v_add_f32_e32 v102, v114, v115
	v_cndmask_b32_e64 v98, v102, v98, s[6:7]
	v_mov_b32_e32 v102, v99
	v_mul_f32_e32 v114, 0x3db504f3, v98
	v_pk_mul_f32 v[98:99], v[102:103], v[230:231]
	global_load_dwordx4 v[30:33], v[26:27], off offset:2048 nt
	s_nop 0
	global_load_dwordx4 v[26:29], v[28:29], off offset:256 nt
	v_sub_f32_e32 v102, v98, v99
	v_add_f32_e32 v98, v98, v99
	v_cndmask_b32_e64 v98, v98, v102, s[6:7]
	v_mul_f32_e32 v102, 0x3db504f3, v98
	v_mov_b32_e32 v98, v100
	v_mov_b32_e32 v99, v104
	v_pk_mul_f32 v[98:99], v[98:99], v[232:233]
	v_mov_b32_e32 v104, v101
	v_sub_f32_e32 v100, v98, v99
	v_add_f32_e32 v98, v98, v99
	v_cndmask_b32_e64 v98, v98, v100, s[6:7]
	v_mul_f32_e32 v103, 0x3db504f3, v98
	v_pk_mul_f32 v[98:99], v[104:105], v[222:223]
	s_waitcnt vmcnt(22)
	v_and_b32_e32 v105, 0xffff0000, v111
	v_sub_f32_e32 v100, v98, v99
	v_add_f32_e32 v98, v98, v99
	v_cndmask_b32_e64 v98, v98, v100, s[6:7]
	v_mul_f32_e32 v101, 0x3db504f3, v98
	v_cvt_pk_bf16_f32 v98, v124, v118
	v_cvt_pk_bf16_f32 v99, v116, v117
	v_cvt_pk_bf16_f32 v100, v114, v102
	v_cvt_pk_bf16_f32 v101, v103, v101
	ds_write_b128 v198, v[98:101]
	v_lshlrev_b32_e32 v99, 16, v110
	v_lshlrev_b32_e32 v98, 16, v106
	v_and_b32_e32 v101, 0xffff0000, v110
	v_and_b32_e32 v100, 0xffff0000, v106
	v_lshlrev_b32_e32 v103, 16, v111
	v_lshlrev_b32_e32 v102, 16, v107
	v_and_b32_e32 v104, 0xffff0000, v107
	v_lshlrev_b32_e32 v107, 16, v112
	v_lshlrev_b32_e32 v106, 16, v108
	v_and_b32_e32 v111, 0xffff0000, v112
	v_and_b32_e32 v110, 0xffff0000, v108
	v_lshlrev_b32_e32 v114, 16, v109
	v_and_b32_e32 v112, 0xffff0000, v109
	s_waitcnt vmcnt(20)
	v_mov_b32_e32 v108, v90
	s_waitcnt vmcnt(18)
	v_mov_b32_e32 v109, v94
	v_pk_mul_f32 v[98:99], v[108:109], v[98:99]
	v_lshlrev_b32_e32 v115, 16, v113
	v_sub_f32_e32 v90, v98, v99
	v_add_f32_e32 v94, v98, v99
	v_cndmask_b32_e64 v90, v94, v90, s[6:7]
	v_mov_b32_e32 v94, v91
	v_mul_f32_e32 v98, 0x3db504f3, v90
	v_pk_mul_f32 v[90:91], v[94:95], v[100:101]
	v_and_b32_e32 v113, 0xffff0000, v113
	v_sub_f32_e32 v94, v90, v91
	v_add_f32_e32 v90, v90, v91
	v_cndmask_b32_e64 v90, v90, v94, s[6:7]
	v_mul_f32_e32 v94, 0x3db504f3, v90
	v_mov_b32_e32 v90, v92
	v_mov_b32_e32 v91, v96
	v_pk_mul_f32 v[90:91], v[90:91], v[102:103]
	v_mov_b32_e32 v96, v93
	v_sub_f32_e32 v92, v90, v91
	v_add_f32_e32 v90, v90, v91
	v_cndmask_b32_e64 v90, v90, v92, s[6:7]
	v_mul_f32_e32 v92, 0x3db504f3, v90
	v_pk_mul_f32 v[90:91], v[96:97], v[104:105]
	s_waitcnt vmcnt(6)
	v_lshlrev_b32_e32 v95, 16, v57
	v_sub_f32_e32 v93, v90, v91
	v_add_f32_e32 v90, v90, v91
	v_cndmask_b32_e64 v90, v90, v93, s[6:7]
	v_mul_f32_e32 v93, 0x3db504f3, v90
	v_mov_b32_e32 v90, v74
	v_mov_b32_e32 v91, v78
	v_pk_mul_f32 v[90:91], v[90:91], v[106:107]
	v_and_b32_e32 v57, 0xffff0000, v57
	v_sub_f32_e32 v74, v90, v91
	v_add_f32_e32 v78, v90, v91
	v_cndmask_b32_e64 v74, v78, v74, s[6:7]
	v_mov_b32_e32 v78, v75
	v_mul_f32_e32 v90, 0x3db504f3, v74
	v_pk_mul_f32 v[74:75], v[78:79], v[110:111]
	v_lshlrev_b32_e32 v91, 16, v89
	v_sub_f32_e32 v78, v74, v75
	v_add_f32_e32 v74, v74, v75
	v_cndmask_b32_e64 v74, v74, v78, s[6:7]
	v_mul_f32_e32 v78, 0x3db504f3, v74
	v_mov_b32_e32 v74, v76
	v_mov_b32_e32 v75, v80
	v_pk_mul_f32 v[74:75], v[74:75], v[114:115]
	v_mov_b32_e32 v80, v77
	v_sub_f32_e32 v76, v74, v75
	v_add_f32_e32 v74, v74, v75
	v_cndmask_b32_e64 v74, v74, v76, s[6:7]
	v_mul_f32_e32 v79, 0x3db504f3, v74
	v_pk_mul_f32 v[74:75], v[80:81], v[112:113]
	v_and_b32_e32 v81, 0xffff0000, v87
	v_sub_f32_e32 v76, v74, v75
	v_add_f32_e32 v74, v74, v75
	v_cndmask_b32_e64 v74, v74, v76, s[6:7]
	v_mul_f32_e32 v77, 0x3db504f3, v74
	v_cvt_pk_bf16_f32 v74, v98, v94
	v_cvt_pk_bf16_f32 v75, v92, v93
	v_cvt_pk_bf16_f32 v76, v90, v78
	v_cvt_pk_bf16_f32 v77, v79, v77
	ds_write_b128 v198, v[74:77] offset:8704
	v_lshlrev_b32_e32 v75, 16, v86
	v_lshlrev_b32_e32 v74, 16, v82
	v_and_b32_e32 v77, 0xffff0000, v86
	v_and_b32_e32 v76, 0xffff0000, v82
	v_lshlrev_b32_e32 v79, 16, v87
	v_lshlrev_b32_e32 v78, 16, v83
	v_and_b32_e32 v80, 0xffff0000, v83
	v_lshlrev_b32_e32 v83, 16, v88
	v_lshlrev_b32_e32 v82, 16, v84
	v_and_b32_e32 v87, 0xffff0000, v88
	v_and_b32_e32 v86, 0xffff0000, v84
	v_lshlrev_b32_e32 v90, 16, v85
	v_and_b32_e32 v88, 0xffff0000, v85
	v_mov_b32_e32 v84, v66
	v_mov_b32_e32 v85, v70
	v_pk_mul_f32 v[74:75], v[84:85], v[74:75]
	v_and_b32_e32 v89, 0xffff0000, v89
	v_sub_f32_e32 v66, v74, v75
	v_add_f32_e32 v70, v74, v75
	v_cndmask_b32_e64 v66, v70, v66, s[6:7]
	v_mov_b32_e32 v70, v67
	v_mul_f32_e32 v74, 0x3db504f3, v66
	v_pk_mul_f32 v[66:67], v[70:71], v[76:77]
	v_and_b32_e32 v92, 0xffff0000, v52
	v_sub_f32_e32 v70, v66, v67
	v_add_f32_e32 v66, v66, v67
	v_cndmask_b32_e64 v66, v66, v70, s[6:7]
	v_mul_f32_e32 v70, 0x3db504f3, v66
	v_mov_b32_e32 v66, v68
	v_mov_b32_e32 v67, v72
	v_pk_mul_f32 v[66:67], v[66:67], v[78:79]
	v_mov_b32_e32 v72, v69
	v_sub_f32_e32 v68, v66, v67
	v_add_f32_e32 v66, v66, v67
	v_cndmask_b32_e64 v66, v66, v68, s[6:7]
	v_mul_f32_e32 v68, 0x3db504f3, v66
	v_pk_mul_f32 v[66:67], v[72:73], v[80:81]
	v_and_b32_e32 v93, 0xffff0000, v56
	v_sub_f32_e32 v69, v66, v67
	v_add_f32_e32 v66, v66, v67
	v_cndmask_b32_e64 v66, v66, v69, s[6:7]
	v_mul_f32_e32 v69, 0x3db504f3, v66
	v_mov_b32_e32 v66, v58
	v_mov_b32_e32 v67, v62
	v_pk_mul_f32 v[66:67], v[66:67], v[82:83]
	v_lshlrev_b32_e32 v94, 16, v53
	v_sub_f32_e32 v58, v66, v67
	v_add_f32_e32 v62, v66, v67
	v_cndmask_b32_e64 v58, v62, v58, s[6:7]
	v_mov_b32_e32 v62, v59
	v_mul_f32_e32 v66, 0x3db504f3, v58
	v_pk_mul_f32 v[58:59], v[62:63], v[86:87]
	v_lshlrev_b32_e32 v86, 16, v50
	v_sub_f32_e32 v62, v58, v59
	v_add_f32_e32 v58, v58, v59
	v_cndmask_b32_e64 v58, v58, v62, s[6:7]
	v_mul_f32_e32 v62, 0x3db504f3, v58
	v_mov_b32_e32 v58, v60
	v_mov_b32_e32 v59, v64
	v_pk_mul_f32 v[58:59], v[58:59], v[90:91]
	v_mov_b32_e32 v64, v61
	v_sub_f32_e32 v60, v58, v59
	v_add_f32_e32 v58, v58, v59
	v_cndmask_b32_e64 v58, v58, v60, s[6:7]
	v_mul_f32_e32 v63, 0x3db504f3, v58
	v_pk_mul_f32 v[58:59], v[64:65], v[88:89]
	v_and_b32_e32 v88, 0xffff0000, v50
	v_sub_f32_e32 v60, v58, v59
	v_add_f32_e32 v58, v58, v59
	v_cndmask_b32_e64 v58, v58, v60, s[6:7]
	v_lshlrev_b32_e32 v50, 16, v52
	v_add_u32_e32 v52, s11, v144
	v_mul_f32_e32 v61, 0x3db504f3, v58
	v_cvt_pk_bf16_f32 v58, v74, v70
	v_cvt_pk_bf16_f32 v59, v68, v69
	v_mul_lo_u32 v124, v52, s96
	v_cvt_pk_bf16_f32 v60, v66, v62
	v_cvt_pk_bf16_f32 v61, v63, v61
	ds_write_b128 v198, v[58:61] offset:17408
	v_lshl_add_u64 v[58:59], v[124:125], 1, s[82:83]
	v_lshl_add_u64 v[58:59], v[58:59], 0, s[84:85]
	v_lshlrev_b32_e32 v124, 1, v130
	v_lshl_add_u64 v[58:59], v[58:59], 0, v[124:125]
	v_lshl_add_u64 v[96:97], v[58:59], 0, s[0:1]
	s_movk_i32 s0, 0x4000
	v_lshlrev_b32_e32 v124, 6, v52
	v_add_co_u32_e32 v58, vcc, s0, v58
	v_lshlrev_b64 v[70:71], 2, v[124:125]
	s_nop 0
	v_addc_co_u32_e32 v59, vcc, 0, v59, vcc
	v_lshl_add_u64 v[98:99], v[132:133], 0, v[70:71]
	global_load_dwordx4 v[62:65], v[58:59], off offset:2048 nt
	s_nop 0
	global_load_dwordx4 v[58:61], v[96:97], off offset:64 nt
	global_load_dwordx4 v[66:69], v[96:97], off offset:128 nt
	v_lshl_add_u64 v[100:101], v[134:135], 0, v[70:71]
	global_load_dwordx4 v[70:73], v[98:99], off offset:16 nt
	global_load_dwordx4 v[78:81], v[98:99], off nt
	global_load_dwordx4 v[74:77], v[100:101], off offset:16 nt
	global_load_dwordx4 v[82:85], v[100:101], off nt
	v_lshlrev_b32_e32 v87, 16, v54
	v_and_b32_e32 v89, 0xffff0000, v54
	v_lshlrev_b32_e32 v90, 16, v51
	v_and_b32_e32 v54, 0xffff0000, v51
	v_lshlrev_b32_e32 v51, 16, v56
	v_and_b32_e32 v56, 0xffff0000, v53
	s_waitcnt vmcnt(11)
	v_mov_b32_e32 v52, v42
	s_waitcnt vmcnt(9)
	v_mov_b32_e32 v53, v46
	v_pk_mul_f32 v[52:53], v[52:53], v[86:87]
	v_lshlrev_b32_e32 v91, 16, v55
	v_sub_f32_e32 v42, v52, v53
	v_add_f32_e32 v46, v52, v53
	v_cndmask_b32_e64 v42, v46, v42, s[6:7]
	v_mov_b32_e32 v46, v43
	v_mul_f32_e32 v52, 0x3db504f3, v42
	v_pk_mul_f32 v[42:43], v[46:47], v[88:89]
	v_and_b32_e32 v55, 0xffff0000, v55
	v_sub_f32_e32 v46, v42, v43
	v_add_f32_e32 v42, v42, v43
	v_cndmask_b32_e64 v42, v42, v46, s[6:7]
	v_mul_f32_e32 v46, 0x3db504f3, v42
	v_mov_b32_e32 v42, v44
	v_mov_b32_e32 v43, v48
	v_pk_mul_f32 v[42:43], v[42:43], v[90:91]
	v_mov_b32_e32 v48, v45
	v_sub_f32_e32 v44, v42, v43
	v_add_f32_e32 v42, v42, v43
	v_cndmask_b32_e64 v42, v42, v44, s[6:7]
	v_mul_f32_e32 v44, 0x3db504f3, v42
	v_pk_mul_f32 v[42:43], v[48:49], v[54:55]
	s_movk_i32 s0, 0x1000
	v_sub_f32_e32 v45, v42, v43
	v_add_f32_e32 v42, v42, v43
	v_cndmask_b32_e64 v42, v42, v45, s[6:7]
	v_mul_f32_e32 v45, 0x3db504f3, v42
	v_mov_b32_e32 v42, v34
	v_mov_b32_e32 v43, v38
	v_pk_mul_f32 v[42:43], v[42:43], v[50:51]
	s_nop 0
	v_sub_f32_e32 v34, v42, v43
	v_add_f32_e32 v38, v42, v43
	v_cndmask_b32_e64 v34, v38, v34, s[6:7]
	v_mov_b32_e32 v38, v35
	v_mul_f32_e32 v42, 0x3db504f3, v34
	v_pk_mul_f32 v[34:35], v[38:39], v[92:93]
	s_nop 0
	v_sub_f32_e32 v38, v34, v35
	v_add_f32_e32 v34, v34, v35
	v_cndmask_b32_e64 v34, v34, v38, s[6:7]
	v_mul_f32_e32 v38, 0x3db504f3, v34
	v_mov_b32_e32 v34, v36
	v_mov_b32_e32 v35, v40
	v_pk_mul_f32 v[34:35], v[34:35], v[94:95]
	v_mov_b32_e32 v40, v37
	v_sub_f32_e32 v36, v34, v35
	v_add_f32_e32 v34, v34, v35
	v_cndmask_b32_e64 v34, v34, v36, s[6:7]
	v_mul_f32_e32 v39, 0x3db504f3, v34
	v_pk_mul_f32 v[34:35], v[40:41], v[56:57]
	s_nop 0
	v_sub_f32_e32 v36, v34, v35
	v_add_f32_e32 v34, v34, v35
	v_cndmask_b32_e64 v34, v34, v36, s[6:7]
	v_mul_f32_e32 v37, 0x3db504f3, v34
	v_cvt_pk_bf16_f32 v34, v52, v46
	v_cvt_pk_bf16_f32 v35, v44, v45
	v_cvt_pk_bf16_f32 v36, v42, v38
	v_cvt_pk_bf16_f32 v37, v39, v37
	ds_write_b128 v198, v[34:37] offset:26112
	ds_write_b128 v199, v[2:5] offset:34816
	ds_write_b128 v199, v[6:9] offset:35072
	ds_write_b128 v199, v[10:13] offset:51712
	ds_write_b128 v199, v[14:17] offset:51968
	ds_write_b128 v200, v[18:21] offset:34816
	ds_write_b128 v200, v[22:25] offset:35072
	s_waitcnt vmcnt(8)
	ds_write_b128 v200, v[30:33] offset:51712
	v_mul_f32_e32 v2, v215, v145
	v_cmp_gt_f32_e32 vcc, s53, v2
	s_waitcnt vmcnt(7)
	ds_write_b128 v200, v[26:29] offset:51968
	s_waitcnt vmcnt(6)
	v_lshlrev_b32_e32 v22, 16, v63
	v_cndmask_b32_e32 v2, 0, v210, vcc
	v_fmac_f32_e32 v2, v215, v145
	v_exp_f32_e32 v6, v2
	v_cndmask_b32_e32 v7, 0, v212, vcc
	s_waitcnt vmcnt(2)
	v_mov_b32_e32 v8, v78
	s_waitcnt vmcnt(0)
	v_mov_b32_e32 v9, v82
	v_ldexp_f32 v30, v6, v7
	v_lshlrev_b32_e32 v6, 16, v62
	v_lshlrev_b32_e32 v7, 16, v66
	v_pk_mul_f32 v[8:9], v[8:9], v[6:7]
	v_lshlrev_b32_e32 v23, 16, v67
	v_sub_f32_e32 v26, v8, v9
	v_mov_b32_e32 v8, v82
	v_mov_b32_e32 v9, v78
	v_pk_mul_f32 v[6:7], v[8:9], v[6:7]
	v_mov_b32_e32 v82, v79
	v_add_f32_e32 v38, v7, v6
	v_and_b32_e32 v7, 0xffff0000, v66
	v_and_b32_e32 v6, 0xffff0000, v62
	v_mov_b32_e32 v78, v83
	v_pk_mul_f32 v[8:9], v[82:83], v[6:7]
	v_pk_mul_f32 v[6:7], v[78:79], v[6:7]
	global_load_dwordx4 v[2:5], v[96:97], off offset:192 nt
	v_add_f32_e32 v39, v7, v6
	v_mov_b32_e32 v6, v80
	v_mov_b32_e32 v7, v84
	v_pk_mul_f32 v[6:7], v[6:7], v[22:23]
	v_sub_f32_e32 v27, v8, v9
	v_sub_f32_e32 v28, v6, v7
	global_load_dwordx4 v[6:9], v[98:99], off offset:144 nt
	global_load_dwordx4 v[10:13], v[98:99], off offset:128 nt
	global_load_dwordx4 v[14:17], v[100:101], off offset:144 nt
	global_load_dwordx4 v[18:21], v[100:101], off offset:128 nt
	v_mov_b32_e32 v24, v84
	v_mov_b32_e32 v25, v80
	v_pk_mul_f32 v[22:23], v[24:25], v[22:23]
	v_mov_b32_e32 v84, v81
	v_add_f32_e32 v40, v23, v22
	v_and_b32_e32 v23, 0xffff0000, v67
	v_and_b32_e32 v22, 0xffff0000, v63
	v_mov_b32_e32 v80, v85
	v_pk_mul_f32 v[24:25], v[84:85], v[22:23]
	v_pk_mul_f32 v[22:23], v[80:81], v[22:23]
	v_sub_f32_e32 v29, v24, v25
	v_add_f32_e32 v41, v23, v22
	v_lshlrev_b32_e32 v22, 16, v64
	v_lshlrev_b32_e32 v23, 16, v68
	v_mov_b32_e32 v24, v70
	v_mov_b32_e32 v25, v74
	v_pk_mul_f32 v[24:25], v[24:25], v[22:23]
	s_nop 0
	v_sub_f32_e32 v31, v24, v25
	v_mov_b32_e32 v24, v74
	v_mov_b32_e32 v25, v70
	v_pk_mul_f32 v[22:23], v[24:25], v[22:23]
	v_mov_b32_e32 v74, v71
	v_add_f32_e32 v46, v23, v22
	v_and_b32_e32 v23, 0xffff0000, v68
	v_and_b32_e32 v22, 0xffff0000, v64
	v_mov_b32_e32 v70, v75
	v_pk_mul_f32 v[24:25], v[74:75], v[22:23]
	v_pk_mul_f32 v[22:23], v[70:71], v[22:23]
	v_sub_f32_e32 v32, v24, v25
	v_add_f32_e32 v47, v23, v22
	v_lshlrev_b32_e32 v22, 16, v65
	v_lshlrev_b32_e32 v23, 16, v69
	v_mov_b32_e32 v24, v72
	v_mov_b32_e32 v25, v76
	v_pk_mul_f32 v[24:25], v[24:25], v[22:23]
	s_nop 0
	v_sub_f32_e32 v33, v24, v25
	v_mov_b32_e32 v24, v76
	v_mov_b32_e32 v25, v72
	v_pk_mul_f32 v[22:23], v[24:25], v[22:23]
	v_mov_b32_e32 v76, v73
	v_add_f32_e32 v48, v23, v22
	v_and_b32_e32 v23, 0xffff0000, v69
	v_and_b32_e32 v22, 0xffff0000, v65
	v_mov_b32_e32 v72, v77
	v_pk_mul_f32 v[24:25], v[76:77], v[22:23]
	v_pk_mul_f32 v[22:23], v[72:73], v[22:23]
	v_sub_f32_e32 v34, v24, v25
	v_add_f32_e32 v49, v23, v22
	v_cvt_pk_bf16_f32 v22, v26, v27
	v_mul_f32_e32 v26, v30, v26
	v_mul_f32_e32 v27, v30, v27
	v_cvt_pk_bf16_f32 v23, v28, v29
	v_cvt_pk_bf16_f32 v26, v26, v27
	v_mul_f32_e32 v27, v30, v28
	v_mul_f32_e32 v28, v30, v29
	v_cvt_pk_bf16_f32 v27, v27, v28
	v_mul_f32_e32 v28, v30, v31
	v_mul_f32_e32 v29, v30, v32
	v_cvt_pk_bf16_f32 v28, v28, v29
	v_mul_f32_e32 v29, v30, v33
	v_cvt_pk_bf16_f32 v24, v31, v32
	v_mul_f32_e32 v31, v30, v34
	v_cvt_pk_bf16_f32 v29, v29, v31
	ds_write_b128 v146, v[26:29]
	v_mul_f32_e32 v26, v30, v38
	v_mul_f32_e32 v27, v30, v39
	v_cvt_pk_bf16_f32 v26, v26, v27
	v_mul_f32_e32 v27, v30, v40
	v_mul_f32_e32 v28, v30, v41
	v_cvt_pk_bf16_f32 v27, v27, v28
	v_mul_f32_e32 v28, v30, v46
	v_mul_f32_e32 v29, v30, v47
	v_cvt_pk_bf16_f32 v28, v28, v29
	v_mul_f32_e32 v29, v30, v48
	v_mul_f32_e32 v31, v30, v49
	v_cvt_pk_bf16_f32 v29, v29, v31
	ds_write_b128 v146, v[26:29] offset:128
	s_waitcnt vmcnt(4)
	v_lshlrev_b32_e32 v27, 16, v2
	v_lshlrev_b32_e32 v26, 16, v58
	s_waitcnt vmcnt(2)
	v_mov_b32_e32 v28, v10
	s_waitcnt vmcnt(0)
	v_mov_b32_e32 v29, v18
	v_pk_mul_f32 v[28:29], v[28:29], v[26:27]
	v_cvt_pk_bf16_f32 v25, v33, v34
	v_cvt_pk_bf16_f32 v38, v38, v39
	v_cvt_pk_bf16_f32 v39, v40, v41
	v_cvt_pk_bf16_f32 v40, v46, v47
	v_cvt_pk_bf16_f32 v41, v48, v49
	s_nop 0
	v_sub_f32_e32 v54, v28, v29
	v_mov_b32_e32 v28, v18
	v_mov_b32_e32 v29, v10
	v_pk_mul_f32 v[26:27], v[28:29], v[26:27]
	v_mov_b32_e32 v10, v19
	v_add_f32_e32 v62, v27, v26
	v_and_b32_e32 v27, 0xffff0000, v2
	v_and_b32_e32 v26, 0xffff0000, v58
	v_mov_b32_e32 v18, v11
	v_pk_mul_f32 v[10:11], v[10:11], v[26:27]
	v_pk_mul_f32 v[28:29], v[18:19], v[26:27]
	v_add_f32_e32 v63, v11, v10
	v_lshlrev_b32_e32 v11, 16, v3
	v_lshlrev_b32_e32 v10, 16, v59
	v_mov_b32_e32 v18, v12
	v_mov_b32_e32 v19, v20
	v_pk_mul_f32 v[18:19], v[18:19], v[10:11]
	v_and_b32_e32 v3, 0xffff0000, v3
	v_sub_f32_e32 v56, v18, v19
	v_mov_b32_e32 v18, v20
	v_mov_b32_e32 v19, v12
	v_pk_mul_f32 v[10:11], v[18:19], v[10:11]
	v_and_b32_e32 v2, 0xffff0000, v59
	v_mov_b32_e32 v20, v13
	v_mov_b32_e32 v12, v21
	v_add_f32_e32 v64, v11, v10
	v_pk_mul_f32 v[10:11], v[20:21], v[2:3]
	v_pk_mul_f32 v[2:3], v[12:13], v[2:3]
	v_sub_f32_e32 v57, v10, v11
	v_add_f32_e32 v65, v3, v2
	v_lshlrev_b32_e32 v3, 16, v4
	v_lshlrev_b32_e32 v2, 16, v60
	v_mov_b32_e32 v10, v6
	v_mov_b32_e32 v11, v14
	v_pk_mul_f32 v[10:11], v[10:11], v[2:3]
	v_sub_f32_e32 v55, v28, v29
	v_sub_f32_e32 v66, v10, v11
	v_mov_b32_e32 v10, v14
	v_mov_b32_e32 v11, v6
	v_pk_mul_f32 v[2:3], v[10:11], v[2:3]
	v_mov_b32_e32 v14, v7
	v_add_f32_e32 v67, v3, v2
	v_and_b32_e32 v3, 0xffff0000, v4
	v_and_b32_e32 v2, 0xffff0000, v60
	v_mov_b32_e32 v6, v15
	v_pk_mul_f32 v[10:11], v[14:15], v[2:3]
	v_pk_mul_f32 v[2:3], v[6:7], v[2:3]
	v_mov_b32_e32 v6, v8
	v_add_f32_e32 v69, v3, v2
	v_lshlrev_b32_e32 v3, 16, v5
	v_lshlrev_b32_e32 v2, 16, v61
	v_mov_b32_e32 v7, v16
	v_pk_mul_f32 v[6:7], v[6:7], v[2:3]
	v_sub_f32_e32 v68, v10, v11
	v_sub_f32_e32 v70, v6, v7
	v_mov_b32_e32 v6, v16
	v_mov_b32_e32 v7, v8
	v_pk_mul_f32 v[2:3], v[6:7], v[2:3]
	v_mov_b32_e32 v16, v9
	v_add_f32_e32 v71, v3, v2
	v_and_b32_e32 v3, 0xffff0000, v5
	v_and_b32_e32 v2, 0xffff0000, v61
	v_mov_b32_e32 v8, v17
	v_pk_mul_f32 v[4:5], v[16:17], v[2:3]
	v_pk_mul_f32 v[2:3], v[8:9], v[2:3]
	v_sub_f32_e32 v72, v4, v5
	v_add_f32_e32 v73, v3, v2
	v_mul_f32_e32 v2, v30, v54
	v_mul_f32_e32 v3, v30, v55
	v_cvt_pk_bf16_f32 v2, v2, v3
	v_mul_f32_e32 v3, v30, v56
	v_mul_f32_e32 v4, v30, v57
	v_cvt_pk_bf16_f32 v3, v3, v4
	v_mul_f32_e32 v4, v30, v66
	v_mul_f32_e32 v5, v30, v68
	v_cvt_pk_bf16_f32 v4, v4, v5
	v_mul_f32_e32 v5, v30, v70
	v_mul_f32_e32 v6, v30, v72
	v_cvt_pk_bf16_f32 v5, v5, v6
	ds_write_b128 v146, v[2:5] offset:64
	v_mul_f32_e32 v2, v30, v62
	v_mul_f32_e32 v3, v30, v63
	v_cvt_pk_bf16_f32 v2, v2, v3
	v_mul_f32_e32 v3, v30, v64
	v_mul_f32_e32 v4, v30, v65
	v_cvt_pk_bf16_f32 v3, v3, v4
	v_mul_f32_e32 v4, v30, v67
	v_mul_f32_e32 v5, v30, v69
	v_cvt_pk_bf16_f32 v4, v4, v5
	v_mul_f32_e32 v5, v30, v71
	v_mul_f32_e32 v6, v30, v73
	v_cvt_pk_bf16_f32 v5, v5, v6
	v_add_co_u32_e32 v6, vcc, s0, v138
	ds_write_b128 v146, v[2:5] offset:192
	s_nop 0
	v_addc_co_u32_e32 v7, vcc, 0, v139, vcc
	global_load_dwordx4 v[30:33], v[138:139], off nt
	global_load_dwordx4 v[18:21], v[138:139], off offset:64 nt
	global_load_dwordx4 v[10:13], v[138:139], off offset:128 nt
	global_load_dwordx4 v[2:5], v[138:139], off offset:192 nt
	global_load_dwordx4 v[34:37], v[6:7], off nt
	global_load_dwordx4 v[26:29], v[6:7], off offset:64 nt
	global_load_dwordx4 v[14:17], v[6:7], off offset:128 nt
	s_nop 0
	global_load_dwordx4 v[6:9], v[6:7], off offset:192 nt
	s_waitcnt lgkmcnt(0)
	s_barrier
	ds_read_b128 v[42:45], v201
	ds_read_b128 v[50:53], v201 offset:64
	v_cvt_pk_bf16_f32 v46, v54, v55
	v_cvt_pk_bf16_f32 v47, v56, v57
	ds_read_b128 v[54:57], v201 offset:128
	s_waitcnt lgkmcnt(2)
	v_mfma_f32_16x16x32_bf16 v[58:61], v[42:45], v[22:25], 0
	v_cvt_pk_bf16_f32 v48, v66, v68
	v_cvt_pk_bf16_f32 v49, v70, v72
	v_mul_f32_e32 v45, v215, v147
	s_waitcnt lgkmcnt(1)
	v_mfma_f32_16x16x32_bf16 v[50:53], v[50:53], v[46:49], v[58:61]
	v_cmp_gt_f32_e32 vcc, s53, v45
	v_cvt_pk_bf16_f32 v42, v62, v63
	v_cvt_pk_bf16_f32 v43, v64, v65
	v_cvt_pk_bf16_f32 v44, v67, v69
	v_readlane_b32 s0, v254, 16
	s_nop 2
	ds_read_b128 v[58:61], v201 offset:192
	v_cndmask_b32_e32 v45, 0, v210, vcc
	v_fmac_f32_e32 v45, v215, v147
	s_waitcnt lgkmcnt(1)
	v_mfma_f32_16x16x32_bf16 v[50:53], v[54:57], v[38:41], v[50:53]
	v_exp_f32_e32 v54, v45
	v_cndmask_b32_e32 v55, 0, v212, vcc
	v_cvt_pk_bf16_f32 v45, v71, v73
	v_readlane_b32 s1, v254, 17
	v_ldexp_f32 v54, v54, v55
	v_mul_f32_e32 v55, v215, v148
	v_cmp_gt_f32_e32 vcc, s53, v55
	s_waitcnt lgkmcnt(0)
	v_mfma_f32_16x16x32_bf16 v[50:53], v[58:61], v[42:45], v[50:53]
	ds_read_b128 v[58:61], v201 offset:4416
	v_cndmask_b32_e32 v55, 0, v210, vcc
	v_fmac_f32_e32 v55, v215, v148
	v_exp_f32_e32 v55, v55
	ds_read_b128 v[62:65], v201 offset:4480
	s_nop 2
	v_mul_f32_e32 v50, v54, v50
	v_cndmask_b32_e64 v66, 0, v50, s[0:1]
	v_cndmask_b32_e32 v50, 0, v212, vcc
	v_ldexp_f32 v50, v55, v50
	v_mul_f32_e32 v50, v50, v51
	v_mul_f32_e32 v51, v215, v149
	ds_read_b128 v[54:57], v201 offset:4352
	v_cmp_gt_f32_e32 vcc, s53, v51
	v_readlane_b32 s0, v254, 18
	v_readlane_b32 s1, v254, 19
	v_cndmask_b32_e32 v51, 0, v210, vcc
	v_fmac_f32_e32 v51, v215, v149
	v_exp_f32_e32 v51, v51
	v_cndmask_b32_e64 v67, 0, v50, s[0:1]
	v_cndmask_b32_e32 v50, 0, v212, vcc
	s_waitcnt lgkmcnt(0)
	v_mfma_f32_16x16x32_bf16 v[54:57], v[54:57], v[22:25], 0
	v_ldexp_f32 v50, v51, v50
	v_mul_f32_e32 v51, v215, v150
	v_cmp_gt_f32_e32 vcc, s53, v51
	v_mfma_f32_16x16x32_bf16 v[54:57], v[58:61], v[46:49], v[54:57]
	v_mul_f32_e32 v50, v50, v52
	v_cndmask_b32_e32 v51, 0, v210, vcc
	v_fmac_f32_e32 v51, v215, v150
	v_exp_f32_e32 v51, v51
	v_cndmask_b32_e64 v68, 0, v50, s[12:13]
	v_cndmask_b32_e32 v50, 0, v212, vcc
	ds_read_b128 v[58:61], v201 offset:4544
	v_ldexp_f32 v50, v51, v50
	v_mul_f32_e32 v69, v50, v53
	v_mfma_f32_16x16x32_bf16 v[50:53], v[62:65], v[38:41], v[54:57]
	ds_read_b128 v[62:65], v201 offset:8832
	v_cndmask_b32_e64 v69, 0, v69, s[14:15]
	s_nop 0
	v_mul_f32_e32 v54, v215, v151
	v_cmp_gt_f32_e32 vcc, s53, v54
	s_waitcnt lgkmcnt(1)
	v_mfma_f32_16x16x32_bf16 v[50:53], v[58:61], v[42:45], v[50:53]
	ds_read_b128 v[58:61], v201 offset:8768
	v_cndmask_b32_e32 v54, 0, v210, vcc
	v_fmac_f32_e32 v54, v215, v151
	v_exp_f32_e32 v54, v54
	v_cndmask_b32_e32 v55, 0, v212, vcc
	v_ldexp_f32 v54, v54, v55
	v_mul_f32_e32 v55, v215, v152
	v_cmp_gt_f32_e32 vcc, s53, v55
	v_mul_f32_e32 v50, v54, v50
	v_cndmask_b32_e64 v70, 0, v50, s[16:17]
	v_cndmask_b32_e32 v55, 0, v210, vcc
	v_fmac_f32_e32 v55, v215, v152
	v_exp_f32_e32 v55, v55
	v_cndmask_b32_e32 v50, 0, v212, vcc
	v_ldexp_f32 v50, v55, v50
	v_mul_f32_e32 v50, v50, v51
	v_mul_f32_e32 v51, v215, v153
	ds_read_b128 v[54:57], v201 offset:8704
	v_cmp_gt_f32_e32 vcc, s53, v51
	v_cndmask_b32_e64 v71, 0, v50, s[18:19]
	s_waitcnt lgkmcnt(0)
	v_mfma_f32_16x16x32_bf16 v[54:57], v[54:57], v[22:25], 0
	v_cndmask_b32_e32 v51, 0, v210, vcc
	v_fmac_f32_e32 v51, v215, v153
	v_exp_f32_e32 v51, v51
	v_cndmask_b32_e32 v50, 0, v212, vcc
	v_mfma_f32_16x16x32_bf16 v[54:57], v[58:61], v[46:49], v[54:57]
	ds_read_b128 v[58:61], v201 offset:8896
	v_ldexp_f32 v50, v51, v50
	v_mul_f32_e32 v51, v215, v154
	v_cmp_gt_f32_e32 vcc, s53, v51
	v_mul_f32_e32 v50, v50, v52
	v_cndmask_b32_e64 v72, 0, v50, s[20:21]
	v_cndmask_b32_e32 v51, 0, v210, vcc
	v_fmac_f32_e32 v51, v215, v154
	v_exp_f32_e32 v51, v51
	v_cndmask_b32_e32 v50, 0, v212, vcc
	v_ldexp_f32 v50, v51, v50
	v_mul_f32_e32 v73, v50, v53
	v_mfma_f32_16x16x32_bf16 v[50:53], v[62:65], v[38:41], v[54:57]
	ds_read_b128 v[62:65], v201 offset:13184
	v_cndmask_b32_e64 v73, 0, v73, s[22:23]
	s_nop 0
	v_mul_f32_e32 v54, v215, v155
	v_cmp_gt_f32_e32 vcc, s53, v54
	s_waitcnt lgkmcnt(1)
	v_mfma_f32_16x16x32_bf16 v[50:53], v[58:61], v[42:45], v[50:53]
	ds_read_b128 v[58:61], v201 offset:13120
	v_cndmask_b32_e32 v54, 0, v210, vcc
	v_fmac_f32_e32 v54, v215, v155
	v_exp_f32_e32 v54, v54
	v_cndmask_b32_e32 v55, 0, v212, vcc
	v_ldexp_f32 v54, v54, v55
	v_mul_f32_e32 v55, v215, v156
	v_cmp_gt_f32_e32 vcc, s53, v55
	v_mul_f32_e32 v50, v54, v50
	v_cndmask_b32_e64 v74, 0, v50, s[24:25]
	v_cndmask_b32_e32 v55, 0, v210, vcc
	v_fmac_f32_e32 v55, v215, v156
	v_exp_f32_e32 v55, v55
	v_cndmask_b32_e32 v50, 0, v212, vcc
	v_ldexp_f32 v50, v55, v50
	v_mul_f32_e32 v50, v50, v51
	v_mul_f32_e32 v51, v215, v157
	ds_read_b128 v[54:57], v201 offset:13056
	v_cmp_gt_f32_e32 vcc, s53, v51
	v_cndmask_b32_e64 v75, 0, v50, s[26:27]
	s_waitcnt lgkmcnt(0)
	v_mfma_f32_16x16x32_bf16 v[54:57], v[54:57], v[22:25], 0
	v_cndmask_b32_e32 v51, 0, v210, vcc
	v_fmac_f32_e32 v51, v215, v157
	v_exp_f32_e32 v51, v51
	v_cndmask_b32_e32 v50, 0, v212, vcc
	v_mfma_f32_16x16x32_bf16 v[54:57], v[58:61], v[46:49], v[54:57]
	ds_read_b128 v[58:61], v201 offset:13248
	v_ldexp_f32 v50, v51, v50
	v_mul_f32_e32 v51, v215, v158
	v_cmp_gt_f32_e32 vcc, s53, v51
	v_mul_f32_e32 v50, v50, v52
	v_cndmask_b32_e64 v76, 0, v50, s[28:29]
	v_cndmask_b32_e32 v51, 0, v210, vcc
	v_fmac_f32_e32 v51, v215, v158
	v_exp_f32_e32 v51, v51
	v_cndmask_b32_e32 v50, 0, v212, vcc
	v_ldexp_f32 v50, v51, v50
	v_mul_f32_e32 v77, v50, v53
	v_mfma_f32_16x16x32_bf16 v[50:53], v[62:65], v[38:41], v[54:57]
	ds_read_b128 v[62:65], v201 offset:17536
	v_cndmask_b32_e64 v77, 0, v77, s[30:31]
	s_nop 0
	v_mul_f32_e32 v54, v215, v159
	v_cmp_gt_f32_e32 vcc, s53, v54
	s_waitcnt lgkmcnt(1)
	v_mfma_f32_16x16x32_bf16 v[50:53], v[58:61], v[42:45], v[50:53]
	ds_read_b128 v[58:61], v201 offset:17472
	v_cndmask_b32_e32 v54, 0, v210, vcc
	v_fmac_f32_e32 v54, v215, v159
	v_exp_f32_e32 v54, v54
	v_cndmask_b32_e32 v55, 0, v212, vcc
	v_ldexp_f32 v54, v54, v55
	v_mul_f32_e32 v55, v215, v160
	v_cmp_gt_f32_e32 vcc, s53, v55
	v_mul_f32_e32 v50, v54, v50
	v_cndmask_b32_e64 v78, 0, v50, s[34:35]
	v_cndmask_b32_e32 v55, 0, v210, vcc
	v_fmac_f32_e32 v55, v215, v160
	v_exp_f32_e32 v55, v55
	v_cndmask_b32_e32 v50, 0, v212, vcc
	v_ldexp_f32 v50, v55, v50
	v_mul_f32_e32 v50, v50, v51
	v_mul_f32_e32 v51, v215, v161
	ds_read_b128 v[54:57], v201 offset:17408
	v_cmp_gt_f32_e32 vcc, s53, v51
	v_cndmask_b32_e64 v79, 0, v50, s[36:37]
	s_waitcnt lgkmcnt(0)
	v_mfma_f32_16x16x32_bf16 v[54:57], v[54:57], v[22:25], 0
	v_cndmask_b32_e32 v51, 0, v210, vcc
	v_fmac_f32_e32 v51, v215, v161
	v_exp_f32_e32 v51, v51
	v_cndmask_b32_e32 v50, 0, v212, vcc
	v_mfma_f32_16x16x32_bf16 v[54:57], v[58:61], v[46:49], v[54:57]
	ds_read_b128 v[58:61], v201 offset:17600
	v_ldexp_f32 v50, v51, v50
	v_mul_f32_e32 v51, v215, v162
	v_cmp_gt_f32_e32 vcc, s53, v51
	v_mul_f32_e32 v50, v50, v52
	v_cndmask_b32_e64 v80, 0, v50, s[38:39]
	v_cndmask_b32_e32 v51, 0, v210, vcc
	v_fmac_f32_e32 v51, v215, v162
	v_exp_f32_e32 v51, v51
	v_cndmask_b32_e32 v50, 0, v212, vcc
	v_ldexp_f32 v50, v51, v50
	v_mul_f32_e32 v81, v50, v53
	v_mfma_f32_16x16x32_bf16 v[50:53], v[62:65], v[38:41], v[54:57]
	ds_read_b128 v[62:65], v201 offset:21888
	v_cndmask_b32_e64 v81, 0, v81, s[40:41]
	s_nop 0
	v_mul_f32_e32 v54, v215, v163
	v_cmp_gt_f32_e32 vcc, s53, v54
	s_waitcnt lgkmcnt(1)
	v_mfma_f32_16x16x32_bf16 v[50:53], v[58:61], v[42:45], v[50:53]
	ds_read_b128 v[58:61], v201 offset:21824
	v_cndmask_b32_e32 v54, 0, v210, vcc
	v_fmac_f32_e32 v54, v215, v163
	v_exp_f32_e32 v54, v54
	v_cndmask_b32_e32 v55, 0, v212, vcc
	v_ldexp_f32 v54, v54, v55
	v_mul_f32_e32 v55, v215, v164
	v_cmp_gt_f32_e32 vcc, s53, v55
	v_mul_f32_e32 v50, v54, v50
	v_cndmask_b32_e64 v82, 0, v50, s[42:43]
	v_cndmask_b32_e32 v55, 0, v210, vcc
	v_fmac_f32_e32 v55, v215, v164
	v_exp_f32_e32 v55, v55
	v_cndmask_b32_e32 v50, 0, v212, vcc
	v_ldexp_f32 v50, v55, v50
	v_mul_f32_e32 v50, v50, v51
	v_mul_f32_e32 v51, v215, v165
	ds_read_b128 v[54:57], v201 offset:21760
	v_cmp_gt_f32_e32 vcc, s53, v51
	v_cndmask_b32_e64 v83, 0, v50, s[44:45]
	s_waitcnt lgkmcnt(0)
	v_mfma_f32_16x16x32_bf16 v[54:57], v[54:57], v[22:25], 0
	v_cndmask_b32_e32 v51, 0, v210, vcc
	v_fmac_f32_e32 v51, v215, v165
	v_exp_f32_e32 v51, v51
	v_cndmask_b32_e32 v50, 0, v212, vcc
	v_mfma_f32_16x16x32_bf16 v[54:57], v[58:61], v[46:49], v[54:57]
	ds_read_b128 v[58:61], v201 offset:21952
	v_ldexp_f32 v50, v51, v50
	v_mul_f32_e32 v51, v215, v166
	v_cmp_gt_f32_e32 vcc, s53, v51
	v_mul_f32_e32 v50, v50, v52
	v_cndmask_b32_e64 v84, 0, v50, s[46:47]
	v_cndmask_b32_e32 v51, 0, v210, vcc
	v_fmac_f32_e32 v51, v215, v166
	v_exp_f32_e32 v51, v51
	v_cndmask_b32_e32 v50, 0, v212, vcc
	v_ldexp_f32 v50, v51, v50
	v_mul_f32_e32 v85, v50, v53
	v_mfma_f32_16x16x32_bf16 v[50:53], v[62:65], v[38:41], v[54:57]
	ds_read_b128 v[62:65], v201 offset:26240
	v_cndmask_b32_e64 v85, 0, v85, s[2:3]
	s_nop 0
	v_mul_f32_e32 v54, v215, v168
	v_cmp_gt_f32_e32 vcc, s53, v54
	s_waitcnt lgkmcnt(1)
	v_mfma_f32_16x16x32_bf16 v[50:53], v[58:61], v[42:45], v[50:53]
	ds_read_b128 v[58:61], v201 offset:26176
	v_cndmask_b32_e32 v54, 0, v210, vcc
	v_fmac_f32_e32 v54, v215, v168
	v_exp_f32_e32 v54, v54
	v_cndmask_b32_e32 v55, 0, v212, vcc
	v_ldexp_f32 v54, v54, v55
	v_mul_f32_e32 v55, v215, v169
	v_cmp_gt_f32_e32 vcc, s53, v55
	v_mul_f32_e32 v50, v54, v50
	v_cndmask_b32_e64 v86, 0, v50, s[4:5]
	v_cndmask_b32_e32 v55, 0, v210, vcc
	v_fmac_f32_e32 v55, v215, v169
	v_exp_f32_e32 v55, v55
	v_cndmask_b32_e32 v50, 0, v212, vcc
	v_ldexp_f32 v50, v55, v50
	v_mul_f32_e32 v50, v50, v51
	v_mul_f32_e32 v51, v215, v170
	ds_read_b128 v[54:57], v201 offset:26112
	v_cmp_gt_f32_e32 vcc, s53, v51
	v_cndmask_b32_e64 v87, 0, v50, s[78:79]
	s_waitcnt lgkmcnt(0)
	v_mfma_f32_16x16x32_bf16 v[54:57], v[54:57], v[22:25], 0
	v_cndmask_b32_e32 v51, 0, v210, vcc
	v_fmac_f32_e32 v51, v215, v170
	v_exp_f32_e32 v51, v51
	v_cndmask_b32_e32 v50, 0, v212, vcc
	v_mfma_f32_16x16x32_bf16 v[54:57], v[58:61], v[46:49], v[54:57]
	ds_read_b128 v[58:61], v201 offset:26304
	v_ldexp_f32 v50, v51, v50
	v_mul_f32_e32 v51, v215, v171
	v_cmp_gt_f32_e32 vcc, s53, v51
	v_mul_f32_e32 v50, v50, v52
	v_cndmask_b32_e64 v88, 0, v50, s[54:55]
	v_cndmask_b32_e32 v51, 0, v210, vcc
	v_fmac_f32_e32 v51, v215, v171
	v_exp_f32_e32 v51, v51
	v_cndmask_b32_e32 v50, 0, v212, vcc
	v_ldexp_f32 v50, v51, v50
	v_mul_f32_e32 v89, v50, v53
	v_mfma_f32_16x16x32_bf16 v[50:53], v[62:65], v[38:41], v[54:57]
	v_mul_f32_e32 v62, v215, v175
	v_cndmask_b32_e64 v89, 0, v89, s[56:57]
	s_nop 0
	v_mul_f32_e32 v54, v215, v172
	v_cmp_gt_f32_e32 vcc, s53, v54
	s_waitcnt lgkmcnt(0)
	v_mfma_f32_16x16x32_bf16 v[50:53], v[58:61], v[42:45], v[50:53]
	v_cndmask_b32_e32 v54, 0, v210, vcc
	v_fmac_f32_e32 v54, v215, v172
	v_exp_f32_e32 v54, v54
	v_cndmask_b32_e32 v55, 0, v212, vcc
	v_ldexp_f32 v54, v54, v55
	v_mul_f32_e32 v55, v215, v173
	v_cmp_gt_f32_e32 vcc, s53, v55
	s_nop 0
	v_mul_f32_e32 v50, v54, v50
	v_cndmask_b32_e64 v50, 0, v50, s[58:59]
	v_cndmask_b32_e32 v55, 0, v210, vcc
	v_fmac_f32_e32 v55, v215, v173
	v_exp_f32_e32 v55, v55
	v_cndmask_b32_e32 v54, 0, v212, vcc
	v_ldexp_f32 v54, v55, v54
	v_mul_f32_e32 v51, v54, v51
	v_mul_f32_e32 v54, v215, v174
	v_cmp_gt_f32_e32 vcc, s53, v54
	v_cndmask_b32_e64 v51, 0, v51, s[60:61]
	s_nop 0
	v_cndmask_b32_e32 v54, 0, v210, vcc
	v_fmac_f32_e32 v54, v215, v174
	v_exp_f32_e32 v58, v54
	ds_read_b128 v[54:57], v201 offset:30464
	v_cndmask_b32_e32 v59, 0, v212, vcc
	v_cmp_gt_f32_e32 vcc, s53, v62
	v_ldexp_f32 v58, v58, v59
	v_mul_f32_e32 v52, v58, v52
	ds_read_b128 v[58:61], v201 offset:30528
	ds_read_b128 v[62:65], v201 offset:30592
	s_waitcnt lgkmcnt(2)
	v_mfma_f32_16x16x32_bf16 v[22:25], v[54:57], v[22:25], 0
	v_cndmask_b32_e32 v90, 0, v210, vcc
	v_cndmask_b32_e32 v55, 0, v212, vcc
	v_fmac_f32_e32 v90, v215, v175
	s_waitcnt lgkmcnt(1)
	v_mfma_f32_16x16x32_bf16 v[22:25], v[58:61], v[46:49], v[22:25]
	ds_read_b128 v[46:49], v201 offset:30656
	v_exp_f32_e32 v54, v90
	s_waitcnt lgkmcnt(0)
	v_mfma_f32_16x16x32_bf16 v[22:25], v[62:65], v[38:41], v[22:25]
	v_mul_f32_e32 v38, v215, v176
	v_cmp_gt_f32_e32 vcc, s53, v38
	v_ldexp_f32 v54, v54, v55
	v_mfma_f32_16x16x32_bf16 v[22:25], v[46:49], v[42:45], v[22:25]
	v_cndmask_b32_e32 v38, 0, v210, vcc
	v_fmac_f32_e32 v38, v215, v176
	v_exp_f32_e32 v38, v38
	v_cndmask_b32_e32 v40, 0, v212, vcc
	s_barrier
	v_ldexp_f32 v38, v38, v40
	v_mul_f32_e32 v40, v215, v177
	v_cmp_gt_f32_e32 vcc, s53, v40
	v_mul_f32_e32 v22, v38, v22
	v_cndmask_b32_e64 v38, 0, v22, s[66:67]
	v_cndmask_b32_e32 v40, 0, v210, vcc
	v_fmac_f32_e32 v40, v215, v177
	v_exp_f32_e32 v40, v40
	v_cndmask_b32_e32 v22, 0, v212, vcc
	v_mul_f32_e32 v53, v54, v53
	v_cndmask_b32_e64 v52, 0, v52, s[62:63]
	v_ldexp_f32 v22, v40, v22
	v_mul_f32_e32 v40, v215, v178
	v_cmp_gt_f32_e32 vcc, s53, v40
	v_mul_f32_e32 v22, v22, v23
	v_mul_f32_e32 v23, v215, v179
	v_cndmask_b32_e32 v40, 0, v210, vcc
	v_fmac_f32_e32 v40, v215, v178
	v_exp_f32_e32 v40, v40
	v_cndmask_b32_e64 v41, 0, v22, s[68:69]
	v_cndmask_b32_e32 v22, 0, v212, vcc
	v_cmp_gt_f32_e32 vcc, s53, v23
	v_ldexp_f32 v22, v40, v22
	v_mul_f32_e32 v22, v22, v24
	v_cndmask_b32_e32 v23, 0, v210, vcc
	v_fmac_f32_e32 v23, v215, v179
	v_exp_f32_e32 v23, v23
	v_cndmask_b32_e64 v40, 0, v22, s[70:71]
	v_cndmask_b32_e32 v22, 0, v212, vcc
	v_cvt_pk_bf16_f32 v24, v70, v71
	v_ldexp_f32 v22, v23, v22
	v_mul_f32_e32 v22, v22, v25
	v_cndmask_b32_e64 v42, 0, v22, s[72:73]
	v_cvt_pk_bf16_f32 v22, v66, v67
	v_cvt_pk_bf16_f32 v23, v68, v69
	v_cvt_pk_bf16_f32 v25, v72, v73
	ds_write2_b64 v202, v[22:23], v[24:25] offset1:4
	v_cvt_pk_bf16_f32 v22, v74, v75
	v_cvt_pk_bf16_f32 v23, v76, v77
	v_cvt_pk_bf16_f32 v24, v78, v79
	v_cvt_pk_bf16_f32 v25, v80, v81
	ds_write2_b64 v202, v[22:23], v[24:25] offset0:8 offset1:12
	v_cvt_pk_bf16_f32 v22, v82, v83
	v_cvt_pk_bf16_f32 v23, v84, v85
	v_cvt_pk_bf16_f32 v24, v86, v87
	v_cvt_pk_bf16_f32 v25, v88, v89
	v_cndmask_b32_e64 v39, 0, v53, s[64:65]
	ds_write2_b64 v202, v[22:23], v[24:25] offset0:16 offset1:20
	v_cvt_pk_bf16_f32 v22, v50, v51
	v_cvt_pk_bf16_f32 v23, v52, v39
	v_cvt_pk_bf16_f32 v24, v38, v41
	v_cvt_pk_bf16_f32 v25, v40, v42
	ds_write2_b64 v202, v[22:23], v[24:25] offset0:24 offset1:28
	s_waitcnt lgkmcnt(0)
	s_barrier
	ds_read_b128 v[22:25], v203
	ds_read_b128 v[38:41], v203 offset:64
	ds_read_b128 v[46:49], v203 offset:4352
	ds_read_b128 v[50:53], v203 offset:4416
	ds_read_b128 v[58:61], v203 offset:8704
	ds_read_b128 v[62:65], v203 offset:8768
	ds_read_b128 v[70:73], v203 offset:13056
	ds_read_b128 v[74:77], v203 offset:13120
	ds_read_b128 v[82:85], v203 offset:17408
	ds_read_b128 v[86:89], v203 offset:17472
	ds_read_b128 v[94:97], v203 offset:21760
	ds_read_b128 v[98:101], v203 offset:21824
	ds_read_b128 v[106:109], v203 offset:26112
	ds_read_b128 v[110:113], v203 offset:26176
	ds_read_b128 v[118:121], v203 offset:30464
	ds_read_b128 v[216:219], v203 offset:30528
	s_waitcnt vmcnt(7) lgkmcnt(14)
	v_mfma_f32_16x16x32_bf16 v[42:45], v[30:33], v[22:25], 0
	s_waitcnt vmcnt(3)
	v_mfma_f32_16x16x32_bf16 v[22:25], v[34:37], v[22:25], 0
	s_waitcnt lgkmcnt(13)
	v_mfma_f32_16x16x32_bf16 v[54:57], v[30:33], v[46:49], 0
	v_mfma_f32_16x16x32_bf16 v[46:49], v[34:37], v[46:49], 0
	s_waitcnt lgkmcnt(11)
	v_mfma_f32_16x16x32_bf16 v[66:69], v[30:33], v[58:61], 0
	v_mfma_f32_16x16x32_bf16 v[58:61], v[34:37], v[58:61], 0
	s_waitcnt lgkmcnt(9)
	v_mfma_f32_16x16x32_bf16 v[78:81], v[30:33], v[70:73], 0
	v_mfma_f32_16x16x32_bf16 v[70:73], v[34:37], v[70:73], 0
	s_waitcnt lgkmcnt(7)
	v_mfma_f32_16x16x32_bf16 v[90:93], v[30:33], v[82:85], 0
	v_mfma_f32_16x16x32_bf16 v[82:85], v[34:37], v[82:85], 0
	s_waitcnt lgkmcnt(5)
	v_mfma_f32_16x16x32_bf16 v[102:105], v[30:33], v[94:97], 0
	v_mfma_f32_16x16x32_bf16 v[94:97], v[34:37], v[94:97], 0
	s_waitcnt lgkmcnt(3)
	v_mfma_f32_16x16x32_bf16 v[114:117], v[30:33], v[106:109], 0
	v_mfma_f32_16x16x32_bf16 v[106:109], v[34:37], v[106:109], 0
	s_waitcnt lgkmcnt(1)
	v_mfma_f32_16x16x32_bf16 v[30:33], v[30:33], v[118:121], 0
	v_mfma_f32_16x16x32_bf16 v[34:37], v[34:37], v[118:121], 0
	v_mfma_f32_16x16x32_bf16 v[42:45], v[18:21], v[38:41], v[42:45]
	s_waitcnt vmcnt(2)
	v_mfma_f32_16x16x32_bf16 v[22:25], v[26:29], v[38:41], v[22:25]
	v_mfma_f32_16x16x32_bf16 v[38:41], v[18:21], v[50:53], v[54:57]
	v_mfma_f32_16x16x32_bf16 v[46:49], v[26:29], v[50:53], v[46:49]
	v_mfma_f32_16x16x32_bf16 v[50:53], v[18:21], v[62:65], v[66:69]
	v_mfma_f32_16x16x32_bf16 v[54:57], v[26:29], v[62:65], v[58:61]
	v_mfma_f32_16x16x32_bf16 v[58:61], v[18:21], v[74:77], v[78:81]
	v_mfma_f32_16x16x32_bf16 v[62:65], v[26:29], v[74:77], v[70:73]
	v_mfma_f32_16x16x32_bf16 v[66:69], v[18:21], v[86:89], v[90:93]
	v_mfma_f32_16x16x32_bf16 v[70:73], v[26:29], v[86:89], v[82:85]
	v_mfma_f32_16x16x32_bf16 v[74:77], v[18:21], v[98:101], v[102:105]
	v_mfma_f32_16x16x32_bf16 v[78:81], v[26:29], v[98:101], v[94:97]
	v_mfma_f32_16x16x32_bf16 v[82:85], v[18:21], v[110:113], v[114:117]
	v_mfma_f32_16x16x32_bf16 v[86:89], v[26:29], v[110:113], v[106:109]
	s_waitcnt lgkmcnt(0)
	v_mfma_f32_16x16x32_bf16 v[18:21], v[18:21], v[216:219], v[30:33]
	v_mfma_f32_16x16x32_bf16 v[26:29], v[26:29], v[216:219], v[34:37]
	s_nop 1
	ds_read_b128 v[30:33], v203 offset:128
	ds_read_b128 v[34:37], v203 offset:192
	s_waitcnt lgkmcnt(1)
	v_mfma_f32_16x16x32_bf16 v[42:45], v[10:13], v[30:33], v[42:45]
	s_waitcnt vmcnt(1)
	v_mfma_f32_16x16x32_bf16 v[22:25], v[14:17], v[30:33], v[22:25]
	ds_read_b128 v[30:33], v203 offset:4480
	ds_read_b128 v[90:93], v203 offset:4544
	s_waitcnt lgkmcnt(1)
	v_mfma_f32_16x16x32_bf16 v[38:41], v[10:13], v[30:33], v[38:41]
	v_mfma_f32_16x16x32_bf16 v[30:33], v[14:17], v[30:33], v[46:49]
	s_nop 2
	ds_read_b128 v[46:49], v203 offset:8832
	ds_read_b128 v[94:97], v203 offset:8896
	s_waitcnt lgkmcnt(1)
	v_mfma_f32_16x16x32_bf16 v[50:53], v[10:13], v[46:49], v[50:53]
	v_mfma_f32_16x16x32_bf16 v[46:49], v[14:17], v[46:49], v[54:57]
	s_nop 2
	ds_read_b128 v[54:57], v203 offset:13184
	ds_read_b128 v[98:101], v203 offset:13248
	s_waitcnt lgkmcnt(1)
	v_mfma_f32_16x16x32_bf16 v[58:61], v[10:13], v[54:57], v[58:61]
	v_mfma_f32_16x16x32_bf16 v[54:57], v[14:17], v[54:57], v[62:65]
	s_nop 2
	ds_read_b128 v[62:65], v203 offset:17536
	ds_read_b128 v[102:105], v203 offset:17600
	s_waitcnt lgkmcnt(1)
	v_mfma_f32_16x16x32_bf16 v[66:69], v[10:13], v[62:65], v[66:69]
	v_mfma_f32_16x16x32_bf16 v[62:65], v[14:17], v[62:65], v[70:73]
	s_nop 2
	ds_read_b128 v[70:73], v203 offset:21888
	ds_read_b128 v[106:109], v203 offset:21952
	s_waitcnt lgkmcnt(1)
	v_mfma_f32_16x16x32_bf16 v[74:77], v[10:13], v[70:73], v[74:77]
	v_mfma_f32_16x16x32_bf16 v[70:73], v[14:17], v[70:73], v[78:81]
	s_nop 2
	ds_read_b128 v[78:81], v203 offset:26240
	ds_read_b128 v[110:113], v203 offset:26304
	s_waitcnt lgkmcnt(1)
	v_mfma_f32_16x16x32_bf16 v[82:85], v[10:13], v[78:81], v[82:85]
	v_mfma_f32_16x16x32_bf16 v[78:81], v[14:17], v[78:81], v[86:89]
	s_nop 2
	ds_read_b128 v[86:89], v203 offset:30592
	ds_read_b128 v[114:117], v203 offset:30656
	s_waitcnt lgkmcnt(1)
	v_mfma_f32_16x16x32_bf16 v[10:13], v[10:13], v[86:89], v[18:21]
	v_mfma_f32_16x16x32_bf16 v[14:17], v[14:17], v[86:89], v[26:29]
	v_mfma_f32_16x16x32_bf16 v[18:21], v[2:5], v[34:37], v[42:45]
	v_mfma_f32_16x16x32_bf16 v[26:29], v[2:5], v[90:93], v[38:41]
	v_mfma_f32_16x16x32_bf16 v[38:41], v[2:5], v[94:97], v[50:53]
	v_mfma_f32_16x16x32_bf16 v[50:53], v[2:5], v[98:101], v[58:61]
	v_mfma_f32_16x16x32_bf16 v[66:69], v[2:5], v[102:105], v[66:69]
	v_mfma_f32_16x16x32_bf16 v[74:77], v[2:5], v[106:109], v[74:77]
	v_mfma_f32_16x16x32_bf16 v[82:85], v[2:5], v[110:113], v[82:85]
	s_waitcnt lgkmcnt(0)
	v_mfma_f32_16x16x32_bf16 v[2:5], v[2:5], v[114:117], v[10:13]
	ds_read_b64_tr_b16 v[10:11], v180 offset:0
	ds_read_b64_tr_b16 v[12:13], v180 offset:0x840
	ds_read_b64_tr_b16 v[86:87], v180 offset:32
	ds_read_b64_tr_b16 v[88:89], v180 offset:0x860
	s_waitcnt vmcnt(0)
	v_mfma_f32_16x16x32_bf16 v[22:25], v[6:9], v[34:37], v[22:25]
	s_waitcnt lgkmcnt(0)
	v_mfma_f32_16x16x32_bf16 v[34:37], v[6:9], v[90:93], v[30:33]
	v_mfma_f32_16x16x32_bf16 v[46:49], v[6:9], v[94:97], v[46:49]
	v_mfma_f32_16x16x32_bf16 v[54:57], v[6:9], v[98:101], v[54:57]
	v_mfma_f32_16x16x32_bf16 v[62:65], v[6:9], v[102:105], v[62:65]
	v_mfma_f32_16x16x32_bf16 v[70:73], v[6:9], v[106:109], v[70:73]
	v_mfma_f32_16x16x32_bf16 v[78:81], v[6:9], v[110:113], v[78:81]
	v_mfma_f32_16x16x32_bf16 v[6:9], v[6:9], v[114:117], v[14:17]
	s_nop 2
	ds_read_b128 v[14:17], v204
	ds_read_b128 v[90:93], v204 offset:4352
	s_waitcnt lgkmcnt(1)
	v_mfma_f32_16x16x32_bf16 v[58:61], v[10:13], v[14:17], v[18:21]
	v_mfma_f32_16x16x32_bf16 v[42:45], v[86:89], v[14:17], v[22:25]
	s_nop 1
	ds_read_b128 v[18:21], v204 offset:8704
	ds_read_b128 v[22:25], v204 offset:13056
	s_waitcnt lgkmcnt(2)
	v_mfma_f32_16x16x32_bf16 v[30:33], v[10:13], v[90:93], v[26:29]
	s_waitcnt lgkmcnt(1)
	v_mfma_f32_16x16x32_bf16 v[26:29], v[10:13], v[18:21], v[38:41]
	v_mfma_f32_16x16x32_bf16 v[18:21], v[86:89], v[18:21], v[46:49]
	s_nop 1
	ds_read_b128 v[38:41], v204 offset:17408
	ds_read_b128 v[46:49], v204 offset:21760
	v_mfma_f32_16x16x32_bf16 v[14:17], v[86:89], v[90:93], v[34:37]
	s_waitcnt lgkmcnt(2)
	v_mfma_f32_16x16x32_bf16 v[34:37], v[10:13], v[22:25], v[50:53]
	v_mfma_f32_16x16x32_bf16 v[22:25], v[86:89], v[22:25], v[54:57]
	s_waitcnt lgkmcnt(1)
	v_mfma_f32_16x16x32_bf16 v[50:53], v[10:13], v[38:41], v[66:69]
	v_mfma_f32_16x16x32_bf16 v[38:41], v[86:89], v[38:41], v[62:65]
	s_waitcnt lgkmcnt(0)
	v_mfma_f32_16x16x32_bf16 v[54:57], v[10:13], v[46:49], v[74:77]
	v_mfma_f32_16x16x32_bf16 v[66:69], v[86:89], v[46:49], v[70:73]
	ds_read_b128 v[46:49], v204 offset:26112
	ds_read_b128 v[62:65], v204 offset:30464
	s_waitcnt lgkmcnt(1)
	v_mfma_f32_16x16x32_bf16 v[70:73], v[10:13], v[46:49], v[82:85]
	s_waitcnt lgkmcnt(0)
	v_mfma_f32_16x16x32_bf16 v[2:5], v[10:13], v[62:65], v[2:5]
	ds_read_b64_tr_b16 v[10:11], v180 offset:0x4200
	ds_read_b64_tr_b16 v[12:13], v180 offset:0x4a40
	v_mfma_f32_16x16x32_bf16 v[74:77], v[86:89], v[46:49], v[78:81]
	ds_read_b64_tr_b16 v[78:79], v180 offset:0x4220
	ds_read_b64_tr_b16 v[80:81], v180 offset:0x4a60
	s_nop 0
	s_waitcnt lgkmcnt(0)
	ds_read_b128 v[46:49], v204 offset:8768
	ds_read_b128 v[82:85], v204 offset:13120
	v_mfma_f32_16x16x32_bf16 v[6:9], v[86:89], v[62:65], v[6:9]
	s_waitcnt lgkmcnt(1)
	v_mfma_f32_16x16x32_bf16 v[62:65], v[10:13], v[46:49], v[26:29]
	v_mfma_f32_16x16x32_bf16 v[46:49], v[78:81], v[46:49], v[18:21]
	s_waitcnt lgkmcnt(0)
	v_mfma_f32_16x16x32_bf16 v[18:21], v[78:81], v[82:85], v[22:25]
	s_nop 2
	ds_read_b128 v[22:25], v204 offset:17472
	ds_read_b128 v[26:29], v204 offset:21824
	v_mfma_f32_16x16x32_bf16 v[34:37], v[10:13], v[82:85], v[34:37]
	s_waitcnt lgkmcnt(1)
	v_mfma_f32_16x16x32_bf16 v[50:53], v[10:13], v[22:25], v[50:53]
	v_mfma_f32_16x16x32_bf16 v[22:25], v[78:81], v[22:25], v[38:41]
	s_waitcnt lgkmcnt(0)
	v_mfma_f32_16x16x32_bf16 v[82:85], v[10:13], v[26:29], v[54:57]
	s_nop 0
	ds_read_b128 v[38:41], v204 offset:26176
	s_nop 0
	ds_read_b128 v[54:57], v204 offset:30528
	v_mfma_f32_16x16x32_bf16 v[26:29], v[78:81], v[26:29], v[66:69]
	s_waitcnt lgkmcnt(1)
	v_mfma_f32_16x16x32_bf16 v[66:69], v[10:13], v[38:41], v[70:73]
	v_mfma_f32_16x16x32_bf16 v[70:73], v[78:81], v[38:41], v[74:77]
	ds_read_b64_tr_b16 v[74:75], v180 offset:0x8400
	ds_read_b64_tr_b16 v[76:77], v180 offset:0x8c40
	s_waitcnt lgkmcnt(0)
	v_mfma_f32_16x16x32_bf16 v[2:5], v[10:13], v[54:57], v[2:5]
	v_mfma_f32_16x16x32_bf16 v[10:13], v[78:81], v[54:57], v[6:9]
	ds_read_b64_tr_b16 v[78:79], v180 offset:0x8420
	ds_read_b64_tr_b16 v[80:81], v180 offset:0x8c60
	s_nop 0
	s_waitcnt lgkmcnt(0)
	s_nop 1
	ds_read_b128 v[6:9], v204 offset:17536
	ds_read_b128 v[86:89], v204 offset:21888
	s_waitcnt lgkmcnt(1)
	v_mfma_f32_16x16x32_bf16 v[54:57], v[74:77], v[6:9], v[50:53]
	v_mfma_f32_16x16x32_bf16 v[38:41], v[78:81], v[6:9], v[22:25]
	s_waitcnt lgkmcnt(0)
	v_mfma_f32_16x16x32_bf16 v[6:9], v[78:81], v[86:89], v[26:29]
	s_nop 2
	ds_read_b128 v[26:29], v204 offset:26240
	ds_read_b128 v[50:53], v204 offset:30592
	v_mfma_f32_16x16x32_bf16 v[22:25], v[74:77], v[86:89], v[82:85]
	s_waitcnt lgkmcnt(1)
	v_mfma_f32_16x16x32_bf16 v[66:69], v[74:77], v[26:29], v[66:69]
	s_waitcnt lgkmcnt(0)
	v_mfma_f32_16x16x32_bf16 v[2:5], v[74:77], v[50:53], v[2:5]
	ds_read_b64_tr_b16 v[74:75], v180 offset:0xc600
	ds_read_b64_tr_b16 v[76:77], v180 offset:0xce40
	v_mfma_f32_16x16x32_bf16 v[70:73], v[78:81], v[26:29], v[70:73]
	v_mfma_f32_16x16x32_bf16 v[50:53], v[78:81], v[50:53], v[10:13]
	ds_read_b64_tr_b16 v[78:79], v180 offset:0xc620
	ds_read_b64_tr_b16 v[80:81], v180 offset:0xce60
	s_nop 0
	s_waitcnt lgkmcnt(0)
	s_nop 1
	ds_read_b128 v[10:13], v204 offset:26304
	ds_read_b128 v[82:85], v204 offset:30656
	s_waitcnt lgkmcnt(1)
	v_mfma_f32_16x16x32_bf16 v[26:29], v[74:77], v[10:13], v[66:69]
	s_nop 2
	v_and_b32_e32 v67, 64, v213
	v_xor_b32_e32 v66, 16, v213
	v_pk_mul_f32 v[68:69], v[58:59], v[58:59]
	v_mfma_f32_16x16x32_bf16 v[10:13], v[78:81], v[10:13], v[70:73]
	v_fmac_f32_e32 v69, v58, v58
	s_nop 1
	v_add_u32_e32 v71, 64, v67
	v_cmp_lt_i32_e32 vcc, v66, v71
	s_waitcnt lgkmcnt(0)
	v_mfma_f32_16x16x32_bf16 v[2:5], v[74:77], v[82:85], v[2:5]
	v_cndmask_b32_e32 v66, v213, v66, vcc
	v_lshlrev_b32_e32 v70, 2, v66
	v_add_f32_e32 v66, 0, v58
	v_add_f32_e32 v66, v59, v66
	v_add_f32_e32 v72, v60, v66
	v_pk_mul_f32 v[66:67], v[60:61], v[60:61]
	v_mfma_f32_16x16x32_bf16 v[50:53], v[78:81], v[82:85], v[50:53]
	v_add_f32_e32 v68, v66, v69
	v_add_f32_e32 v66, v61, v72
	v_add_f32_e32 v69, v42, v66
	v_mov_b32_e32 v66, v42
	v_mov_b32_e32 v67, v61
	v_pk_mul_f32 v[66:67], v[66:67], v[66:67]
	v_pk_mul_f32 v[72:73], v[42:43], v[42:43]
	v_add_f32_e32 v67, v67, v68
	v_add_f32_e32 v67, v66, v67
	v_add_f32_e32 v66, v43, v69
	v_pk_mul_f32 v[68:69], v[44:45], v[44:45]
	v_add_f32_e32 v67, v73, v67
	v_add_f32_e32 v66, v44, v66
	v_add_f32_e32 v69, v68, v67
	v_mul_f32_e32 v67, v45, v45
	v_mov_b32_e32 v68, v45
	v_pk_add_f32 v[66:67], v[68:69], v[66:67]
	ds_bpermute_b32 v68, v70, v66
	ds_bpermute_b32 v69, v70, v67
	v_xor_b32_e32 v72, 32, v213
	v_cmp_lt_i32_e32 vcc, v72, v71
	s_waitcnt lgkmcnt(0)
	v_pk_add_f32 v[66:67], v[66:67], v[68:69]
	v_cndmask_b32_e32 v71, v213, v72, vcc
	v_lshlrev_b32_e32 v71, 2, v71
	ds_bpermute_b32 v68, v71, v66
	ds_bpermute_b32 v69, v71, v67
	s_and_saveexec_b64 s[0:1], s[74:75]
	s_cbranch_execz .LBB0_940
	v_readlane_b32 s94, v254, 20
	s_waitcnt lgkmcnt(0)
	v_pk_add_f32 v[66:67], v[66:67], v[68:69]
	v_add_u32_e32 v68, s94, v181
	ds_write_b64 v68, v[66:67]

.LBB0_982:
	v_lshl_or_b32 v2, s57, 8, v202
	v_add_u32_e32 v4, s56, v201
	v_ashrrev_i32_e32 v3, 31, v2
	v_mov_b64_e32 v[6:7], s[16:17]
	v_mad_i64_i32 v[10:11], s[2:3], v4, s47, v[6:7]
	v_lshlrev_b64 v[8:9], 1, v[2:3]
	v_mad_u32_u24 v213, v4, s47, v8
	global_load_dwordx4 v[214:217], v213, s[16:17] nt
	global_load_dwordx4 v[218:221], v213, s[16:17] offset:256 nt
	v_add_u32_e32 v213, 16, v4
	v_mad_u32_u24 v213, v213, s47, v8
	global_load_dwordx4 v[222:225], v213, s[16:17] nt
	global_load_dwordx4 v[226:229], v213, s[16:17] offset:256 nt
	v_add_u32_e32 v213, 32, v4
	v_mad_u32_u24 v213, v213, s47, v8
	global_load_dwordx4 v[230:233], v213, s[16:17] nt
	global_load_dwordx4 v[234:237], v213, s[16:17] offset:256 nt
	v_add_u32_e32 v213, 48, v4
	v_mad_u32_u24 v213, v213, s47, v8
	global_load_dwordx4 v[238:241], v213, s[16:17] nt
	global_load_dwordx4 v[242:245], v213, s[16:17] offset:256 nt
	v_add_u32_e32 v213, 128, v4
	v_mad_u32_u24 v213, v213, s47, v8
	global_load_dwordx4 v[246:249], v213, s[16:17] nt
	global_load_dwordx4 v[250:253], v213, s[16:17] offset:256 nt
	s_nop 15
	s_nop 15
	s_nop 15
	v_lshl_add_u64 v[10:11], v[10:11], 0, v[8:9]
	v_pk_mul_f32 v[20:21], v[156:157], s[24:25] op_sel_hi:[1,0]
	v_pk_mul_f32 v[18:19], v[158:159], s[24:25] op_sel_hi:[1,0]
	v_pk_mul_f32 v[16:17], v[160:161], s[24:25] op_sel_hi:[1,0]
	v_pk_mul_f32 v[22:23], v[154:155], s[24:25] op_sel_hi:[1,0]
	v_ashrrev_i32_e32 v5, 31, v4
	s_waitcnt vmcnt(9)
	v_mov_b64_e32 v[12:13], v[214:215]
	v_mov_b64_e32 v[14:15], v[216:217]
	v_add_u32_e32 v213, 144, v4
	v_mad_u32_u24 v213, v213, s47, v8
	global_load_dwordx4 v[214:217], v213, s[16:17] nt
	v_lshlrev_b32_e32 v24, 16, v12
	v_and_b32_e32 v12, 0xffff0000, v12
	v_mul_f32_e32 v24, 0xbfb8aa3b, v24
	v_lshlrev_b32_e32 v25, 16, v13
	v_mul_f32_e32 v12, 0xbfb8aa3b, v12
	v_exp_f32_e32 v24, v24
	v_mul_f32_e32 v25, 0xbfb8aa3b, v25
	v_exp_f32_e32 v12, v12
	v_and_b32_e32 v13, 0xffff0000, v13
	v_exp_f32_e32 v25, v25
	v_mul_f32_e32 v13, 0xbfb8aa3b, v13
	v_exp_f32_e32 v13, v13
	v_add_f32_e32 v24, 1.0, v24
	v_lshlrev_b32_e32 v26, 16, v14
	v_add_f32_e32 v12, 1.0, v12
	v_mul_f32_e32 v26, 0xbfb8aa3b, v26
	v_add_f32_e32 v25, 1.0, v25
	v_exp_f32_e32 v26, v26
	v_add_f32_e32 v13, 1.0, v13
	v_add_f32_e32 v26, 1.0, v26
	v_and_b32_e32 v14, 0xffff0000, v14
	v_mul_f32_e32 v14, 0xbfb8aa3b, v14
	v_exp_f32_e32 v14, v14
	v_rcp_f32_e32 v24, v24
	s_nop 0
	v_mul_f32_e32 v18, v18, v24
	v_rcp_f32_e32 v12, v12
	s_nop 0
	v_mul_f32_e32 v12, v19, v12
	v_rcp_f32_e32 v19, v25
	v_add_f32_e32 v14, 1.0, v14
	v_mul_f32_e32 v16, v16, v19
	v_rcp_f32_e32 v13, v13
	s_nop 0
	v_mul_f32_e32 v13, v17, v13
	v_rcp_f32_e32 v17, v26
	v_lshlrev_b32_e32 v26, 16, v15
	v_mul_f32_e32 v17, v22, v17
	v_mul_f32_e32 v26, 0xbfb8aa3b, v26
	v_exp_f32_e32 v26, v26
	s_nop 0
	v_add_f32_e32 v22, 1.0, v26
	v_and_b32_e32 v15, 0xffff0000, v15
	v_mul_f32_e32 v15, 0xbfb8aa3b, v15
	v_rcp_f32_e32 v14, v14
	v_exp_f32_e32 v15, v15
	v_mul_f32_e32 v19, v23, v14
	v_add_f32_e32 v15, 1.0, v15
	v_rcp_f32_e32 v14, v22
	s_nop 0
	v_mul_f32_e32 v20, v20, v14
	v_rcp_f32_e32 v14, v15
	s_nop 0
	v_mul_f32_e32 v21, v21, v14
	v_mul_f32_e32 v14, 0x41800000, v18
	v_mul_f32_e32 v12, 0x41800000, v12
	v_mul_f32_e32 v15, 0x41800000, v16
	v_med3_f32 v16, v14, s53, v205
	v_med3_f32 v12, v12, s53, v205
	v_mov_b32_e32 v14, v167
	v_cvt_pk_fp8_f32 v14, v16, v12
	v_mul_f32_e32 v12, 0x41800000, v13
	v_med3_f32 v13, v15, s53, v205
	v_med3_f32 v12, v12, s53, v205
	v_cvt_pk_fp8_f32 v14, v13, v12 op_sel:[0,0,1]
	v_mul_f32_e32 v12, 0x41800000, v17
	v_mul_f32_e32 v13, 0x41800000, v19
	v_med3_f32 v12, v12, s53, v205
	v_med3_f32 v13, v13, s53, v205
	v_mov_b32_e32 v15, v167
	v_cvt_pk_fp8_f32 v15, v12, v13
	v_mul_f32_e32 v16, 0x41800000, v20
	v_mul_f32_e32 v12, 0x41800000, v21
	v_med3_f32 v13, v16, s53, v205
	v_med3_f32 v12, v12, s53, v205
	v_cvt_pk_fp8_f32 v15, v13, v12 op_sel:[0,0,1]
	v_lshlrev_b64 v[12:13], 11, v[4:5]
	v_lshl_add_u64 v[12:13], s[14:15], 0, v[12:13]
	v_lshl_add_u64 v[12:13], v[12:13], 0, v[2:3]
	global_store_dwordx2 v[12:13], v[14:15], off
	v_pk_mul_f32 v[18:19], v[150:151], s[24:25] op_sel_hi:[1,0]
	v_pk_mul_f32 v[10:11], v[152:153], s[24:25] op_sel_hi:[1,0]
	v_pk_mul_f32 v[22:23], v[146:147], s[24:25] op_sel_hi:[1,0]
	v_pk_mul_f32 v[20:21], v[148:149], s[24:25] op_sel_hi:[1,0]
	s_waitcnt vmcnt(9)
	v_mov_b64_e32 v[14:15], v[218:219]
	v_mov_b64_e32 v[16:17], v[220:221]
	v_add_u32_e32 v213, 144, v4
	v_mad_u32_u24 v213, v213, s47, v8
	global_load_dwordx4 v[218:221], v213, s[16:17] offset:256 nt
	v_lshlrev_b32_e32 v5, 16, v14
	v_mul_f32_e32 v5, 0xbfb8aa3b, v5
	v_exp_f32_e32 v5, v5
	v_and_b32_e32 v14, 0xffff0000, v14
	v_mul_f32_e32 v14, 0xbfb8aa3b, v14
	v_exp_f32_e32 v14, v14
	v_add_f32_e32 v5, 1.0, v5
	v_add_f32_e32 v14, 1.0, v14
	v_lshlrev_b32_e32 v25, 16, v15
	v_rcp_f32_e32 v5, v5
	v_mul_f32_e32 v25, 0xbfb8aa3b, v25
	v_mul_f32_e32 v5, v18, v5
	v_exp_f32_e32 v25, v25
	s_nop 0
	v_add_f32_e32 v25, 1.0, v25
	v_and_b32_e32 v15, 0xffff0000, v15
	v_mul_f32_e32 v15, 0xbfb8aa3b, v15
	v_exp_f32_e32 v15, v15
	v_rcp_f32_e32 v14, v14
	s_nop 0
	v_mul_f32_e32 v14, v19, v14
	v_add_f32_e32 v15, 1.0, v15
	v_rcp_f32_e32 v18, v25
	v_lshlrev_b32_e32 v25, 16, v16
	v_mul_f32_e32 v10, v10, v18
	v_mul_f32_e32 v25, 0xbfb8aa3b, v25
	v_exp_f32_e32 v25, v25
	s_nop 0
	v_add_f32_e32 v24, 1.0, v25
	v_and_b32_e32 v16, 0xffff0000, v16
	v_mul_f32_e32 v16, 0xbfb8aa3b, v16
	v_rcp_f32_e32 v15, v15
	v_exp_f32_e32 v16, v16
	v_mul_f32_e32 v11, v11, v15
	v_add_f32_e32 v16, 1.0, v16
	v_rcp_f32_e32 v15, v24
	v_lshlrev_b32_e32 v24, 16, v17
	v_mul_f32_e32 v24, 0xbfb8aa3b, v24
	v_exp_f32_e32 v24, v24
	v_mul_f32_e32 v15, v22, v15
	v_add_f32_e32 v19, 1.0, v24
	v_and_b32_e32 v17, 0xffff0000, v17
	v_mul_f32_e32 v17, 0xbfb8aa3b, v17
	v_exp_f32_e32 v17, v17
	v_rcp_f32_e32 v16, v16
	s_nop 0
	v_mul_f32_e32 v16, v23, v16
	v_add_f32_e32 v17, 1.0, v17
	v_rcp_f32_e32 v18, v19
	s_nop 0
	v_mul_f32_e32 v18, v20, v18
	v_mul_f32_e32 v5, 0x41800000, v5
	v_mul_f32_e32 v14, 0x41800000, v14
	v_rcp_f32_e32 v17, v17
	v_mul_f32_e32 v19, 0x41800000, v10
	v_med3_f32 v5, v5, s53, v205
	v_med3_f32 v14, v14, s53, v205
	v_mov_b32_e32 v10, v167
	v_cvt_pk_fp8_f32 v10, v5, v14
	v_mul_f32_e32 v5, 0x41800000, v11
	v_med3_f32 v11, v19, s53, v205
	v_med3_f32 v5, v5, s53, v205
	v_cvt_pk_fp8_f32 v10, v11, v5 op_sel:[0,0,1]
	v_mul_f32_e32 v5, 0x41800000, v15
	v_mul_f32_e32 v11, 0x41800000, v16
	v_med3_f32 v5, v5, s53, v205
	v_med3_f32 v15, v11, s53, v205
	v_mov_b32_e32 v11, v167
	v_cvt_pk_fp8_f32 v11, v5, v15
	v_mul_f32_e32 v17, v21, v17
	v_mul_f32_e32 v14, 0x41800000, v18
	v_mul_f32_e32 v5, 0x41800000, v17
	v_med3_f32 v14, v14, s53, v205
	v_med3_f32 v5, v5, s53, v205
	v_cvt_pk_fp8_f32 v11, v14, v5 op_sel:[0,0,1]
	v_add_u32_e32 v16, 16, v4
	v_pk_mul_f32 v[20:21], v[142:143], s[24:25] op_sel_hi:[1,0]
	v_pk_mul_f32 v[18:19], v[144:145], s[24:25] op_sel_hi:[1,0]
	global_store_dwordx2 v[12:13], v[10:11], off offset:128
	v_mad_i64_i32 v[10:11], s[2:3], v16, s47, v[6:7]
	v_lshl_add_u64 v[10:11], v[10:11], 0, v[8:9]
	v_pk_mul_f32 v[24:25], v[138:139], s[24:25] op_sel_hi:[1,0]
	v_pk_mul_f32 v[22:23], v[140:141], s[24:25] op_sel_hi:[1,0]
	v_ashrrev_i32_e32 v17, 31, v16
	s_waitcnt vmcnt(9)
	v_mov_b64_e32 v[12:13], v[222:223]
	v_mov_b64_e32 v[14:15], v[224:225]
	v_add_u32_e32 v213, 160, v4
	v_mad_u32_u24 v213, v213, s47, v8
	global_load_dwordx4 v[222:225], v213, s[16:17] nt
	v_lshlrev_b32_e32 v5, 16, v12
	v_mul_f32_e32 v5, 0xbfb8aa3b, v5
	v_exp_f32_e32 v5, v5
	v_and_b32_e32 v12, 0xffff0000, v12
	v_mul_f32_e32 v12, 0xbfb8aa3b, v12
	v_exp_f32_e32 v12, v12
	v_add_f32_e32 v5, 1.0, v5
	v_add_f32_e32 v12, 1.0, v12
	v_lshlrev_b32_e32 v27, 16, v13
	v_rcp_f32_e32 v5, v5
	v_mul_f32_e32 v27, 0xbfb8aa3b, v27
	v_mul_f32_e32 v5, v20, v5
	v_exp_f32_e32 v27, v27
	s_nop 0
	v_add_f32_e32 v27, 1.0, v27
	v_and_b32_e32 v13, 0xffff0000, v13
	v_mul_f32_e32 v13, 0xbfb8aa3b, v13
	v_exp_f32_e32 v13, v13
	v_rcp_f32_e32 v12, v12
	s_nop 0
	v_mul_f32_e32 v12, v21, v12
	v_add_f32_e32 v13, 1.0, v13
	v_rcp_f32_e32 v20, v27
	v_lshlrev_b32_e32 v27, 16, v14
	v_mul_f32_e32 v18, v18, v20
	v_mul_f32_e32 v27, 0xbfb8aa3b, v27
	v_exp_f32_e32 v27, v27
	s_nop 0
	v_add_f32_e32 v26, 1.0, v27
	v_and_b32_e32 v14, 0xffff0000, v14
	v_mul_f32_e32 v14, 0xbfb8aa3b, v14
	v_rcp_f32_e32 v13, v13
	v_exp_f32_e32 v14, v14
	v_mul_f32_e32 v13, v19, v13
	v_add_f32_e32 v14, 1.0, v14
	v_rcp_f32_e32 v19, v26
	v_lshlrev_b32_e32 v26, 16, v15
	v_mul_f32_e32 v26, 0xbfb8aa3b, v26
	v_exp_f32_e32 v26, v26
	v_mul_f32_e32 v19, v24, v19
	v_add_f32_e32 v21, 1.0, v26
	v_and_b32_e32 v15, 0xffff0000, v15
	v_mul_f32_e32 v15, 0xbfb8aa3b, v15
	v_exp_f32_e32 v15, v15
	v_rcp_f32_e32 v14, v14
	s_nop 0
	v_mul_f32_e32 v14, v25, v14
	v_add_f32_e32 v15, 1.0, v15
	v_rcp_f32_e32 v20, v21
	s_nop 0
	v_mul_f32_e32 v20, v22, v20
	v_mul_f32_e32 v5, 0x41800000, v5
	v_mul_f32_e32 v12, 0x41800000, v12
	v_rcp_f32_e32 v15, v15
	v_med3_f32 v5, v5, s53, v205
	v_med3_f32 v21, v12, s53, v205
	v_mov_b32_e32 v12, v167
	v_cvt_pk_fp8_f32 v12, v5, v21
	v_mul_f32_e32 v18, 0x41800000, v18
	v_mul_f32_e32 v5, 0x41800000, v13
	v_med3_f32 v13, v18, s53, v205
	v_med3_f32 v5, v5, s53, v205
	v_cvt_pk_fp8_f32 v12, v13, v5 op_sel:[0,0,1]
	v_mul_f32_e32 v5, 0x41800000, v19
	v_mul_f32_e32 v13, 0x41800000, v14
	v_med3_f32 v5, v5, s53, v205
	v_med3_f32 v18, v13, s53, v205
	v_mov_b32_e32 v13, v167
	v_cvt_pk_fp8_f32 v13, v5, v18
	v_mul_f32_e32 v15, v23, v15
	v_mul_f32_e32 v14, 0x41800000, v20
	v_mul_f32_e32 v5, 0x41800000, v15
	v_med3_f32 v14, v14, s53, v205
	v_med3_f32 v5, v5, s53, v205
	v_cvt_pk_fp8_f32 v13, v14, v5 op_sel:[0,0,1]
	v_lshlrev_b64 v[14:15], 11, v[16:17]
	v_lshl_add_u64 v[14:15], s[14:15], 0, v[14:15]
	v_lshl_add_u64 v[14:15], v[14:15], 0, v[2:3]
	global_store_dwordx2 v[14:15], v[12:13], off
	v_pk_mul_f32 v[18:19], v[134:135], s[24:25] op_sel_hi:[1,0]
	v_pk_mul_f32 v[16:17], v[136:137], s[24:25] op_sel_hi:[1,0]
	v_pk_mul_f32 v[22:23], v[130:131], s[24:25] op_sel_hi:[1,0]
	v_pk_mul_f32 v[20:21], v[132:133], s[24:25] op_sel_hi:[1,0]
	s_waitcnt vmcnt(9)
	v_mov_b64_e32 v[10:11], v[226:227]
	v_mov_b64_e32 v[12:13], v[228:229]
	v_add_u32_e32 v213, 160, v4
	v_mad_u32_u24 v213, v213, s47, v8
	global_load_dwordx4 v[226:229], v213, s[16:17] offset:256 nt
	v_lshlrev_b32_e32 v5, 16, v10
	v_mul_f32_e32 v5, 0xbfb8aa3b, v5
	v_exp_f32_e32 v5, v5
	v_and_b32_e32 v10, 0xffff0000, v10
	v_mul_f32_e32 v10, 0xbfb8aa3b, v10
	v_exp_f32_e32 v10, v10
	v_add_f32_e32 v5, 1.0, v5
	v_add_f32_e32 v10, 1.0, v10
	v_lshlrev_b32_e32 v25, 16, v11
	v_rcp_f32_e32 v5, v5
	v_mul_f32_e32 v25, 0xbfb8aa3b, v25
	v_mul_f32_e32 v5, v18, v5
	v_exp_f32_e32 v25, v25
	s_nop 0
	v_add_f32_e32 v25, 1.0, v25
	v_and_b32_e32 v11, 0xffff0000, v11
	v_mul_f32_e32 v11, 0xbfb8aa3b, v11
	v_exp_f32_e32 v11, v11
	v_rcp_f32_e32 v10, v10
	s_nop 0
	v_mul_f32_e32 v10, v19, v10
	v_add_f32_e32 v11, 1.0, v11
	v_rcp_f32_e32 v18, v25
	v_lshlrev_b32_e32 v25, 16, v12
	v_mul_f32_e32 v16, v16, v18
	v_mul_f32_e32 v25, 0xbfb8aa3b, v25
	v_exp_f32_e32 v25, v25
	s_nop 0
	v_add_f32_e32 v24, 1.0, v25
	v_and_b32_e32 v12, 0xffff0000, v12
	v_mul_f32_e32 v12, 0xbfb8aa3b, v12
	v_rcp_f32_e32 v11, v11
	v_exp_f32_e32 v12, v12
	v_mul_f32_e32 v11, v17, v11
	v_add_f32_e32 v12, 1.0, v12
	v_rcp_f32_e32 v17, v24
	v_lshlrev_b32_e32 v24, 16, v13
	v_mul_f32_e32 v24, 0xbfb8aa3b, v24
	v_exp_f32_e32 v24, v24
	v_mul_f32_e32 v17, v22, v17
	v_add_f32_e32 v19, 1.0, v24
	v_and_b32_e32 v13, 0xffff0000, v13
	v_mul_f32_e32 v13, 0xbfb8aa3b, v13
	v_exp_f32_e32 v13, v13
	v_rcp_f32_e32 v12, v12
	s_nop 0
	v_mul_f32_e32 v12, v23, v12
	v_add_f32_e32 v13, 1.0, v13
	v_rcp_f32_e32 v18, v19
	s_nop 0
	v_mul_f32_e32 v18, v20, v18
	v_mul_f32_e32 v5, 0x41800000, v5
	v_mul_f32_e32 v10, 0x41800000, v10
	v_rcp_f32_e32 v13, v13
	v_med3_f32 v5, v5, s53, v205
	v_med3_f32 v19, v10, s53, v205
	v_mov_b32_e32 v10, v167
	v_cvt_pk_fp8_f32 v10, v5, v19
	v_mul_f32_e32 v16, 0x41800000, v16
	v_mul_f32_e32 v5, 0x41800000, v11
	v_med3_f32 v11, v16, s53, v205
	v_med3_f32 v5, v5, s53, v205
	v_cvt_pk_fp8_f32 v10, v11, v5 op_sel:[0,0,1]
	v_mul_f32_e32 v5, 0x41800000, v17
	v_mul_f32_e32 v11, 0x41800000, v12
	v_med3_f32 v5, v5, s53, v205
	v_med3_f32 v16, v11, s53, v205
	v_mov_b32_e32 v11, v167
	v_cvt_pk_fp8_f32 v11, v5, v16
	v_mul_f32_e32 v13, v21, v13
	v_mul_f32_e32 v12, 0x41800000, v18
	v_mul_f32_e32 v5, 0x41800000, v13
	v_med3_f32 v12, v12, s53, v205
	v_med3_f32 v5, v5, s53, v205
	v_cvt_pk_fp8_f32 v11, v12, v5 op_sel:[0,0,1]
	v_add_u32_e32 v16, 32, v4
	v_pk_mul_f32 v[20:21], v[126:127], s[24:25] op_sel_hi:[1,0]
	v_pk_mul_f32 v[18:19], v[128:129], s[24:25] op_sel_hi:[1,0]
	global_store_dwordx2 v[14:15], v[10:11], off offset:128
	v_mad_i64_i32 v[10:11], s[2:3], v16, s47, v[6:7]
	v_lshl_add_u64 v[10:11], v[10:11], 0, v[8:9]
	v_pk_mul_f32 v[24:25], v[122:123], s[24:25] op_sel_hi:[1,0]
	v_pk_mul_f32 v[22:23], v[124:125], s[24:25] op_sel_hi:[1,0]
	v_ashrrev_i32_e32 v17, 31, v16
	s_waitcnt vmcnt(9)
	v_mov_b64_e32 v[12:13], v[230:231]
	v_mov_b64_e32 v[14:15], v[232:233]
	v_add_u32_e32 v213, 176, v4
	v_mad_u32_u24 v213, v213, s47, v8
	global_load_dwordx4 v[230:233], v213, s[16:17] nt
	v_lshlrev_b32_e32 v5, 16, v12
	v_mul_f32_e32 v5, 0xbfb8aa3b, v5
	v_exp_f32_e32 v5, v5
	v_and_b32_e32 v12, 0xffff0000, v12
	v_mul_f32_e32 v12, 0xbfb8aa3b, v12
	v_exp_f32_e32 v12, v12
	v_add_f32_e32 v5, 1.0, v5
	v_add_f32_e32 v12, 1.0, v12
	v_lshlrev_b32_e32 v27, 16, v13
	v_rcp_f32_e32 v5, v5
	v_mul_f32_e32 v27, 0xbfb8aa3b, v27
	v_mul_f32_e32 v5, v20, v5
	v_exp_f32_e32 v27, v27
	s_nop 0
	v_add_f32_e32 v27, 1.0, v27
	v_and_b32_e32 v13, 0xffff0000, v13
	v_mul_f32_e32 v13, 0xbfb8aa3b, v13
	v_exp_f32_e32 v13, v13
	v_rcp_f32_e32 v12, v12
	s_nop 0
	v_mul_f32_e32 v12, v21, v12
	v_add_f32_e32 v13, 1.0, v13
	v_rcp_f32_e32 v20, v27
	v_lshlrev_b32_e32 v27, 16, v14
	v_mul_f32_e32 v18, v18, v20
	v_mul_f32_e32 v27, 0xbfb8aa3b, v27
	v_exp_f32_e32 v27, v27
	s_nop 0
	v_add_f32_e32 v26, 1.0, v27
	v_and_b32_e32 v14, 0xffff0000, v14
	v_mul_f32_e32 v14, 0xbfb8aa3b, v14
	v_rcp_f32_e32 v13, v13
	v_exp_f32_e32 v14, v14
	v_mul_f32_e32 v13, v19, v13
	v_add_f32_e32 v14, 1.0, v14
	v_rcp_f32_e32 v19, v26
	v_lshlrev_b32_e32 v26, 16, v15
	v_mul_f32_e32 v26, 0xbfb8aa3b, v26
	v_exp_f32_e32 v26, v26
	v_mul_f32_e32 v19, v24, v19
	v_add_f32_e32 v21, 1.0, v26
	v_and_b32_e32 v15, 0xffff0000, v15
	v_mul_f32_e32 v15, 0xbfb8aa3b, v15
	v_exp_f32_e32 v15, v15
	v_rcp_f32_e32 v14, v14
	s_nop 0
	v_mul_f32_e32 v14, v25, v14
	v_add_f32_e32 v15, 1.0, v15
	v_rcp_f32_e32 v20, v21
	s_nop 0
	v_mul_f32_e32 v20, v22, v20
	v_mul_f32_e32 v5, 0x41800000, v5
	v_mul_f32_e32 v12, 0x41800000, v12
	v_rcp_f32_e32 v15, v15
	v_med3_f32 v5, v5, s53, v205
	v_med3_f32 v21, v12, s53, v205
	v_mov_b32_e32 v12, v167
	v_cvt_pk_fp8_f32 v12, v5, v21
	v_mul_f32_e32 v18, 0x41800000, v18
	v_mul_f32_e32 v5, 0x41800000, v13
	v_med3_f32 v13, v18, s53, v205
	v_med3_f32 v5, v5, s53, v205
	v_cvt_pk_fp8_f32 v12, v13, v5 op_sel:[0,0,1]
	v_mul_f32_e32 v5, 0x41800000, v19
	v_mul_f32_e32 v13, 0x41800000, v14
	v_med3_f32 v5, v5, s53, v205
	v_med3_f32 v18, v13, s53, v205
	v_mov_b32_e32 v13, v167
	v_cvt_pk_fp8_f32 v13, v5, v18
	v_mul_f32_e32 v15, v23, v15
	v_mul_f32_e32 v14, 0x41800000, v20
	v_mul_f32_e32 v5, 0x41800000, v15
	v_med3_f32 v14, v14, s53, v205
	v_med3_f32 v5, v5, s53, v205
	v_cvt_pk_fp8_f32 v13, v14, v5 op_sel:[0,0,1]
	v_lshlrev_b64 v[14:15], 11, v[16:17]
	v_lshl_add_u64 v[14:15], s[14:15], 0, v[14:15]
	v_lshl_add_u64 v[14:15], v[14:15], 0, v[2:3]
	global_store_dwordx2 v[14:15], v[12:13], off
	v_pk_mul_f32 v[18:19], v[118:119], s[24:25] op_sel_hi:[1,0]
	v_pk_mul_f32 v[16:17], v[120:121], s[24:25] op_sel_hi:[1,0]
	v_pk_mul_f32 v[22:23], v[114:115], s[24:25] op_sel_hi:[1,0]
	v_pk_mul_f32 v[20:21], v[116:117], s[24:25] op_sel_hi:[1,0]
	s_waitcnt vmcnt(9)
	v_mov_b64_e32 v[10:11], v[234:235]
	v_mov_b64_e32 v[12:13], v[236:237]
	v_add_u32_e32 v213, 176, v4
	v_mad_u32_u24 v213, v213, s47, v8
	global_load_dwordx4 v[234:237], v213, s[16:17] offset:256 nt
	v_lshlrev_b32_e32 v5, 16, v10
	v_mul_f32_e32 v5, 0xbfb8aa3b, v5
	v_exp_f32_e32 v5, v5
	v_and_b32_e32 v10, 0xffff0000, v10
	v_mul_f32_e32 v10, 0xbfb8aa3b, v10
	v_exp_f32_e32 v10, v10
	v_add_f32_e32 v5, 1.0, v5
	v_add_f32_e32 v10, 1.0, v10
	v_lshlrev_b32_e32 v25, 16, v11
	v_rcp_f32_e32 v5, v5
	v_mul_f32_e32 v25, 0xbfb8aa3b, v25
	v_mul_f32_e32 v5, v18, v5
	v_exp_f32_e32 v25, v25
	s_nop 0
	v_add_f32_e32 v25, 1.0, v25
	v_and_b32_e32 v11, 0xffff0000, v11
	v_mul_f32_e32 v11, 0xbfb8aa3b, v11
	v_exp_f32_e32 v11, v11
	v_rcp_f32_e32 v10, v10
	s_nop 0
	v_mul_f32_e32 v10, v19, v10
	v_add_f32_e32 v11, 1.0, v11
	v_rcp_f32_e32 v18, v25
	v_lshlrev_b32_e32 v25, 16, v12
	v_mul_f32_e32 v16, v16, v18
	v_mul_f32_e32 v25, 0xbfb8aa3b, v25
	v_exp_f32_e32 v25, v25
	s_nop 0
	v_add_f32_e32 v24, 1.0, v25
	v_and_b32_e32 v12, 0xffff0000, v12
	v_mul_f32_e32 v12, 0xbfb8aa3b, v12
	v_rcp_f32_e32 v11, v11
	v_exp_f32_e32 v12, v12
	v_mul_f32_e32 v11, v17, v11
	v_add_f32_e32 v12, 1.0, v12
	v_rcp_f32_e32 v17, v24
	v_lshlrev_b32_e32 v24, 16, v13
	v_mul_f32_e32 v24, 0xbfb8aa3b, v24
	v_exp_f32_e32 v24, v24
	v_mul_f32_e32 v17, v22, v17
	v_add_f32_e32 v19, 1.0, v24
	v_and_b32_e32 v13, 0xffff0000, v13
	v_mul_f32_e32 v13, 0xbfb8aa3b, v13
	v_exp_f32_e32 v13, v13
	v_rcp_f32_e32 v12, v12
	s_nop 0
	v_mul_f32_e32 v12, v23, v12
	v_add_f32_e32 v13, 1.0, v13
	v_rcp_f32_e32 v18, v19
	s_nop 0
	v_mul_f32_e32 v18, v20, v18
	v_mul_f32_e32 v5, 0x41800000, v5
	v_mul_f32_e32 v10, 0x41800000, v10
	v_rcp_f32_e32 v13, v13
	v_med3_f32 v5, v5, s53, v205
	v_med3_f32 v19, v10, s53, v205
	v_mov_b32_e32 v10, v167
	v_cvt_pk_fp8_f32 v10, v5, v19
	v_mul_f32_e32 v16, 0x41800000, v16
	v_mul_f32_e32 v5, 0x41800000, v11
	v_med3_f32 v11, v16, s53, v205
	v_med3_f32 v5, v5, s53, v205
	v_cvt_pk_fp8_f32 v10, v11, v5 op_sel:[0,0,1]
	v_mul_f32_e32 v5, 0x41800000, v17
	v_mul_f32_e32 v11, 0x41800000, v12
	v_med3_f32 v5, v5, s53, v205
	v_med3_f32 v16, v11, s53, v205
	v_mov_b32_e32 v11, v167
	v_cvt_pk_fp8_f32 v11, v5, v16
	v_mul_f32_e32 v13, v21, v13
	v_mul_f32_e32 v12, 0x41800000, v18
	v_mul_f32_e32 v5, 0x41800000, v13
	v_med3_f32 v12, v12, s53, v205
	v_med3_f32 v5, v5, s53, v205
	v_cvt_pk_fp8_f32 v11, v12, v5 op_sel:[0,0,1]
	v_add_u32_e32 v16, 48, v4
	v_pk_mul_f32 v[20:21], v[110:111], s[24:25] op_sel_hi:[1,0]
	v_pk_mul_f32 v[18:19], v[112:113], s[24:25] op_sel_hi:[1,0]
	global_store_dwordx2 v[14:15], v[10:11], off offset:128
	v_mad_i64_i32 v[10:11], s[2:3], v16, s47, v[6:7]
	v_lshl_add_u64 v[10:11], v[10:11], 0, v[8:9]
	v_pk_mul_f32 v[24:25], v[106:107], s[24:25] op_sel_hi:[1,0]
	v_pk_mul_f32 v[22:23], v[108:109], s[24:25] op_sel_hi:[1,0]
	v_ashrrev_i32_e32 v17, 31, v16
	s_waitcnt vmcnt(9)
	v_mov_b64_e32 v[12:13], v[238:239]
	v_mov_b64_e32 v[14:15], v[240:241]
	v_lshlrev_b32_e32 v5, 16, v12
	v_mul_f32_e32 v5, 0xbfb8aa3b, v5
	v_exp_f32_e32 v5, v5
	v_and_b32_e32 v12, 0xffff0000, v12
	v_mul_f32_e32 v12, 0xbfb8aa3b, v12
	v_exp_f32_e32 v12, v12
	v_add_f32_e32 v5, 1.0, v5
	v_add_f32_e32 v12, 1.0, v12
	v_lshlrev_b32_e32 v27, 16, v13
	v_rcp_f32_e32 v5, v5
	v_mul_f32_e32 v27, 0xbfb8aa3b, v27
	v_mul_f32_e32 v5, v20, v5
	v_exp_f32_e32 v27, v27
	s_nop 0
	v_add_f32_e32 v27, 1.0, v27
	v_and_b32_e32 v13, 0xffff0000, v13
	v_mul_f32_e32 v13, 0xbfb8aa3b, v13
	v_exp_f32_e32 v13, v13
	v_rcp_f32_e32 v12, v12
	s_nop 0
	v_mul_f32_e32 v12, v21, v12
	v_add_f32_e32 v13, 1.0, v13
	v_rcp_f32_e32 v20, v27
	v_lshlrev_b32_e32 v27, 16, v14
	v_mul_f32_e32 v18, v18, v20
	v_mul_f32_e32 v27, 0xbfb8aa3b, v27
	v_exp_f32_e32 v27, v27
	s_nop 0
	v_add_f32_e32 v26, 1.0, v27
	v_and_b32_e32 v14, 0xffff0000, v14
	v_mul_f32_e32 v14, 0xbfb8aa3b, v14
	v_rcp_f32_e32 v13, v13
	v_exp_f32_e32 v14, v14
	v_mul_f32_e32 v13, v19, v13
	v_add_f32_e32 v14, 1.0, v14
	v_rcp_f32_e32 v19, v26
	v_lshlrev_b32_e32 v26, 16, v15
	v_mul_f32_e32 v26, 0xbfb8aa3b, v26
	v_exp_f32_e32 v26, v26
	v_mul_f32_e32 v19, v24, v19
	v_add_f32_e32 v21, 1.0, v26
	v_and_b32_e32 v15, 0xffff0000, v15
	v_mul_f32_e32 v15, 0xbfb8aa3b, v15
	v_exp_f32_e32 v15, v15
	v_rcp_f32_e32 v14, v14
	s_nop 0
	v_mul_f32_e32 v14, v25, v14
	v_add_f32_e32 v15, 1.0, v15
	v_rcp_f32_e32 v20, v21
	s_nop 0
	v_mul_f32_e32 v20, v22, v20
	v_mul_f32_e32 v5, 0x41800000, v5
	v_mul_f32_e32 v12, 0x41800000, v12
	v_rcp_f32_e32 v15, v15
	v_med3_f32 v5, v5, s53, v205
	v_med3_f32 v21, v12, s53, v205
	v_mov_b32_e32 v12, v167
	v_cvt_pk_fp8_f32 v12, v5, v21
	v_mul_f32_e32 v18, 0x41800000, v18
	v_mul_f32_e32 v5, 0x41800000, v13
	v_med3_f32 v13, v18, s53, v205
	v_med3_f32 v5, v5, s53, v205
	v_cvt_pk_fp8_f32 v12, v13, v5 op_sel:[0,0,1]
	v_mul_f32_e32 v5, 0x41800000, v19
	v_mul_f32_e32 v13, 0x41800000, v14
	v_med3_f32 v5, v5, s53, v205
	v_med3_f32 v18, v13, s53, v205
	v_mov_b32_e32 v13, v167
	v_cvt_pk_fp8_f32 v13, v5, v18
	v_mul_f32_e32 v15, v23, v15
	v_mul_f32_e32 v14, 0x41800000, v20
	v_mul_f32_e32 v5, 0x41800000, v15
	v_med3_f32 v14, v14, s53, v205
	v_med3_f32 v5, v5, s53, v205
	v_cvt_pk_fp8_f32 v13, v14, v5 op_sel:[0,0,1]
	v_lshlrev_b64 v[14:15], 11, v[16:17]
	v_lshl_add_u64 v[14:15], s[14:15], 0, v[14:15]
	v_lshl_add_u64 v[14:15], v[14:15], 0, v[2:3]
	global_store_dwordx2 v[14:15], v[12:13], off
	v_pk_mul_f32 v[18:19], v[102:103], s[24:25] op_sel_hi:[1,0]
	v_pk_mul_f32 v[16:17], v[104:105], s[24:25] op_sel_hi:[1,0]
	v_pk_mul_f32 v[22:23], v[98:99], s[24:25] op_sel_hi:[1,0]
	v_pk_mul_f32 v[20:21], v[100:101], s[24:25] op_sel_hi:[1,0]
	s_waitcnt vmcnt(8)
	v_mov_b64_e32 v[10:11], v[242:243]
	v_mov_b64_e32 v[12:13], v[244:245]
	v_lshlrev_b32_e32 v5, 16, v10
	v_mul_f32_e32 v5, 0xbfb8aa3b, v5
	v_exp_f32_e32 v5, v5
	v_and_b32_e32 v10, 0xffff0000, v10
	v_mul_f32_e32 v10, 0xbfb8aa3b, v10
	v_exp_f32_e32 v10, v10
	v_add_f32_e32 v5, 1.0, v5
	v_add_f32_e32 v10, 1.0, v10
	v_lshlrev_b32_e32 v25, 16, v11
	v_rcp_f32_e32 v5, v5
	v_mul_f32_e32 v25, 0xbfb8aa3b, v25
	v_mul_f32_e32 v5, v18, v5
	v_exp_f32_e32 v25, v25
	s_nop 0
	v_add_f32_e32 v25, 1.0, v25
	v_and_b32_e32 v11, 0xffff0000, v11
	v_mul_f32_e32 v11, 0xbfb8aa3b, v11
	v_exp_f32_e32 v11, v11
	v_rcp_f32_e32 v10, v10
	s_nop 0
	v_mul_f32_e32 v10, v19, v10
	v_add_f32_e32 v11, 1.0, v11
	v_rcp_f32_e32 v18, v25
	v_lshlrev_b32_e32 v25, 16, v12
	v_mul_f32_e32 v16, v16, v18
	v_mul_f32_e32 v25, 0xbfb8aa3b, v25
	v_exp_f32_e32 v25, v25
	s_nop 0
	v_add_f32_e32 v24, 1.0, v25
	v_and_b32_e32 v12, 0xffff0000, v12
	v_mul_f32_e32 v12, 0xbfb8aa3b, v12
	v_rcp_f32_e32 v11, v11
	v_exp_f32_e32 v12, v12
	v_mul_f32_e32 v11, v17, v11
	v_add_f32_e32 v12, 1.0, v12
	v_rcp_f32_e32 v17, v24
	v_lshlrev_b32_e32 v24, 16, v13
	v_mul_f32_e32 v24, 0xbfb8aa3b, v24
	v_exp_f32_e32 v24, v24
	v_mul_f32_e32 v17, v22, v17
	v_add_f32_e32 v19, 1.0, v24
	v_and_b32_e32 v13, 0xffff0000, v13
	v_mul_f32_e32 v13, 0xbfb8aa3b, v13
	v_exp_f32_e32 v13, v13
	v_rcp_f32_e32 v12, v12
	s_nop 0
	v_mul_f32_e32 v12, v23, v12
	v_add_f32_e32 v13, 1.0, v13
	v_rcp_f32_e32 v18, v19
	s_nop 0
	v_mul_f32_e32 v18, v20, v18
	v_mul_f32_e32 v5, 0x41800000, v5
	v_mul_f32_e32 v10, 0x41800000, v10
	v_rcp_f32_e32 v13, v13
	v_med3_f32 v5, v5, s53, v205
	v_med3_f32 v19, v10, s53, v205
	v_mov_b32_e32 v10, v167
	v_cvt_pk_fp8_f32 v10, v5, v19
	v_mul_f32_e32 v16, 0x41800000, v16
	v_mul_f32_e32 v5, 0x41800000, v11
	v_med3_f32 v11, v16, s53, v205
	v_med3_f32 v5, v5, s53, v205
	v_cvt_pk_fp8_f32 v10, v11, v5 op_sel:[0,0,1]
	v_mul_f32_e32 v5, 0x41800000, v17
	v_mul_f32_e32 v11, 0x41800000, v12
	v_med3_f32 v5, v5, s53, v205
	v_med3_f32 v16, v11, s53, v205
	v_mov_b32_e32 v11, v167
	v_cvt_pk_fp8_f32 v11, v5, v16
	v_mul_f32_e32 v13, v21, v13
	v_mul_f32_e32 v12, 0x41800000, v18
	v_mul_f32_e32 v5, 0x41800000, v13
	v_med3_f32 v12, v12, s53, v205
	v_med3_f32 v5, v5, s53, v205
	v_cvt_pk_fp8_f32 v11, v12, v5 op_sel:[0,0,1]
	v_add_u32_e32 v16, 0x80, v4
	v_pk_mul_f32 v[20:21], v[94:95], s[24:25] op_sel_hi:[1,0]
	v_pk_mul_f32 v[18:19], v[96:97], s[24:25] op_sel_hi:[1,0]
	global_store_dwordx2 v[14:15], v[10:11], off offset:128
	v_mad_i64_i32 v[10:11], s[2:3], v16, s47, v[6:7]
	v_lshl_add_u64 v[10:11], v[10:11], 0, v[8:9]
	v_pk_mul_f32 v[24:25], v[90:91], s[24:25] op_sel_hi:[1,0]
	v_pk_mul_f32 v[22:23], v[92:93], s[24:25] op_sel_hi:[1,0]
	v_ashrrev_i32_e32 v17, 31, v16
	s_waitcnt vmcnt(7)
	v_mov_b64_e32 v[12:13], v[246:247]
	v_mov_b64_e32 v[14:15], v[248:249]
	v_lshlrev_b32_e32 v5, 16, v12
	v_mul_f32_e32 v5, 0xbfb8aa3b, v5
	v_exp_f32_e32 v5, v5
	v_and_b32_e32 v12, 0xffff0000, v12
	v_mul_f32_e32 v12, 0xbfb8aa3b, v12
	v_exp_f32_e32 v12, v12
	v_add_f32_e32 v5, 1.0, v5
	v_add_f32_e32 v12, 1.0, v12
	v_lshlrev_b32_e32 v27, 16, v13
	v_rcp_f32_e32 v5, v5
	v_mul_f32_e32 v27, 0xbfb8aa3b, v27
	v_mul_f32_e32 v5, v20, v5
	v_exp_f32_e32 v27, v27
	s_nop 0
	v_add_f32_e32 v27, 1.0, v27
	v_and_b32_e32 v13, 0xffff0000, v13
	v_mul_f32_e32 v13, 0xbfb8aa3b, v13
	v_exp_f32_e32 v13, v13
	v_rcp_f32_e32 v12, v12
	s_nop 0
	v_mul_f32_e32 v12, v21, v12
	v_add_f32_e32 v13, 1.0, v13
	v_rcp_f32_e32 v20, v27
	v_lshlrev_b32_e32 v27, 16, v14
	v_mul_f32_e32 v18, v18, v20
	v_mul_f32_e32 v27, 0xbfb8aa3b, v27
	v_exp_f32_e32 v27, v27
	s_nop 0
	v_add_f32_e32 v26, 1.0, v27
	v_and_b32_e32 v14, 0xffff0000, v14
	v_mul_f32_e32 v14, 0xbfb8aa3b, v14
	v_rcp_f32_e32 v13, v13
	v_exp_f32_e32 v14, v14
	v_mul_f32_e32 v13, v19, v13
	v_add_f32_e32 v14, 1.0, v14
	v_rcp_f32_e32 v19, v26
	v_lshlrev_b32_e32 v26, 16, v15
	v_mul_f32_e32 v26, 0xbfb8aa3b, v26
	v_exp_f32_e32 v26, v26
	v_mul_f32_e32 v19, v24, v19
	v_add_f32_e32 v21, 1.0, v26
	v_and_b32_e32 v15, 0xffff0000, v15
	v_mul_f32_e32 v15, 0xbfb8aa3b, v15
	v_exp_f32_e32 v15, v15
	v_rcp_f32_e32 v14, v14
	s_nop 0
	v_mul_f32_e32 v14, v25, v14
	v_add_f32_e32 v15, 1.0, v15
	v_rcp_f32_e32 v20, v21
	s_nop 0
	v_mul_f32_e32 v20, v22, v20
	v_mul_f32_e32 v5, 0x41800000, v5
	v_mul_f32_e32 v12, 0x41800000, v12
	v_rcp_f32_e32 v15, v15
	v_med3_f32 v5, v5, s53, v205
	v_med3_f32 v21, v12, s53, v205
	v_mov_b32_e32 v12, v167
	v_cvt_pk_fp8_f32 v12, v5, v21
	v_mul_f32_e32 v18, 0x41800000, v18
	v_mul_f32_e32 v5, 0x41800000, v13
	v_med3_f32 v13, v18, s53, v205
	v_med3_f32 v5, v5, s53, v205
	v_cvt_pk_fp8_f32 v12, v13, v5 op_sel:[0,0,1]
	v_mul_f32_e32 v5, 0x41800000, v19
	v_mul_f32_e32 v13, 0x41800000, v14
	v_med3_f32 v5, v5, s53, v205
	v_med3_f32 v18, v13, s53, v205
	v_mov_b32_e32 v13, v167
	v_cvt_pk_fp8_f32 v13, v5, v18
	v_mul_f32_e32 v15, v23, v15
	v_mul_f32_e32 v14, 0x41800000, v20
	v_mul_f32_e32 v5, 0x41800000, v15
	v_med3_f32 v14, v14, s53, v205
	v_med3_f32 v5, v5, s53, v205
	v_cvt_pk_fp8_f32 v13, v14, v5 op_sel:[0,0,1]
	v_lshlrev_b64 v[14:15], 11, v[16:17]
	v_lshl_add_u64 v[14:15], s[14:15], 0, v[14:15]
	v_lshl_add_u64 v[14:15], v[14:15], 0, v[2:3]
	global_store_dwordx2 v[14:15], v[12:13], off
	v_pk_mul_f32 v[18:19], v[86:87], s[24:25] op_sel_hi:[1,0]
	v_pk_mul_f32 v[16:17], v[88:89], s[24:25] op_sel_hi:[1,0]
	v_pk_mul_f32 v[22:23], v[82:83], s[24:25] op_sel_hi:[1,0]
	v_pk_mul_f32 v[20:21], v[84:85], s[24:25] op_sel_hi:[1,0]
	s_waitcnt vmcnt(6)
	v_mov_b64_e32 v[10:11], v[250:251]
	v_mov_b64_e32 v[12:13], v[252:253]
	v_lshlrev_b32_e32 v5, 16, v10
	v_mul_f32_e32 v5, 0xbfb8aa3b, v5
	v_exp_f32_e32 v5, v5
	v_and_b32_e32 v10, 0xffff0000, v10
	v_mul_f32_e32 v10, 0xbfb8aa3b, v10
	v_exp_f32_e32 v10, v10
	v_add_f32_e32 v5, 1.0, v5
	v_add_f32_e32 v10, 1.0, v10
	v_lshlrev_b32_e32 v25, 16, v11
	v_rcp_f32_e32 v5, v5
	v_mul_f32_e32 v25, 0xbfb8aa3b, v25
	v_mul_f32_e32 v5, v18, v5
	v_exp_f32_e32 v25, v25
	s_nop 0
	v_add_f32_e32 v25, 1.0, v25
	v_and_b32_e32 v11, 0xffff0000, v11
	v_mul_f32_e32 v11, 0xbfb8aa3b, v11
	v_exp_f32_e32 v11, v11
	v_rcp_f32_e32 v10, v10
	s_nop 0
	v_mul_f32_e32 v10, v19, v10
	v_add_f32_e32 v11, 1.0, v11
	v_rcp_f32_e32 v18, v25
	v_lshlrev_b32_e32 v25, 16, v12
	v_mul_f32_e32 v16, v16, v18
	v_mul_f32_e32 v25, 0xbfb8aa3b, v25
	v_exp_f32_e32 v25, v25
	s_nop 0
	v_add_f32_e32 v24, 1.0, v25
	v_and_b32_e32 v12, 0xffff0000, v12
	v_mul_f32_e32 v12, 0xbfb8aa3b, v12
	v_rcp_f32_e32 v11, v11
	v_exp_f32_e32 v12, v12
	v_mul_f32_e32 v11, v17, v11
	v_add_f32_e32 v12, 1.0, v12
	v_rcp_f32_e32 v17, v24
	v_lshlrev_b32_e32 v24, 16, v13
	v_mul_f32_e32 v24, 0xbfb8aa3b, v24
	v_exp_f32_e32 v24, v24
	v_mul_f32_e32 v17, v22, v17
	v_add_f32_e32 v19, 1.0, v24
	v_and_b32_e32 v13, 0xffff0000, v13
	v_mul_f32_e32 v13, 0xbfb8aa3b, v13
	v_exp_f32_e32 v13, v13
	v_rcp_f32_e32 v12, v12
	s_nop 0
	v_mul_f32_e32 v12, v23, v12
	v_add_f32_e32 v13, 1.0, v13
	v_rcp_f32_e32 v18, v19
	s_nop 0
	v_mul_f32_e32 v18, v20, v18
	v_mul_f32_e32 v5, 0x41800000, v5
	v_mul_f32_e32 v10, 0x41800000, v10
	v_rcp_f32_e32 v13, v13
	v_med3_f32 v5, v5, s53, v205
	v_med3_f32 v19, v10, s53, v205
	v_mov_b32_e32 v10, v167
	v_cvt_pk_fp8_f32 v10, v5, v19
	v_mul_f32_e32 v16, 0x41800000, v16
	v_mul_f32_e32 v5, 0x41800000, v11
	v_med3_f32 v11, v16, s53, v205
	v_med3_f32 v5, v5, s53, v205
	v_cvt_pk_fp8_f32 v10, v11, v5 op_sel:[0,0,1]
	v_mul_f32_e32 v5, 0x41800000, v17
	v_mul_f32_e32 v11, 0x41800000, v12
	v_med3_f32 v5, v5, s53, v205
	v_med3_f32 v16, v11, s53, v205
	v_mov_b32_e32 v11, v167
	v_cvt_pk_fp8_f32 v11, v5, v16
	v_mul_f32_e32 v13, v21, v13
	v_mul_f32_e32 v12, 0x41800000, v18
	v_mul_f32_e32 v5, 0x41800000, v13
	v_med3_f32 v12, v12, s53, v205
	v_med3_f32 v5, v5, s53, v205
	v_cvt_pk_fp8_f32 v11, v12, v5 op_sel:[0,0,1]
	v_add_u32_e32 v16, 0x90, v4
	v_pk_mul_f32 v[20:21], v[78:79], s[24:25] op_sel_hi:[1,0]
	v_pk_mul_f32 v[18:19], v[80:81], s[24:25] op_sel_hi:[1,0]
	global_store_dwordx2 v[14:15], v[10:11], off offset:128
	v_mad_i64_i32 v[10:11], s[2:3], v16, s47, v[6:7]
	v_lshl_add_u64 v[10:11], v[10:11], 0, v[8:9]
	v_pk_mul_f32 v[24:25], v[74:75], s[24:25] op_sel_hi:[1,0]
	v_pk_mul_f32 v[22:23], v[76:77], s[24:25] op_sel_hi:[1,0]
	v_ashrrev_i32_e32 v17, 31, v16
	s_waitcnt vmcnt(5)
	v_mov_b64_e32 v[12:13], v[214:215]
	v_mov_b64_e32 v[14:15], v[216:217]
	v_lshlrev_b32_e32 v5, 16, v12
	v_mul_f32_e32 v5, 0xbfb8aa3b, v5
	v_exp_f32_e32 v5, v5
	v_and_b32_e32 v12, 0xffff0000, v12
	v_mul_f32_e32 v12, 0xbfb8aa3b, v12
	v_exp_f32_e32 v12, v12
	v_add_f32_e32 v5, 1.0, v5
	v_add_f32_e32 v12, 1.0, v12
	v_lshlrev_b32_e32 v27, 16, v13
	v_rcp_f32_e32 v5, v5
	v_mul_f32_e32 v27, 0xbfb8aa3b, v27
	v_mul_f32_e32 v5, v20, v5
	v_exp_f32_e32 v27, v27
	s_nop 0
	v_add_f32_e32 v27, 1.0, v27
	v_and_b32_e32 v13, 0xffff0000, v13
	v_mul_f32_e32 v13, 0xbfb8aa3b, v13
	v_exp_f32_e32 v13, v13
	v_rcp_f32_e32 v12, v12
	s_nop 0
	v_mul_f32_e32 v12, v21, v12
	v_add_f32_e32 v13, 1.0, v13
	v_rcp_f32_e32 v20, v27
	v_lshlrev_b32_e32 v27, 16, v14
	v_mul_f32_e32 v18, v18, v20
	v_mul_f32_e32 v27, 0xbfb8aa3b, v27
	v_exp_f32_e32 v27, v27
	s_nop 0
	v_add_f32_e32 v26, 1.0, v27
	v_and_b32_e32 v14, 0xffff0000, v14
	v_mul_f32_e32 v14, 0xbfb8aa3b, v14
	v_rcp_f32_e32 v13, v13
	v_exp_f32_e32 v14, v14
	v_mul_f32_e32 v13, v19, v13
	v_add_f32_e32 v14, 1.0, v14
	v_rcp_f32_e32 v19, v26
	v_lshlrev_b32_e32 v26, 16, v15
	v_mul_f32_e32 v26, 0xbfb8aa3b, v26
	v_exp_f32_e32 v26, v26
	v_mul_f32_e32 v19, v24, v19
	v_add_f32_e32 v21, 1.0, v26
	v_and_b32_e32 v15, 0xffff0000, v15
	v_mul_f32_e32 v15, 0xbfb8aa3b, v15
	v_exp_f32_e32 v15, v15
	v_rcp_f32_e32 v14, v14
	s_nop 0
	v_mul_f32_e32 v14, v25, v14
	v_add_f32_e32 v15, 1.0, v15
	v_rcp_f32_e32 v20, v21
	s_nop 0
	v_mul_f32_e32 v20, v22, v20
	v_mul_f32_e32 v5, 0x41800000, v5
	v_mul_f32_e32 v12, 0x41800000, v12
	v_rcp_f32_e32 v15, v15
	v_med3_f32 v5, v5, s53, v205
	v_med3_f32 v21, v12, s53, v205
	v_mov_b32_e32 v12, v167
	v_cvt_pk_fp8_f32 v12, v5, v21
	v_mul_f32_e32 v18, 0x41800000, v18
	v_mul_f32_e32 v5, 0x41800000, v13
	v_med3_f32 v13, v18, s53, v205
	v_med3_f32 v5, v5, s53, v205
	v_cvt_pk_fp8_f32 v12, v13, v5 op_sel:[0,0,1]
	v_mul_f32_e32 v5, 0x41800000, v19
	v_mul_f32_e32 v13, 0x41800000, v14
	v_med3_f32 v5, v5, s53, v205
	v_med3_f32 v18, v13, s53, v205
	v_mov_b32_e32 v13, v167
	v_cvt_pk_fp8_f32 v13, v5, v18
	v_mul_f32_e32 v15, v23, v15
	v_mul_f32_e32 v14, 0x41800000, v20
	v_mul_f32_e32 v5, 0x41800000, v15
	v_med3_f32 v14, v14, s53, v205
	v_med3_f32 v5, v5, s53, v205
	v_cvt_pk_fp8_f32 v13, v14, v5 op_sel:[0,0,1]
	v_lshlrev_b64 v[14:15], 11, v[16:17]
	v_lshl_add_u64 v[14:15], s[14:15], 0, v[14:15]
	v_lshl_add_u64 v[14:15], v[14:15], 0, v[2:3]
	global_store_dwordx2 v[14:15], v[12:13], off
	v_pk_mul_f32 v[18:19], v[70:71], s[24:25] op_sel_hi:[1,0]
	v_pk_mul_f32 v[16:17], v[72:73], s[24:25] op_sel_hi:[1,0]
	v_pk_mul_f32 v[22:23], v[66:67], s[24:25] op_sel_hi:[1,0]
	v_pk_mul_f32 v[20:21], v[68:69], s[24:25] op_sel_hi:[1,0]
	s_waitcnt vmcnt(4)
	v_mov_b64_e32 v[10:11], v[218:219]
	v_mov_b64_e32 v[12:13], v[220:221]
	v_lshlrev_b32_e32 v5, 16, v10
	v_mul_f32_e32 v5, 0xbfb8aa3b, v5
	v_exp_f32_e32 v5, v5
	v_and_b32_e32 v10, 0xffff0000, v10
	v_mul_f32_e32 v10, 0xbfb8aa3b, v10
	v_exp_f32_e32 v10, v10
	v_add_f32_e32 v5, 1.0, v5
	v_add_f32_e32 v10, 1.0, v10
	v_lshlrev_b32_e32 v25, 16, v11
	v_rcp_f32_e32 v5, v5
	v_mul_f32_e32 v25, 0xbfb8aa3b, v25
	v_mul_f32_e32 v5, v18, v5
	v_exp_f32_e32 v25, v25
	s_nop 0
	v_add_f32_e32 v25, 1.0, v25
	v_and_b32_e32 v11, 0xffff0000, v11
	v_mul_f32_e32 v11, 0xbfb8aa3b, v11
	v_exp_f32_e32 v11, v11
	v_rcp_f32_e32 v10, v10
	s_nop 0
	v_mul_f32_e32 v10, v19, v10
	v_add_f32_e32 v11, 1.0, v11
	v_rcp_f32_e32 v18, v25
	v_lshlrev_b32_e32 v25, 16, v12
	v_mul_f32_e32 v16, v16, v18
	v_mul_f32_e32 v25, 0xbfb8aa3b, v25
	v_exp_f32_e32 v25, v25
	s_nop 0
	v_add_f32_e32 v24, 1.0, v25
	v_and_b32_e32 v12, 0xffff0000, v12
	v_mul_f32_e32 v12, 0xbfb8aa3b, v12
	v_rcp_f32_e32 v11, v11
	v_exp_f32_e32 v12, v12
	v_mul_f32_e32 v11, v17, v11
	v_add_f32_e32 v12, 1.0, v12
	v_rcp_f32_e32 v17, v24
	v_lshlrev_b32_e32 v24, 16, v13
	v_mul_f32_e32 v24, 0xbfb8aa3b, v24
	v_exp_f32_e32 v24, v24
	v_mul_f32_e32 v17, v22, v17
	v_add_f32_e32 v19, 1.0, v24
	v_and_b32_e32 v13, 0xffff0000, v13
	v_mul_f32_e32 v13, 0xbfb8aa3b, v13
	v_exp_f32_e32 v13, v13
	v_rcp_f32_e32 v12, v12
	s_nop 0
	v_mul_f32_e32 v12, v23, v12
	v_add_f32_e32 v13, 1.0, v13
	v_rcp_f32_e32 v18, v19
	s_nop 0
	v_mul_f32_e32 v18, v20, v18
	v_mul_f32_e32 v5, 0x41800000, v5
	v_mul_f32_e32 v10, 0x41800000, v10
	v_rcp_f32_e32 v13, v13
	v_med3_f32 v5, v5, s53, v205
	v_med3_f32 v19, v10, s53, v205
	v_mov_b32_e32 v10, v167
	v_cvt_pk_fp8_f32 v10, v5, v19
	v_mul_f32_e32 v16, 0x41800000, v16
	v_mul_f32_e32 v5, 0x41800000, v11
	v_med3_f32 v11, v16, s53, v205
	v_med3_f32 v5, v5, s53, v205
	v_cvt_pk_fp8_f32 v10, v11, v5 op_sel:[0,0,1]
	v_mul_f32_e32 v5, 0x41800000, v17
	v_mul_f32_e32 v11, 0x41800000, v12
	v_med3_f32 v5, v5, s53, v205
	v_med3_f32 v16, v11, s53, v205
	v_mov_b32_e32 v11, v167
	v_cvt_pk_fp8_f32 v11, v5, v16
	v_mul_f32_e32 v13, v21, v13
	v_mul_f32_e32 v12, 0x41800000, v18
	v_mul_f32_e32 v5, 0x41800000, v13
	v_med3_f32 v12, v12, s53, v205
	v_med3_f32 v5, v5, s53, v205
	v_cvt_pk_fp8_f32 v11, v12, v5 op_sel:[0,0,1]
	v_add_u32_e32 v16, 0xa0, v4
	v_pk_mul_f32 v[20:21], v[62:63], s[24:25] op_sel_hi:[1,0]
	v_pk_mul_f32 v[18:19], v[64:65], s[24:25] op_sel_hi:[1,0]
	global_store_dwordx2 v[14:15], v[10:11], off offset:128
	v_mad_i64_i32 v[10:11], s[2:3], v16, s47, v[6:7]
	v_lshl_add_u64 v[10:11], v[10:11], 0, v[8:9]
	v_pk_mul_f32 v[24:25], v[58:59], s[24:25] op_sel_hi:[1,0]
	v_pk_mul_f32 v[22:23], v[60:61], s[24:25] op_sel_hi:[1,0]
	v_ashrrev_i32_e32 v17, 31, v16
	s_waitcnt vmcnt(3)
	v_mov_b64_e32 v[12:13], v[222:223]
	v_mov_b64_e32 v[14:15], v[224:225]
	v_lshlrev_b32_e32 v5, 16, v12
	v_mul_f32_e32 v5, 0xbfb8aa3b, v5
	v_exp_f32_e32 v5, v5
	v_and_b32_e32 v12, 0xffff0000, v12
	v_mul_f32_e32 v12, 0xbfb8aa3b, v12
	v_exp_f32_e32 v12, v12
	v_add_f32_e32 v5, 1.0, v5
	v_add_f32_e32 v12, 1.0, v12
	v_lshlrev_b32_e32 v27, 16, v13
	v_rcp_f32_e32 v5, v5
	v_mul_f32_e32 v27, 0xbfb8aa3b, v27
	v_mul_f32_e32 v5, v20, v5
	v_exp_f32_e32 v27, v27
	s_nop 0
	v_add_f32_e32 v27, 1.0, v27
	v_and_b32_e32 v13, 0xffff0000, v13
	v_mul_f32_e32 v13, 0xbfb8aa3b, v13
	v_exp_f32_e32 v13, v13
	v_rcp_f32_e32 v12, v12
	s_nop 0
	v_mul_f32_e32 v12, v21, v12
	v_add_f32_e32 v13, 1.0, v13
	v_rcp_f32_e32 v20, v27
	v_lshlrev_b32_e32 v27, 16, v14
	v_mul_f32_e32 v18, v18, v20
	v_mul_f32_e32 v27, 0xbfb8aa3b, v27
	v_exp_f32_e32 v27, v27
	s_nop 0
	v_add_f32_e32 v26, 1.0, v27
	v_and_b32_e32 v14, 0xffff0000, v14
	v_mul_f32_e32 v14, 0xbfb8aa3b, v14
	v_rcp_f32_e32 v13, v13
	v_exp_f32_e32 v14, v14
	v_mul_f32_e32 v13, v19, v13
	v_add_f32_e32 v14, 1.0, v14
	v_rcp_f32_e32 v19, v26
	v_lshlrev_b32_e32 v26, 16, v15
	v_mul_f32_e32 v26, 0xbfb8aa3b, v26
	v_exp_f32_e32 v26, v26
	v_mul_f32_e32 v19, v24, v19
	v_add_f32_e32 v21, 1.0, v26
	v_and_b32_e32 v15, 0xffff0000, v15
	v_mul_f32_e32 v15, 0xbfb8aa3b, v15
	v_exp_f32_e32 v15, v15
	v_rcp_f32_e32 v14, v14
	s_nop 0
	v_mul_f32_e32 v14, v25, v14
	v_add_f32_e32 v15, 1.0, v15
	v_rcp_f32_e32 v20, v21
	s_nop 0
	v_mul_f32_e32 v20, v22, v20
	v_mul_f32_e32 v5, 0x41800000, v5
	v_mul_f32_e32 v12, 0x41800000, v12
	v_rcp_f32_e32 v15, v15
	v_med3_f32 v5, v5, s53, v205
	v_med3_f32 v21, v12, s53, v205
	v_mov_b32_e32 v12, v167
	v_cvt_pk_fp8_f32 v12, v5, v21
	v_mul_f32_e32 v18, 0x41800000, v18
	v_mul_f32_e32 v5, 0x41800000, v13
	v_med3_f32 v13, v18, s53, v205
	v_med3_f32 v5, v5, s53, v205
	v_cvt_pk_fp8_f32 v12, v13, v5 op_sel:[0,0,1]
	v_mul_f32_e32 v5, 0x41800000, v19
	v_mul_f32_e32 v13, 0x41800000, v14
	v_med3_f32 v5, v5, s53, v205
	v_med3_f32 v18, v13, s53, v205
	v_mov_b32_e32 v13, v167
	v_cvt_pk_fp8_f32 v13, v5, v18
	v_mul_f32_e32 v15, v23, v15
	v_mul_f32_e32 v14, 0x41800000, v20
	v_mul_f32_e32 v5, 0x41800000, v15
	v_med3_f32 v14, v14, s53, v205
	v_med3_f32 v5, v5, s53, v205
	v_cvt_pk_fp8_f32 v13, v14, v5 op_sel:[0,0,1]
	v_lshlrev_b64 v[14:15], 11, v[16:17]
	v_lshl_add_u64 v[14:15], s[14:15], 0, v[14:15]
	v_lshl_add_u64 v[14:15], v[14:15], 0, v[2:3]
	global_store_dwordx2 v[14:15], v[12:13], off
	v_pk_mul_f32 v[18:19], v[54:55], s[24:25] op_sel_hi:[1,0]
	v_pk_mul_f32 v[16:17], v[56:57], s[24:25] op_sel_hi:[1,0]
	v_pk_mul_f32 v[22:23], v[50:51], s[24:25] op_sel_hi:[1,0]
	v_pk_mul_f32 v[20:21], v[52:53], s[24:25] op_sel_hi:[1,0]
	s_waitcnt vmcnt(2)
	v_mov_b64_e32 v[10:11], v[226:227]
	v_mov_b64_e32 v[12:13], v[228:229]
	v_lshlrev_b32_e32 v5, 16, v10
	v_mul_f32_e32 v5, 0xbfb8aa3b, v5
	v_exp_f32_e32 v5, v5
	v_and_b32_e32 v10, 0xffff0000, v10
	v_mul_f32_e32 v10, 0xbfb8aa3b, v10
	v_exp_f32_e32 v10, v10
	v_add_f32_e32 v5, 1.0, v5
	v_add_f32_e32 v10, 1.0, v10
	v_lshlrev_b32_e32 v25, 16, v11
	v_rcp_f32_e32 v5, v5
	v_mul_f32_e32 v25, 0xbfb8aa3b, v25
	v_mul_f32_e32 v5, v18, v5
	v_exp_f32_e32 v25, v25
	s_nop 0
	v_add_f32_e32 v25, 1.0, v25
	v_and_b32_e32 v11, 0xffff0000, v11
	v_mul_f32_e32 v11, 0xbfb8aa3b, v11
	v_exp_f32_e32 v11, v11
	v_rcp_f32_e32 v10, v10
	s_nop 0
	v_mul_f32_e32 v10, v19, v10
	v_add_f32_e32 v11, 1.0, v11
	v_rcp_f32_e32 v18, v25
	v_lshlrev_b32_e32 v25, 16, v12
	v_mul_f32_e32 v16, v16, v18
	v_mul_f32_e32 v25, 0xbfb8aa3b, v25
	v_exp_f32_e32 v25, v25
	s_nop 0
	v_add_f32_e32 v24, 1.0, v25
	v_and_b32_e32 v12, 0xffff0000, v12
	v_mul_f32_e32 v12, 0xbfb8aa3b, v12
	v_rcp_f32_e32 v11, v11
	v_exp_f32_e32 v12, v12
	v_mul_f32_e32 v11, v17, v11
	v_add_f32_e32 v12, 1.0, v12
	v_rcp_f32_e32 v17, v24
	v_lshlrev_b32_e32 v24, 16, v13
	v_mul_f32_e32 v24, 0xbfb8aa3b, v24
	v_exp_f32_e32 v24, v24
	v_mul_f32_e32 v17, v22, v17
	v_add_f32_e32 v19, 1.0, v24
	v_and_b32_e32 v13, 0xffff0000, v13
	v_mul_f32_e32 v13, 0xbfb8aa3b, v13
	v_exp_f32_e32 v13, v13
	v_rcp_f32_e32 v12, v12
	s_nop 0
	v_mul_f32_e32 v12, v23, v12
	v_add_f32_e32 v13, 1.0, v13
	v_rcp_f32_e32 v18, v19
	s_nop 0
	v_mul_f32_e32 v18, v20, v18
	v_mul_f32_e32 v5, 0x41800000, v5
	v_mul_f32_e32 v10, 0x41800000, v10
	v_rcp_f32_e32 v13, v13
	v_med3_f32 v5, v5, s53, v205
	v_med3_f32 v19, v10, s53, v205
	v_mov_b32_e32 v10, v167
	v_cvt_pk_fp8_f32 v10, v5, v19
	v_mul_f32_e32 v16, 0x41800000, v16
	v_mul_f32_e32 v5, 0x41800000, v11
	v_med3_f32 v11, v16, s53, v205
	v_med3_f32 v5, v5, s53, v205
	v_cvt_pk_fp8_f32 v10, v11, v5 op_sel:[0,0,1]
	v_mul_f32_e32 v5, 0x41800000, v17
	v_mul_f32_e32 v11, 0x41800000, v12
	v_med3_f32 v5, v5, s53, v205
	v_med3_f32 v16, v11, s53, v205
	v_mov_b32_e32 v11, v167
	v_cvt_pk_fp8_f32 v11, v5, v16
	v_mul_f32_e32 v13, v21, v13
	v_mul_f32_e32 v12, 0x41800000, v18
	v_mul_f32_e32 v5, 0x41800000, v13
	v_med3_f32 v12, v12, s53, v205
	v_med3_f32 v5, v5, s53, v205
	v_cvt_pk_fp8_f32 v11, v12, v5 op_sel:[0,0,1]
	v_pk_mul_f32 v[12:13], v[48:49], s[24:25] op_sel_hi:[1,0]
	v_pk_mul_f32 v[18:19], v[42:43], s[24:25] op_sel_hi:[1,0]
	v_pk_mul_f32 v[16:17], v[44:45], s[24:25] op_sel_hi:[1,0]
	global_store_dwordx2 v[14:15], v[10:11], off offset:128
	v_add_u32_e32 v10, 0xb0, v4
	v_mad_i64_i32 v[4:5], s[2:3], v10, s47, v[6:7]
	v_lshl_add_u64 v[4:5], v[4:5], 0, v[8:9]
	s_waitcnt vmcnt(1)
	v_mov_b64_e32 v[6:7], v[230:231]
	v_mov_b64_e32 v[8:9], v[232:233]
	v_lshlrev_b32_e32 v11, 16, v6
	v_mul_f32_e32 v11, 0xbfb8aa3b, v11
	v_exp_f32_e32 v14, v11
	v_and_b32_e32 v6, 0xffff0000, v6
	v_mul_f32_e32 v6, 0xbfb8aa3b, v6
	v_exp_f32_e32 v6, v6
	v_add_f32_e32 v20, 1.0, v14
	v_add_f32_e32 v6, 1.0, v6
	v_pk_mul_f32 v[14:15], v[46:47], s[24:25] op_sel_hi:[1,0]
	v_ashrrev_i32_e32 v11, 31, v10
	v_lshlrev_b32_e32 v22, 16, v7
	v_rcp_f32_e32 v20, v20
	v_mul_f32_e32 v22, 0xbfb8aa3b, v22
	v_mul_f32_e32 v14, v14, v20
	v_exp_f32_e32 v22, v22
	s_nop 0
	v_add_f32_e32 v22, 1.0, v22
	v_and_b32_e32 v7, 0xffff0000, v7
	v_mul_f32_e32 v7, 0xbfb8aa3b, v7
	v_rcp_f32_e32 v6, v6
	v_exp_f32_e32 v7, v7
	v_mul_f32_e32 v6, v15, v6
	v_add_f32_e32 v7, 1.0, v7
	v_rcp_f32_e32 v15, v22
	v_lshlrev_b32_e32 v22, 16, v8
	v_mul_f32_e32 v12, v12, v15
	v_mul_f32_e32 v22, 0xbfb8aa3b, v22
	v_exp_f32_e32 v22, v22
	s_nop 0
	v_add_f32_e32 v21, 1.0, v22
	v_and_b32_e32 v8, 0xffff0000, v8
	v_mul_f32_e32 v8, 0xbfb8aa3b, v8
	v_rcp_f32_e32 v7, v7
	v_exp_f32_e32 v8, v8
	v_mul_f32_e32 v7, v13, v7
	v_add_f32_e32 v8, 1.0, v8
	v_rcp_f32_e32 v13, v21
	v_lshlrev_b32_e32 v21, 16, v9
	v_mul_f32_e32 v21, 0xbfb8aa3b, v21
	v_exp_f32_e32 v21, v21
	v_mul_f32_e32 v13, v18, v13
	v_add_f32_e32 v20, 1.0, v21
	v_and_b32_e32 v9, 0xffff0000, v9
	v_mul_f32_e32 v9, 0xbfb8aa3b, v9
	v_exp_f32_e32 v9, v9
	v_rcp_f32_e32 v8, v8
	s_nop 0
	v_mul_f32_e32 v8, v19, v8
	v_add_f32_e32 v9, 1.0, v9
	v_rcp_f32_e32 v15, v20
	s_nop 0
	v_mul_f32_e32 v15, v16, v15
	v_mul_f32_e32 v14, 0x41800000, v14
	v_mul_f32_e32 v6, 0x41800000, v6
	v_rcp_f32_e32 v9, v9
	v_med3_f32 v14, v14, s53, v205
	v_med3_f32 v16, v6, s53, v205
	v_mov_b32_e32 v6, v167
	v_cvt_pk_fp8_f32 v6, v14, v16
	v_mul_f32_e32 v12, 0x41800000, v12
	v_mul_f32_e32 v7, 0x41800000, v7
	v_med3_f32 v12, v12, s53, v205
	v_med3_f32 v7, v7, s53, v205
	v_cvt_pk_fp8_f32 v6, v12, v7 op_sel:[0,0,1]
	v_mul_f32_e32 v7, 0x41800000, v13
	v_mul_f32_e32 v8, 0x41800000, v8
	v_med3_f32 v13, v7, s53, v205
	v_med3_f32 v8, v8, s53, v205
	v_mov_b32_e32 v7, v167
	v_cvt_pk_fp8_f32 v7, v13, v8
	v_mul_f32_e32 v9, v17, v9
	v_mul_f32_e32 v12, 0x41800000, v15
	v_mul_f32_e32 v8, 0x41800000, v9
	v_med3_f32 v9, v12, s53, v205
	v_med3_f32 v8, v8, s53, v205
	v_cvt_pk_fp8_f32 v7, v9, v8 op_sel:[0,0,1]
	v_lshlrev_b64 v[8:9], 11, v[10:11]
	v_lshl_add_u64 v[8:9], s[14:15], 0, v[8:9]
	v_lshl_add_u64 v[8:9], v[8:9], 0, v[2:3]
	global_store_dwordx2 v[8:9], v[6:7], off
	v_pk_mul_f32 v[14:15], v[34:35], s[24:25] op_sel_hi:[1,0]
	v_pk_mul_f32 v[12:13], v[36:37], s[24:25] op_sel_hi:[1,0]
	s_waitcnt vmcnt(0)
	v_mov_b64_e32 v[2:3], v[234:235]
	v_mov_b64_e32 v[4:5], v[236:237]
	v_lshlrev_b32_e32 v6, 16, v2
	v_mul_f32_e32 v6, 0xbfb8aa3b, v6
	v_exp_f32_e32 v10, v6
	v_and_b32_e32 v2, 0xffff0000, v2
	v_mul_f32_e32 v2, 0xbfb8aa3b, v2
	v_exp_f32_e32 v2, v2
	v_add_f32_e32 v16, 1.0, v10
	v_add_f32_e32 v2, 1.0, v2
	v_pk_mul_f32 v[10:11], v[38:39], s[24:25] op_sel_hi:[1,0]
	v_pk_mul_f32 v[6:7], v[40:41], s[24:25] op_sel_hi:[1,0]
	v_lshlrev_b32_e32 v18, 16, v3
	v_rcp_f32_e32 v16, v16
	v_mul_f32_e32 v18, 0xbfb8aa3b, v18
	v_mul_f32_e32 v10, v10, v16
	v_exp_f32_e32 v18, v18
	s_nop 0
	v_add_f32_e32 v18, 1.0, v18
	v_and_b32_e32 v3, 0xffff0000, v3
	v_mul_f32_e32 v3, 0xbfb8aa3b, v3
	v_rcp_f32_e32 v2, v2
	v_exp_f32_e32 v3, v3
	v_mul_f32_e32 v2, v11, v2
	v_add_f32_e32 v3, 1.0, v3
	v_rcp_f32_e32 v11, v18
	v_lshlrev_b32_e32 v18, 16, v4
	v_mul_f32_e32 v6, v6, v11
	v_mul_f32_e32 v18, 0xbfb8aa3b, v18
	v_exp_f32_e32 v18, v18
	s_nop 0
	v_add_f32_e32 v17, 1.0, v18
	v_and_b32_e32 v4, 0xffff0000, v4
	v_mul_f32_e32 v4, 0xbfb8aa3b, v4
	v_rcp_f32_e32 v3, v3
	v_exp_f32_e32 v4, v4
	v_mul_f32_e32 v3, v7, v3
	v_add_f32_e32 v4, 1.0, v4
	v_rcp_f32_e32 v7, v17
	v_lshlrev_b32_e32 v17, 16, v5
	v_mul_f32_e32 v17, 0xbfb8aa3b, v17
	v_exp_f32_e32 v17, v17
	v_mul_f32_e32 v7, v14, v7
	v_add_f32_e32 v16, 1.0, v17
	v_and_b32_e32 v5, 0xffff0000, v5
	v_mul_f32_e32 v5, 0xbfb8aa3b, v5
	v_exp_f32_e32 v5, v5
	v_rcp_f32_e32 v4, v4
	s_nop 0
	v_mul_f32_e32 v4, v15, v4
	v_add_f32_e32 v5, 1.0, v5
	v_rcp_f32_e32 v11, v16
	s_nop 0
	v_mul_f32_e32 v11, v12, v11
	v_mul_f32_e32 v10, 0x41800000, v10
	v_mul_f32_e32 v2, 0x41800000, v2
	v_rcp_f32_e32 v5, v5
	v_med3_f32 v10, v10, s53, v205
	v_med3_f32 v12, v2, s53, v205
	v_mov_b32_e32 v2, v167
	v_cvt_pk_fp8_f32 v2, v10, v12
	v_mul_f32_e32 v6, 0x41800000, v6
	v_mul_f32_e32 v3, 0x41800000, v3
	v_med3_f32 v6, v6, s53, v205
	v_med3_f32 v3, v3, s53, v205
	v_cvt_pk_fp8_f32 v2, v6, v3 op_sel:[0,0,1]
	v_mul_f32_e32 v3, 0x41800000, v7
	v_mul_f32_e32 v4, 0x41800000, v4
	v_med3_f32 v7, v3, s53, v205
	v_med3_f32 v4, v4, s53, v205
	v_mov_b32_e32 v3, v167
	v_cvt_pk_fp8_f32 v3, v7, v4
	v_mul_f32_e32 v5, v13, v5
	v_mul_f32_e32 v6, 0x41800000, v11
	v_mul_f32_e32 v4, 0x41800000, v5
	v_med3_f32 v5, v6, s53, v205
	v_med3_f32 v4, v4, s53, v205
	v_cvt_pk_fp8_f32 v3, v5, v4 op_sel:[0,0,1]
	s_andn2_b64 vcc, exec, s[0:1]
	s_mov_b64 s[0:1], -1
	global_store_dwordx2 v[8:9], v[2:3], off offset:128
	s_cbranch_vccnz .LBB0_966
	s_andn2_b64 vcc, exec, s[12:13]
	s_cbranch_vccnz .LBB0_965
	s_barrier
	s_branch .LBB0_965

.LBB0_1066:
	v_lshl_or_b32 v6, s61, 8, v204
	v_add_u32_e32 v8, s60, v202
	v_ashrrev_i32_e32 v7, 31, v6
	v_mov_b64_e32 v[10:11], s[18:19]
	v_mad_i64_i32 v[2:3], s[0:1], v8, s56, v[10:11]
	v_lshlrev_b64 v[12:13], 1, v[6:7]
	v_lshl_add_u32 v251, v8, 11, v6
	v_mad_u32_u24 v250, v8, s56, v12
	global_load_dwordx4 v[214:217], v250, s[18:19] nt
	global_load_dwordx2 v[238:239], v251, s[16:17] nt
	v_lshl_add_u32 v251, v8, 11, v6
	v_mad_u32_u24 v250, v8, s56, v12
	global_load_dwordx4 v[218:221], v250, s[18:19] offset:256 nt
	global_load_dwordx2 v[240:241], v251, s[16:17] offset:128 nt
	v_add_u32_e32 v250, 16, v8
	v_lshl_add_u32 v251, v250, 11, v6
	v_mad_u32_u24 v250, v250, s56, v12
	global_load_dwordx4 v[222:225], v250, s[18:19] nt
	global_load_dwordx2 v[242:243], v251, s[16:17] nt
	v_add_u32_e32 v250, 16, v8
	v_lshl_add_u32 v251, v250, 11, v6
	v_mad_u32_u24 v250, v250, s56, v12
	global_load_dwordx4 v[226:229], v250, s[18:19] offset:256 nt
	global_load_dwordx2 v[244:245], v251, s[16:17] offset:128 nt
	v_add_u32_e32 v250, 32, v8
	v_lshl_add_u32 v251, v250, 11, v6
	v_mad_u32_u24 v250, v250, s56, v12
	global_load_dwordx4 v[230:233], v250, s[18:19] nt
	global_load_dwordx2 v[246:247], v251, s[16:17] nt
	v_add_u32_e32 v250, 32, v8
	v_lshl_add_u32 v251, v250, 11, v6
	v_mad_u32_u24 v250, v250, s56, v12
	global_load_dwordx4 v[234:237], v250, s[18:19] offset:256 nt
	global_load_dwordx2 v[248:249], v251, s[16:17] offset:128 nt
	s_nop 15
	s_nop 15
	s_nop 15
	v_lshl_add_u64 v[14:15], v[2:3], 0, v[12:13]
	v_ashrrev_i32_e32 v9, 31, v8
	v_lshlrev_b64 v[16:17], 11, v[8:9]
	v_lshl_add_u64 v[18:19], s[16:17], 0, v[16:17]
	v_lshl_add_u64 v[18:19], v[18:19], 0, v[6:7]
	v_pk_mul_f32 v[22:23], v[154:155], s[28:29] op_sel_hi:[1,0]
	v_pk_mul_f32 v[20:21], v[156:157], s[28:29] op_sel_hi:[1,0]
	v_pk_mul_f32 v[26:27], v[158:159], s[28:29] op_sel_hi:[1,0]
	v_pk_mul_f32 v[24:25], v[160:161], s[28:29] op_sel_hi:[1,0]
	s_waitcnt vmcnt(11)
	v_mov_b64_e32 v[2:3], v[214:215]
	v_mov_b64_e32 v[4:5], v[216:217]
	s_waitcnt vmcnt(10)
	v_mov_b64_e32 v[28:29], v[238:239]
	v_add_u32_e32 v250, 48, v8
	v_lshl_add_u32 v251, v250, 11, v6
	v_mad_u32_u24 v250, v250, s56, v12
	global_load_dwordx4 v[214:217], v250, s[18:19] nt
	global_load_dwordx2 v[238:239], v251, s[16:17] nt
	v_lshlrev_b32_e32 v9, 16, v2
	v_and_b32_e32 v2, 0xffff0000, v2
	v_mul_f32_e32 v9, 0xbfb8aa3b, v9
	v_lshlrev_b32_e32 v30, 16, v3
	v_mul_f32_e32 v2, 0xbfb8aa3b, v2
	v_exp_f32_e32 v9, v9
	v_and_b32_e32 v3, 0xffff0000, v3
	v_mul_f32_e32 v30, 0xbfb8aa3b, v30
	v_exp_f32_e32 v2, v2
	v_mul_f32_e32 v3, 0xbfb8aa3b, v3
	v_exp_f32_e32 v30, v30
	v_exp_f32_e32 v3, v3
	v_add_f32_e32 v9, 1.0, v9
	v_add_f32_e32 v2, 1.0, v2
	v_add_f32_e32 v30, 1.0, v30
	v_lshlrev_b32_e32 v31, 16, v4
	v_add_f32_e32 v3, 1.0, v3
	v_mul_f32_e32 v31, 0xbfb8aa3b, v31
	v_exp_f32_e32 v31, v31
	s_nop 0
	v_add_f32_e32 v31, 1.0, v31
	v_and_b32_e32 v4, 0xffff0000, v4
	v_mul_f32_e32 v4, 0xbfb8aa3b, v4
	v_exp_f32_e32 v4, v4
	v_rcp_f32_e32 v179, v9
	v_rcp_f32_e32 v9, v2
	v_rcp_f32_e32 v154, v30
	v_rcp_f32_e32 v155, v3
	v_add_f32_e32 v3, 1.0, v4
	v_lshlrev_b32_e32 v32, 16, v5
	v_rcp_f32_e32 v156, v31
	v_mul_f32_e32 v32, 0xbfb8aa3b, v32
	v_exp_f32_e32 v32, v32
	s_nop 0
	v_add_f32_e32 v4, 1.0, v32
	v_and_b32_e32 v5, 0xffff0000, v5
	v_mul_f32_e32 v5, 0xbfb8aa3b, v5
	v_exp_f32_e32 v5, v5
	v_rcp_f32_e32 v157, v3
	v_add_f32_e32 v5, 1.0, v5
	v_rcp_f32_e32 v158, v4
	v_rcp_f32_e32 v159, v5
	v_cvt_pk_f32_fp8_e32 v[2:3], v28
	v_cvt_pk_f32_fp8_sdwa v[4:5], v28 src0_sel:WORD_1
	v_mov_b32_e32 v33, v26
	v_cvt_pk_f32_fp8_e32 v[30:31], v29
	v_mov_b32_e32 v32, v2
	v_pk_mul_f32 v[32:33], v[32:33], v[178:179]
	v_mov_b32_e32 v26, v3
	v_mov_b32_e32 v179, v9
	v_pk_mul_f32 v[2:3], v[26:27], v[178:179]
	v_mov_b32_e32 v179, v154
	v_add_f32_e32 v9, v2, v3
	v_mov_b32_e32 v2, v4
	v_mov_b32_e32 v3, v24
	v_pk_mul_f32 v[2:3], v[2:3], v[178:179]
	v_mov_b32_e32 v24, v5
	v_mov_b32_e32 v179, v155
	v_cvt_pk_f32_fp8_sdwa v[28:29], v29 src0_sel:WORD_1
	v_add_f32_e32 v4, v2, v3
	v_pk_mul_f32 v[2:3], v[24:25], v[178:179]
	v_mov_b32_e32 v179, v156
	v_add_f32_e32 v5, v2, v3
	v_mov_b32_e32 v2, v30
	v_mov_b32_e32 v3, v22
	v_pk_mul_f32 v[2:3], v[2:3], v[178:179]
	v_mov_b32_e32 v22, v31
	v_mov_b32_e32 v179, v157
	v_add_f32_e32 v24, v2, v3
	v_pk_mul_f32 v[2:3], v[22:23], v[178:179]
	v_mov_b32_e32 v179, v158
	v_add_f32_e32 v22, v2, v3
	v_mov_b32_e32 v2, v28
	v_mov_b32_e32 v3, v20
	v_pk_mul_f32 v[2:3], v[2:3], v[178:179]
	v_mov_b32_e32 v20, v29
	v_mov_b32_e32 v179, v159
	v_add_f32_e32 v32, v32, v33
	v_add_f32_e32 v23, v2, v3
	v_pk_mul_f32 v[2:3], v[20:21], v[178:179]
	v_mul_f32_e32 v4, 0x41800000, v4
	v_add_f32_e32 v20, v2, v3
	v_mul_f32_e32 v2, 0x41800000, v32
	v_mul_f32_e32 v3, 0x41800000, v9
	v_med3_f32 v9, v2, s57, v207
	v_med3_f32 v3, v3, s57, v207
	v_mov_b32_e32 v2, v167
	v_cvt_pk_fp8_f32 v2, v9, v3
	v_mul_f32_e32 v3, 0x41800000, v5
	v_med3_f32 v4, v4, s57, v207
	v_med3_f32 v3, v3, s57, v207
	v_cvt_pk_fp8_f32 v2, v4, v3 op_sel:[0,0,1]
	v_mul_f32_e32 v3, 0x41800000, v24
	v_mul_f32_e32 v4, 0x41800000, v22
	v_med3_f32 v9, v3, s57, v207
	v_med3_f32 v4, v4, s57, v207
	v_mov_b32_e32 v3, v167
	v_cvt_pk_fp8_f32 v3, v9, v4
	v_mul_f32_e32 v5, 0x41800000, v23
	v_mul_f32_e32 v4, 0x41800000, v20
	v_med3_f32 v5, v5, s57, v207
	v_med3_f32 v4, v4, s57, v207
	v_cvt_pk_fp8_f32 v3, v5, v4 op_sel:[0,0,1]
	v_lshl_add_u64 v[4:5], s[20:21], 0, v[16:17]
	v_lshl_add_u64 v[16:17], v[4:5], 0, v[6:7]
	v_pk_mul_f32 v[24:25], v[146:147], s[28:29] op_sel_hi:[1,0]
	global_store_dwordx2 v[16:17], v[2:3], off
	s_nop 0
	v_pk_mul_f32 v[20:21], v[150:151], s[28:29] op_sel_hi:[1,0]
	v_pk_mul_f32 v[18:19], v[152:153], s[28:29] op_sel_hi:[1,0]
	v_pk_mul_f32 v[22:23], v[148:149], s[28:29] op_sel_hi:[1,0]
	s_waitcnt vmcnt(11)
	v_mov_b64_e32 v[2:3], v[218:219]
	v_mov_b64_e32 v[4:5], v[220:221]
	v_lshlrev_b32_e32 v9, 16, v2
	v_mul_f32_e32 v9, 0xbfb8aa3b, v9
	v_exp_f32_e32 v9, v9
	v_and_b32_e32 v2, 0xffff0000, v2
	v_mul_f32_e32 v2, 0xbfb8aa3b, v2
	v_exp_f32_e32 v2, v2
	v_add_f32_e32 v9, 1.0, v9
	v_add_f32_e32 v2, 1.0, v2
	v_lshlrev_b32_e32 v27, 16, v3
	v_mul_f32_e32 v27, 0xbfb8aa3b, v27
	v_rcp_f32_e32 v179, v9
	v_exp_f32_e32 v27, v27
	s_nop 0
	v_add_f32_e32 v27, 1.0, v27
	v_and_b32_e32 v3, 0xffff0000, v3
	v_mul_f32_e32 v3, 0xbfb8aa3b, v3
	v_rcp_f32_e32 v9, v2
	v_exp_f32_e32 v3, v3
	s_nop 0
	v_add_f32_e32 v3, 1.0, v3
	v_rcp_f32_e32 v31, v27
	v_lshlrev_b32_e32 v27, 16, v4
	v_mul_f32_e32 v27, 0xbfb8aa3b, v27
	v_exp_f32_e32 v27, v27
	s_nop 0
	v_add_f32_e32 v27, 1.0, v27
	v_and_b32_e32 v4, 0xffff0000, v4
	v_mul_f32_e32 v4, 0xbfb8aa3b, v4
	v_exp_f32_e32 v4, v4
	v_rcp_f32_e32 v30, v3
	v_add_f32_e32 v4, 1.0, v4
	v_rcp_f32_e32 v32, v27
	v_lshlrev_b32_e32 v27, 16, v5
	v_mul_f32_e32 v27, 0xbfb8aa3b, v27
	v_exp_f32_e32 v27, v27
	s_nop 0
	v_add_f32_e32 v26, 1.0, v27
	v_rcp_f32_e32 v33, v4
	v_and_b32_e32 v4, 0xffff0000, v5
	v_mul_f32_e32 v4, 0xbfb8aa3b, v4
	v_exp_f32_e32 v4, v4
	s_nop 0
	v_add_f32_e32 v4, 1.0, v4
	v_rcp_f32_e32 v146, v26
	v_mov_b32_e32 v29, v20
	v_rcp_f32_e32 v147, v4
	s_waitcnt vmcnt(10)
	v_mov_b64_e32 v[14:15], v[240:241]
	v_add_u32_e32 v250, 48, v8
	v_lshl_add_u32 v251, v250, 11, v6
	v_mad_u32_u24 v250, v250, s56, v12
	global_load_dwordx4 v[218:221], v250, s[18:19] offset:256 nt
	global_load_dwordx2 v[240:241], v251, s[16:17] offset:128 nt
	v_cvt_pk_f32_fp8_e32 v[2:3], v14
	v_cvt_pk_f32_fp8_sdwa v[4:5], v14 src0_sel:WORD_1
	v_cvt_pk_f32_fp8_e32 v[26:27], v15
	v_cvt_pk_f32_fp8_sdwa v[14:15], v15 src0_sel:WORD_1
	v_mov_b32_e32 v28, v2
	v_pk_mul_f32 v[28:29], v[28:29], v[178:179]
	v_mov_b32_e32 v20, v3
	v_mov_b32_e32 v179, v9
	v_pk_mul_f32 v[2:3], v[20:21], v[178:179]
	v_mov_b32_e32 v179, v31
	v_add_f32_e32 v9, v2, v3
	v_mov_b32_e32 v2, v4
	v_mov_b32_e32 v3, v18
	v_pk_mul_f32 v[2:3], v[2:3], v[178:179]
	v_mov_b32_e32 v18, v5
	v_mov_b32_e32 v179, v30
	v_add_f32_e32 v4, v2, v3
	v_pk_mul_f32 v[2:3], v[18:19], v[178:179]
	v_mov_b32_e32 v179, v32
	v_add_f32_e32 v5, v2, v3
	v_mov_b32_e32 v2, v26
	v_mov_b32_e32 v3, v24
	v_pk_mul_f32 v[2:3], v[2:3], v[178:179]
	v_mov_b32_e32 v24, v27
	v_mov_b32_e32 v179, v33
	v_add_f32_e32 v18, v2, v3
	v_pk_mul_f32 v[2:3], v[24:25], v[178:179]
	v_mov_b32_e32 v179, v146
	v_add_f32_e32 v19, v2, v3
	v_mov_b32_e32 v2, v14
	v_mov_b32_e32 v3, v22
	v_pk_mul_f32 v[2:3], v[2:3], v[178:179]
	v_mov_b32_e32 v22, v15
	v_mov_b32_e32 v179, v147
	v_add_f32_e32 v28, v28, v29
	v_add_f32_e32 v14, v2, v3
	v_pk_mul_f32 v[2:3], v[22:23], v[178:179]
	v_mul_f32_e32 v4, 0x41800000, v4
	v_add_f32_e32 v15, v2, v3
	v_mul_f32_e32 v2, 0x41800000, v28
	v_mul_f32_e32 v3, 0x41800000, v9
	v_med3_f32 v9, v2, s57, v207
	v_med3_f32 v3, v3, s57, v207
	v_mov_b32_e32 v2, v167
	v_cvt_pk_fp8_f32 v2, v9, v3
	v_mul_f32_e32 v3, 0x41800000, v5
	v_med3_f32 v4, v4, s57, v207
	v_med3_f32 v3, v3, s57, v207
	v_cvt_pk_fp8_f32 v2, v4, v3 op_sel:[0,0,1]
	v_mul_f32_e32 v3, 0x41800000, v18
	v_mul_f32_e32 v4, 0x41800000, v19
	v_med3_f32 v9, v3, s57, v207
	v_med3_f32 v4, v4, s57, v207
	v_mov_b32_e32 v3, v167
	v_cvt_pk_fp8_f32 v3, v9, v4
	v_mul_f32_e32 v5, 0x41800000, v14
	v_mul_f32_e32 v4, 0x41800000, v15
	v_med3_f32 v5, v5, s57, v207
	v_med3_f32 v4, v4, s57, v207
	v_cvt_pk_fp8_f32 v3, v5, v4 op_sel:[0,0,1]
	v_pk_mul_f32 v[28:29], v[138:139], s[28:29] op_sel_hi:[1,0]
	v_pk_mul_f32 v[26:27], v[140:141], s[28:29] op_sel_hi:[1,0]
	v_pk_mul_f32 v[24:25], v[142:143], s[28:29] op_sel_hi:[1,0]
	global_store_dwordx2 v[16:17], v[2:3], off offset:128
	v_add_u32_e32 v16, 16, v8
	v_mad_i64_i32 v[2:3], s[0:1], v16, s56, v[10:11]
	v_lshl_add_u64 v[14:15], v[2:3], 0, v[12:13]
	v_ashrrev_i32_e32 v17, 31, v16
	v_lshlrev_b64 v[18:19], 11, v[16:17]
	v_lshl_add_u64 v[16:17], s[16:17], 0, v[18:19]
	v_lshl_add_u64 v[16:17], v[16:17], 0, v[6:7]
	v_pk_mul_f32 v[22:23], v[144:145], s[28:29] op_sel_hi:[1,0]
	s_waitcnt vmcnt(11)
	v_mov_b64_e32 v[2:3], v[222:223]
	v_mov_b64_e32 v[4:5], v[224:225]
	v_lshlrev_b32_e32 v9, 16, v2
	v_mul_f32_e32 v9, 0xbfb8aa3b, v9
	v_exp_f32_e32 v9, v9
	v_and_b32_e32 v2, 0xffff0000, v2
	v_mul_f32_e32 v2, 0xbfb8aa3b, v2
	v_exp_f32_e32 v2, v2
	v_add_f32_e32 v9, 1.0, v9
	v_add_f32_e32 v2, 1.0, v2
	v_lshlrev_b32_e32 v31, 16, v3
	v_mul_f32_e32 v31, 0xbfb8aa3b, v31
	v_rcp_f32_e32 v179, v9
	v_exp_f32_e32 v31, v31
	s_nop 0
	v_add_f32_e32 v31, 1.0, v31
	v_and_b32_e32 v3, 0xffff0000, v3
	v_mul_f32_e32 v3, 0xbfb8aa3b, v3
	v_rcp_f32_e32 v9, v2
	v_exp_f32_e32 v3, v3
	s_nop 0
	v_add_f32_e32 v3, 1.0, v3
	v_rcp_f32_e32 v139, v31
	v_lshlrev_b32_e32 v31, 16, v4
	v_mul_f32_e32 v31, 0xbfb8aa3b, v31
	v_exp_f32_e32 v31, v31
	s_nop 0
	v_add_f32_e32 v31, 1.0, v31
	v_and_b32_e32 v4, 0xffff0000, v4
	v_mul_f32_e32 v4, 0xbfb8aa3b, v4
	v_exp_f32_e32 v4, v4
	v_rcp_f32_e32 v138, v3
	v_add_f32_e32 v4, 1.0, v4
	v_rcp_f32_e32 v140, v31
	v_lshlrev_b32_e32 v31, 16, v5
	v_mul_f32_e32 v31, 0xbfb8aa3b, v31
	v_exp_f32_e32 v31, v31
	s_nop 0
	v_add_f32_e32 v30, 1.0, v31
	v_rcp_f32_e32 v141, v4
	v_and_b32_e32 v4, 0xffff0000, v5
	v_mul_f32_e32 v4, 0xbfb8aa3b, v4
	v_exp_f32_e32 v4, v4
	s_nop 0
	v_add_f32_e32 v4, 1.0, v4
	v_rcp_f32_e32 v142, v30
	v_mov_b32_e32 v33, v24
	v_rcp_f32_e32 v143, v4
	s_waitcnt vmcnt(10)
	v_mov_b64_e32 v[20:21], v[242:243]
	v_add_u32_e32 v250, 128, v8
	v_lshl_add_u32 v251, v250, 11, v6
	v_mad_u32_u24 v250, v250, s56, v12
	global_load_dwordx4 v[222:225], v250, s[18:19] nt
	global_load_dwordx2 v[242:243], v251, s[16:17] nt
	v_cvt_pk_f32_fp8_e32 v[2:3], v20
	v_cvt_pk_f32_fp8_sdwa v[4:5], v20 src0_sel:WORD_1
	v_cvt_pk_f32_fp8_e32 v[30:31], v21
	v_cvt_pk_f32_fp8_sdwa v[20:21], v21 src0_sel:WORD_1
	v_mov_b32_e32 v32, v2
	v_pk_mul_f32 v[32:33], v[32:33], v[178:179]
	v_mov_b32_e32 v24, v3
	v_mov_b32_e32 v179, v9
	v_pk_mul_f32 v[2:3], v[24:25], v[178:179]
	v_mov_b32_e32 v179, v139
	v_add_f32_e32 v9, v2, v3
	v_mov_b32_e32 v2, v4
	v_mov_b32_e32 v3, v22
	v_pk_mul_f32 v[2:3], v[2:3], v[178:179]
	v_mov_b32_e32 v22, v5
	v_mov_b32_e32 v179, v138
	v_add_f32_e32 v4, v2, v3
	v_pk_mul_f32 v[2:3], v[22:23], v[178:179]
	v_mov_b32_e32 v179, v140
	v_add_f32_e32 v5, v2, v3
	v_mov_b32_e32 v2, v30
	v_mov_b32_e32 v3, v28
	v_pk_mul_f32 v[2:3], v[2:3], v[178:179]
	v_mov_b32_e32 v28, v31
	v_mov_b32_e32 v179, v141
	v_add_f32_e32 v22, v2, v3
	v_pk_mul_f32 v[2:3], v[28:29], v[178:179]
	v_mov_b32_e32 v179, v142
	v_add_f32_e32 v23, v2, v3
	v_mov_b32_e32 v2, v20
	v_mov_b32_e32 v3, v26
	v_pk_mul_f32 v[2:3], v[2:3], v[178:179]
	v_mov_b32_e32 v26, v21
	v_mov_b32_e32 v179, v143
	v_add_f32_e32 v32, v32, v33
	v_add_f32_e32 v20, v2, v3
	v_pk_mul_f32 v[2:3], v[26:27], v[178:179]
	v_mul_f32_e32 v4, 0x41800000, v4
	v_add_f32_e32 v21, v2, v3
	v_mul_f32_e32 v2, 0x41800000, v32
	v_mul_f32_e32 v3, 0x41800000, v9
	v_med3_f32 v9, v2, s57, v207
	v_med3_f32 v3, v3, s57, v207
	v_mov_b32_e32 v2, v167
	v_cvt_pk_fp8_f32 v2, v9, v3
	v_mul_f32_e32 v3, 0x41800000, v5
	v_med3_f32 v4, v4, s57, v207
	v_med3_f32 v3, v3, s57, v207
	v_cvt_pk_fp8_f32 v2, v4, v3 op_sel:[0,0,1]
	v_mul_f32_e32 v3, 0x41800000, v22
	v_mul_f32_e32 v4, 0x41800000, v23
	v_med3_f32 v9, v3, s57, v207
	v_med3_f32 v4, v4, s57, v207
	v_mov_b32_e32 v3, v167
	v_cvt_pk_fp8_f32 v3, v9, v4
	v_mul_f32_e32 v5, 0x41800000, v20
	v_mul_f32_e32 v4, 0x41800000, v21
	v_med3_f32 v5, v5, s57, v207
	v_med3_f32 v4, v4, s57, v207
	v_cvt_pk_fp8_f32 v3, v5, v4 op_sel:[0,0,1]
	v_lshl_add_u64 v[4:5], s[20:21], 0, v[18:19]
	v_lshl_add_u64 v[18:19], v[4:5], 0, v[6:7]
	v_pk_mul_f32 v[24:25], v[130:131], s[28:29] op_sel_hi:[1,0]
	global_store_dwordx2 v[18:19], v[2:3], off
	s_nop 0
	v_pk_mul_f32 v[20:21], v[134:135], s[28:29] op_sel_hi:[1,0]
	v_pk_mul_f32 v[16:17], v[136:137], s[28:29] op_sel_hi:[1,0]
	v_pk_mul_f32 v[22:23], v[132:133], s[28:29] op_sel_hi:[1,0]
	s_waitcnt vmcnt(11)
	v_mov_b64_e32 v[2:3], v[226:227]
	v_mov_b64_e32 v[4:5], v[228:229]
	v_lshlrev_b32_e32 v9, 16, v2
	v_mul_f32_e32 v9, 0xbfb8aa3b, v9
	v_exp_f32_e32 v9, v9
	v_and_b32_e32 v2, 0xffff0000, v2
	v_mul_f32_e32 v2, 0xbfb8aa3b, v2
	v_exp_f32_e32 v2, v2
	v_add_f32_e32 v9, 1.0, v9
	v_add_f32_e32 v2, 1.0, v2
	v_lshlrev_b32_e32 v27, 16, v3
	v_mul_f32_e32 v27, 0xbfb8aa3b, v27
	v_rcp_f32_e32 v179, v9
	v_exp_f32_e32 v27, v27
	s_nop 0
	v_add_f32_e32 v27, 1.0, v27
	v_and_b32_e32 v3, 0xffff0000, v3
	v_mul_f32_e32 v3, 0xbfb8aa3b, v3
	v_rcp_f32_e32 v9, v2
	v_exp_f32_e32 v3, v3
	s_nop 0
	v_add_f32_e32 v3, 1.0, v3
	v_rcp_f32_e32 v31, v27
	v_lshlrev_b32_e32 v27, 16, v4
	v_mul_f32_e32 v27, 0xbfb8aa3b, v27
	v_exp_f32_e32 v27, v27
	s_nop 0
	v_add_f32_e32 v27, 1.0, v27
	v_and_b32_e32 v4, 0xffff0000, v4
	v_mul_f32_e32 v4, 0xbfb8aa3b, v4
	v_exp_f32_e32 v4, v4
	v_rcp_f32_e32 v30, v3
	v_add_f32_e32 v4, 1.0, v4
	v_rcp_f32_e32 v32, v27
	v_lshlrev_b32_e32 v27, 16, v5
	v_mul_f32_e32 v27, 0xbfb8aa3b, v27
	v_exp_f32_e32 v27, v27
	s_nop 0
	v_add_f32_e32 v26, 1.0, v27
	v_rcp_f32_e32 v33, v4
	v_and_b32_e32 v4, 0xffff0000, v5
	v_mul_f32_e32 v4, 0xbfb8aa3b, v4
	v_exp_f32_e32 v4, v4
	s_nop 0
	v_add_f32_e32 v4, 1.0, v4
	v_rcp_f32_e32 v130, v26
	v_mov_b32_e32 v29, v20
	v_rcp_f32_e32 v131, v4
	s_waitcnt vmcnt(10)
	v_mov_b64_e32 v[14:15], v[244:245]
	v_add_u32_e32 v250, 128, v8
	v_lshl_add_u32 v251, v250, 11, v6
	v_mad_u32_u24 v250, v250, s56, v12
	global_load_dwordx4 v[226:229], v250, s[18:19] offset:256 nt
	global_load_dwordx2 v[244:245], v251, s[16:17] offset:128 nt
	v_cvt_pk_f32_fp8_e32 v[2:3], v14
	v_cvt_pk_f32_fp8_sdwa v[4:5], v14 src0_sel:WORD_1
	v_cvt_pk_f32_fp8_e32 v[26:27], v15
	v_cvt_pk_f32_fp8_sdwa v[14:15], v15 src0_sel:WORD_1
	v_mov_b32_e32 v28, v2
	v_pk_mul_f32 v[28:29], v[28:29], v[178:179]
	v_mov_b32_e32 v20, v3
	v_mov_b32_e32 v179, v9
	v_pk_mul_f32 v[2:3], v[20:21], v[178:179]
	v_mov_b32_e32 v179, v31
	v_add_f32_e32 v9, v2, v3
	v_mov_b32_e32 v2, v4
	v_mov_b32_e32 v3, v16
	v_pk_mul_f32 v[2:3], v[2:3], v[178:179]
	v_mov_b32_e32 v16, v5
	v_mov_b32_e32 v179, v30
	v_add_f32_e32 v4, v2, v3
	v_pk_mul_f32 v[2:3], v[16:17], v[178:179]
	v_mov_b32_e32 v179, v32
	v_add_f32_e32 v5, v2, v3
	v_mov_b32_e32 v2, v26
	v_mov_b32_e32 v3, v24
	v_pk_mul_f32 v[2:3], v[2:3], v[178:179]
	v_mov_b32_e32 v24, v27
	v_mov_b32_e32 v179, v33
	v_add_f32_e32 v16, v2, v3
	v_pk_mul_f32 v[2:3], v[24:25], v[178:179]
	v_mov_b32_e32 v179, v130
	v_add_f32_e32 v17, v2, v3
	v_mov_b32_e32 v2, v14
	v_mov_b32_e32 v3, v22
	v_pk_mul_f32 v[2:3], v[2:3], v[178:179]
	v_mov_b32_e32 v22, v15
	v_mov_b32_e32 v179, v131
	v_add_f32_e32 v28, v28, v29
	v_add_f32_e32 v14, v2, v3
	v_pk_mul_f32 v[2:3], v[22:23], v[178:179]
	v_mul_f32_e32 v4, 0x41800000, v4
	v_add_f32_e32 v15, v2, v3
	v_mul_f32_e32 v2, 0x41800000, v28
	v_mul_f32_e32 v3, 0x41800000, v9
	v_med3_f32 v9, v2, s57, v207
	v_med3_f32 v3, v3, s57, v207
	v_mov_b32_e32 v2, v167
	v_cvt_pk_fp8_f32 v2, v9, v3
	v_mul_f32_e32 v3, 0x41800000, v5
	v_med3_f32 v4, v4, s57, v207
	v_med3_f32 v3, v3, s57, v207
	v_cvt_pk_fp8_f32 v2, v4, v3 op_sel:[0,0,1]
	v_mul_f32_e32 v3, 0x41800000, v16
	v_mul_f32_e32 v4, 0x41800000, v17
	v_med3_f32 v9, v3, s57, v207
	v_med3_f32 v4, v4, s57, v207
	v_mov_b32_e32 v3, v167
	v_cvt_pk_fp8_f32 v3, v9, v4
	v_mul_f32_e32 v5, 0x41800000, v14
	v_mul_f32_e32 v4, 0x41800000, v15
	v_med3_f32 v5, v5, s57, v207
	v_med3_f32 v4, v4, s57, v207
	v_cvt_pk_fp8_f32 v3, v5, v4 op_sel:[0,0,1]
	v_add_u32_e32 v16, 32, v8
	v_ashrrev_i32_e32 v17, 31, v16
	v_pk_mul_f32 v[28:29], v[122:123], s[28:29] op_sel_hi:[1,0]
	global_store_dwordx2 v[18:19], v[2:3], off offset:128
	v_mad_i64_i32 v[2:3], s[0:1], v16, s56, v[10:11]
	v_lshl_add_u64 v[14:15], v[2:3], 0, v[12:13]
	v_lshlrev_b64 v[18:19], 11, v[16:17]
	v_lshl_add_u64 v[16:17], s[16:17], 0, v[18:19]
	v_lshl_add_u64 v[16:17], v[16:17], 0, v[6:7]
	v_pk_mul_f32 v[26:27], v[124:125], s[28:29] op_sel_hi:[1,0]
	v_pk_mul_f32 v[24:25], v[126:127], s[28:29] op_sel_hi:[1,0]
	v_pk_mul_f32 v[22:23], v[128:129], s[28:29] op_sel_hi:[1,0]
	s_waitcnt vmcnt(11)
	v_mov_b64_e32 v[2:3], v[230:231]
	v_mov_b64_e32 v[4:5], v[232:233]
	v_lshlrev_b32_e32 v9, 16, v2
	v_mul_f32_e32 v9, 0xbfb8aa3b, v9
	v_exp_f32_e32 v9, v9
	v_and_b32_e32 v2, 0xffff0000, v2
	v_mul_f32_e32 v2, 0xbfb8aa3b, v2
	v_exp_f32_e32 v2, v2
	v_add_f32_e32 v9, 1.0, v9
	v_add_f32_e32 v2, 1.0, v2
	v_lshlrev_b32_e32 v31, 16, v3
	v_mul_f32_e32 v31, 0xbfb8aa3b, v31
	v_rcp_f32_e32 v179, v9
	v_exp_f32_e32 v31, v31
	s_nop 0
	v_add_f32_e32 v31, 1.0, v31
	v_and_b32_e32 v3, 0xffff0000, v3
	v_mul_f32_e32 v3, 0xbfb8aa3b, v3
	v_rcp_f32_e32 v9, v2
	v_exp_f32_e32 v3, v3
	s_nop 0
	v_add_f32_e32 v3, 1.0, v3
	v_rcp_f32_e32 v123, v31
	v_lshlrev_b32_e32 v31, 16, v4
	v_mul_f32_e32 v31, 0xbfb8aa3b, v31
	v_exp_f32_e32 v31, v31
	s_nop 0
	v_add_f32_e32 v31, 1.0, v31
	v_and_b32_e32 v4, 0xffff0000, v4
	v_mul_f32_e32 v4, 0xbfb8aa3b, v4
	v_exp_f32_e32 v4, v4
	v_rcp_f32_e32 v122, v3
	v_add_f32_e32 v4, 1.0, v4
	v_rcp_f32_e32 v124, v31
	v_lshlrev_b32_e32 v31, 16, v5
	v_mul_f32_e32 v31, 0xbfb8aa3b, v31
	v_exp_f32_e32 v31, v31
	s_nop 0
	v_add_f32_e32 v30, 1.0, v31
	v_rcp_f32_e32 v125, v4
	v_and_b32_e32 v4, 0xffff0000, v5
	v_mul_f32_e32 v4, 0xbfb8aa3b, v4
	v_exp_f32_e32 v4, v4
	s_nop 0
	v_add_f32_e32 v4, 1.0, v4
	v_rcp_f32_e32 v126, v30
	v_mov_b32_e32 v33, v24
	v_rcp_f32_e32 v127, v4
	s_waitcnt vmcnt(10)
	v_mov_b64_e32 v[20:21], v[246:247]
	v_add_u32_e32 v250, 144, v8
	v_lshl_add_u32 v251, v250, 11, v6
	v_mad_u32_u24 v250, v250, s56, v12
	global_load_dwordx4 v[230:233], v250, s[18:19] nt
	global_load_dwordx2 v[246:247], v251, s[16:17] nt
	v_cvt_pk_f32_fp8_e32 v[2:3], v20
	v_cvt_pk_f32_fp8_sdwa v[4:5], v20 src0_sel:WORD_1
	v_cvt_pk_f32_fp8_e32 v[30:31], v21
	v_cvt_pk_f32_fp8_sdwa v[20:21], v21 src0_sel:WORD_1
	v_mov_b32_e32 v32, v2
	v_pk_mul_f32 v[32:33], v[32:33], v[178:179]
	v_mov_b32_e32 v24, v3
	v_mov_b32_e32 v179, v9
	v_pk_mul_f32 v[2:3], v[24:25], v[178:179]
	v_mov_b32_e32 v179, v123
	v_add_f32_e32 v9, v2, v3
	v_mov_b32_e32 v2, v4
	v_mov_b32_e32 v3, v22
	v_pk_mul_f32 v[2:3], v[2:3], v[178:179]
	v_mov_b32_e32 v22, v5
	v_mov_b32_e32 v179, v122
	v_add_f32_e32 v4, v2, v3
	v_pk_mul_f32 v[2:3], v[22:23], v[178:179]
	v_mov_b32_e32 v179, v124
	v_add_f32_e32 v5, v2, v3
	v_mov_b32_e32 v2, v30
	v_mov_b32_e32 v3, v28
	v_pk_mul_f32 v[2:3], v[2:3], v[178:179]
	v_mov_b32_e32 v28, v31
	v_mov_b32_e32 v179, v125
	v_add_f32_e32 v22, v2, v3
	v_pk_mul_f32 v[2:3], v[28:29], v[178:179]
	v_mov_b32_e32 v179, v126
	v_add_f32_e32 v23, v2, v3
	v_mov_b32_e32 v2, v20
	v_mov_b32_e32 v3, v26
	v_pk_mul_f32 v[2:3], v[2:3], v[178:179]
	v_mov_b32_e32 v26, v21
	v_mov_b32_e32 v179, v127
	v_add_f32_e32 v32, v32, v33
	v_add_f32_e32 v20, v2, v3
	v_pk_mul_f32 v[2:3], v[26:27], v[178:179]
	v_mul_f32_e32 v4, 0x41800000, v4
	v_add_f32_e32 v21, v2, v3
	v_mul_f32_e32 v2, 0x41800000, v32
	v_mul_f32_e32 v3, 0x41800000, v9
	v_med3_f32 v9, v2, s57, v207
	v_med3_f32 v3, v3, s57, v207
	v_mov_b32_e32 v2, v167
	v_cvt_pk_fp8_f32 v2, v9, v3
	v_mul_f32_e32 v3, 0x41800000, v5
	v_med3_f32 v4, v4, s57, v207
	v_med3_f32 v3, v3, s57, v207
	v_cvt_pk_fp8_f32 v2, v4, v3 op_sel:[0,0,1]
	v_mul_f32_e32 v3, 0x41800000, v22
	v_mul_f32_e32 v4, 0x41800000, v23
	v_med3_f32 v9, v3, s57, v207
	v_med3_f32 v4, v4, s57, v207
	v_mov_b32_e32 v3, v167
	v_cvt_pk_fp8_f32 v3, v9, v4
	v_mul_f32_e32 v5, 0x41800000, v20
	v_mul_f32_e32 v4, 0x41800000, v21
	v_med3_f32 v5, v5, s57, v207
	v_med3_f32 v4, v4, s57, v207
	v_cvt_pk_fp8_f32 v3, v5, v4 op_sel:[0,0,1]
	v_lshl_add_u64 v[4:5], s[20:21], 0, v[18:19]
	v_lshl_add_u64 v[18:19], v[4:5], 0, v[6:7]
	v_pk_mul_f32 v[24:25], v[114:115], s[28:29] op_sel_hi:[1,0]
	global_store_dwordx2 v[18:19], v[2:3], off
	s_nop 0
	v_pk_mul_f32 v[20:21], v[118:119], s[28:29] op_sel_hi:[1,0]
	v_pk_mul_f32 v[16:17], v[120:121], s[28:29] op_sel_hi:[1,0]
	v_pk_mul_f32 v[22:23], v[116:117], s[28:29] op_sel_hi:[1,0]
	s_waitcnt vmcnt(11)
	v_mov_b64_e32 v[2:3], v[234:235]
	v_mov_b64_e32 v[4:5], v[236:237]
	v_lshlrev_b32_e32 v9, 16, v2
	v_mul_f32_e32 v9, 0xbfb8aa3b, v9
	v_exp_f32_e32 v9, v9
	v_and_b32_e32 v2, 0xffff0000, v2
	v_mul_f32_e32 v2, 0xbfb8aa3b, v2
	v_exp_f32_e32 v2, v2
	v_add_f32_e32 v9, 1.0, v9
	v_add_f32_e32 v2, 1.0, v2
	v_lshlrev_b32_e32 v27, 16, v3
	v_mul_f32_e32 v27, 0xbfb8aa3b, v27
	v_rcp_f32_e32 v179, v9
	v_exp_f32_e32 v27, v27
	s_nop 0
	v_add_f32_e32 v27, 1.0, v27
	v_and_b32_e32 v3, 0xffff0000, v3
	v_mul_f32_e32 v3, 0xbfb8aa3b, v3
	v_rcp_f32_e32 v9, v2
	v_exp_f32_e32 v3, v3
	s_nop 0
	v_add_f32_e32 v3, 1.0, v3
	v_rcp_f32_e32 v31, v27
	v_lshlrev_b32_e32 v27, 16, v4
	v_mul_f32_e32 v27, 0xbfb8aa3b, v27
	v_exp_f32_e32 v27, v27
	s_nop 0
	v_add_f32_e32 v27, 1.0, v27
	v_and_b32_e32 v4, 0xffff0000, v4
	v_mul_f32_e32 v4, 0xbfb8aa3b, v4
	v_exp_f32_e32 v4, v4
	v_rcp_f32_e32 v30, v3
	v_add_f32_e32 v4, 1.0, v4
	v_rcp_f32_e32 v32, v27
	v_lshlrev_b32_e32 v27, 16, v5
	v_mul_f32_e32 v27, 0xbfb8aa3b, v27
	v_exp_f32_e32 v27, v27
	s_nop 0
	v_add_f32_e32 v26, 1.0, v27
	v_rcp_f32_e32 v33, v4
	v_and_b32_e32 v4, 0xffff0000, v5
	v_mul_f32_e32 v4, 0xbfb8aa3b, v4
	v_exp_f32_e32 v4, v4
	s_nop 0
	v_add_f32_e32 v4, 1.0, v4
	v_rcp_f32_e32 v114, v26
	v_mov_b32_e32 v29, v20
	v_rcp_f32_e32 v115, v4
	s_waitcnt vmcnt(10)
	v_mov_b64_e32 v[14:15], v[248:249]
	v_add_u32_e32 v250, 144, v8
	v_lshl_add_u32 v251, v250, 11, v6
	v_mad_u32_u24 v250, v250, s56, v12
	global_load_dwordx4 v[234:237], v250, s[18:19] offset:256 nt
	global_load_dwordx2 v[248:249], v251, s[16:17] offset:128 nt
	v_cvt_pk_f32_fp8_e32 v[2:3], v14
	v_cvt_pk_f32_fp8_sdwa v[4:5], v14 src0_sel:WORD_1
	v_cvt_pk_f32_fp8_e32 v[26:27], v15
	v_cvt_pk_f32_fp8_sdwa v[14:15], v15 src0_sel:WORD_1
	v_mov_b32_e32 v28, v2
	v_pk_mul_f32 v[28:29], v[28:29], v[178:179]
	v_mov_b32_e32 v20, v3
	v_mov_b32_e32 v179, v9
	v_pk_mul_f32 v[2:3], v[20:21], v[178:179]
	v_mov_b32_e32 v179, v31
	v_add_f32_e32 v9, v2, v3
	v_mov_b32_e32 v2, v4
	v_mov_b32_e32 v3, v16
	v_pk_mul_f32 v[2:3], v[2:3], v[178:179]
	v_mov_b32_e32 v16, v5
	v_mov_b32_e32 v179, v30
	v_add_f32_e32 v4, v2, v3
	v_pk_mul_f32 v[2:3], v[16:17], v[178:179]
	v_mov_b32_e32 v179, v32
	v_add_f32_e32 v5, v2, v3
	v_mov_b32_e32 v2, v26
	v_mov_b32_e32 v3, v24
	v_pk_mul_f32 v[2:3], v[2:3], v[178:179]
	v_mov_b32_e32 v24, v27
	v_mov_b32_e32 v179, v33
	v_add_f32_e32 v16, v2, v3
	v_pk_mul_f32 v[2:3], v[24:25], v[178:179]
	v_mov_b32_e32 v179, v114
	v_add_f32_e32 v17, v2, v3
	v_mov_b32_e32 v2, v14
	v_mov_b32_e32 v3, v22
	v_pk_mul_f32 v[2:3], v[2:3], v[178:179]
	v_mov_b32_e32 v22, v15
	v_mov_b32_e32 v179, v115
	v_add_f32_e32 v28, v28, v29
	v_add_f32_e32 v14, v2, v3
	v_pk_mul_f32 v[2:3], v[22:23], v[178:179]
	v_mul_f32_e32 v4, 0x41800000, v4
	v_add_f32_e32 v15, v2, v3
	v_mul_f32_e32 v2, 0x41800000, v28
	v_mul_f32_e32 v3, 0x41800000, v9
	v_med3_f32 v9, v2, s57, v207
	v_med3_f32 v3, v3, s57, v207
	v_mov_b32_e32 v2, v167
	v_cvt_pk_fp8_f32 v2, v9, v3
	v_mul_f32_e32 v3, 0x41800000, v5
	v_med3_f32 v4, v4, s57, v207
	v_med3_f32 v3, v3, s57, v207
	v_cvt_pk_fp8_f32 v2, v4, v3 op_sel:[0,0,1]
	v_mul_f32_e32 v3, 0x41800000, v16
	v_mul_f32_e32 v4, 0x41800000, v17
	v_med3_f32 v9, v3, s57, v207
	v_med3_f32 v4, v4, s57, v207
	v_mov_b32_e32 v3, v167
	v_cvt_pk_fp8_f32 v3, v9, v4
	v_mul_f32_e32 v5, 0x41800000, v14
	v_mul_f32_e32 v4, 0x41800000, v15
	v_med3_f32 v5, v5, s57, v207
	v_med3_f32 v4, v4, s57, v207
	v_cvt_pk_fp8_f32 v3, v5, v4 op_sel:[0,0,1]
	v_add_u32_e32 v16, 48, v8
	v_ashrrev_i32_e32 v17, 31, v16
	v_pk_mul_f32 v[28:29], v[106:107], s[28:29] op_sel_hi:[1,0]
	global_store_dwordx2 v[18:19], v[2:3], off offset:128
	v_mad_i64_i32 v[2:3], s[0:1], v16, s56, v[10:11]
	v_lshl_add_u64 v[14:15], v[2:3], 0, v[12:13]
	v_lshlrev_b64 v[18:19], 11, v[16:17]
	v_lshl_add_u64 v[16:17], s[16:17], 0, v[18:19]
	v_lshl_add_u64 v[16:17], v[16:17], 0, v[6:7]
	v_pk_mul_f32 v[26:27], v[108:109], s[28:29] op_sel_hi:[1,0]
	v_pk_mul_f32 v[24:25], v[110:111], s[28:29] op_sel_hi:[1,0]
	v_pk_mul_f32 v[22:23], v[112:113], s[28:29] op_sel_hi:[1,0]
	s_waitcnt vmcnt(11)
	v_mov_b64_e32 v[2:3], v[214:215]
	v_mov_b64_e32 v[4:5], v[216:217]
	v_lshlrev_b32_e32 v9, 16, v2
	v_mul_f32_e32 v9, 0xbfb8aa3b, v9
	v_exp_f32_e32 v9, v9
	v_and_b32_e32 v2, 0xffff0000, v2
	v_mul_f32_e32 v2, 0xbfb8aa3b, v2
	v_exp_f32_e32 v2, v2
	v_add_f32_e32 v9, 1.0, v9
	v_add_f32_e32 v2, 1.0, v2
	v_lshlrev_b32_e32 v31, 16, v3
	v_mul_f32_e32 v31, 0xbfb8aa3b, v31
	v_rcp_f32_e32 v179, v9
	v_exp_f32_e32 v31, v31
	s_nop 0
	v_add_f32_e32 v31, 1.0, v31
	v_and_b32_e32 v3, 0xffff0000, v3
	v_mul_f32_e32 v3, 0xbfb8aa3b, v3
	v_rcp_f32_e32 v9, v2
	v_exp_f32_e32 v3, v3
	s_nop 0
	v_add_f32_e32 v3, 1.0, v3
	v_rcp_f32_e32 v107, v31
	v_lshlrev_b32_e32 v31, 16, v4
	v_mul_f32_e32 v31, 0xbfb8aa3b, v31
	v_exp_f32_e32 v31, v31
	s_nop 0
	v_add_f32_e32 v31, 1.0, v31
	v_and_b32_e32 v4, 0xffff0000, v4
	v_mul_f32_e32 v4, 0xbfb8aa3b, v4
	v_exp_f32_e32 v4, v4
	v_rcp_f32_e32 v106, v3
	v_add_f32_e32 v4, 1.0, v4
	v_rcp_f32_e32 v108, v31
	v_lshlrev_b32_e32 v31, 16, v5
	v_mul_f32_e32 v31, 0xbfb8aa3b, v31
	v_exp_f32_e32 v31, v31
	s_nop 0
	v_add_f32_e32 v30, 1.0, v31
	v_rcp_f32_e32 v109, v4
	v_and_b32_e32 v4, 0xffff0000, v5
	v_mul_f32_e32 v4, 0xbfb8aa3b, v4
	v_exp_f32_e32 v4, v4
	s_nop 0
	v_add_f32_e32 v4, 1.0, v4
	v_rcp_f32_e32 v110, v30
	v_mov_b32_e32 v33, v24
	v_rcp_f32_e32 v111, v4
	s_waitcnt vmcnt(10)
	v_mov_b64_e32 v[20:21], v[238:239]
	v_add_u32_e32 v250, 160, v8
	v_lshl_add_u32 v251, v250, 11, v6
	v_mad_u32_u24 v250, v250, s56, v12
	global_load_dwordx4 v[214:217], v250, s[18:19] nt
	global_load_dwordx2 v[238:239], v251, s[16:17] nt
	v_cvt_pk_f32_fp8_e32 v[2:3], v20
	v_cvt_pk_f32_fp8_sdwa v[4:5], v20 src0_sel:WORD_1
	v_cvt_pk_f32_fp8_e32 v[30:31], v21
	v_cvt_pk_f32_fp8_sdwa v[20:21], v21 src0_sel:WORD_1
	v_mov_b32_e32 v32, v2
	v_pk_mul_f32 v[32:33], v[32:33], v[178:179]
	v_mov_b32_e32 v24, v3
	v_mov_b32_e32 v179, v9
	v_pk_mul_f32 v[2:3], v[24:25], v[178:179]
	v_mov_b32_e32 v179, v107
	v_add_f32_e32 v9, v2, v3
	v_mov_b32_e32 v2, v4
	v_mov_b32_e32 v3, v22
	v_pk_mul_f32 v[2:3], v[2:3], v[178:179]
	v_mov_b32_e32 v22, v5
	v_mov_b32_e32 v179, v106
	v_add_f32_e32 v4, v2, v3
	v_pk_mul_f32 v[2:3], v[22:23], v[178:179]
	v_mov_b32_e32 v179, v108
	v_add_f32_e32 v5, v2, v3
	v_mov_b32_e32 v2, v30
	v_mov_b32_e32 v3, v28
	v_pk_mul_f32 v[2:3], v[2:3], v[178:179]
	v_mov_b32_e32 v28, v31
	v_mov_b32_e32 v179, v109
	v_add_f32_e32 v22, v2, v3
	v_pk_mul_f32 v[2:3], v[28:29], v[178:179]
	v_mov_b32_e32 v179, v110
	v_add_f32_e32 v23, v2, v3
	v_mov_b32_e32 v2, v20
	v_mov_b32_e32 v3, v26
	v_pk_mul_f32 v[2:3], v[2:3], v[178:179]
	v_mov_b32_e32 v26, v21
	v_mov_b32_e32 v179, v111
	v_add_f32_e32 v32, v32, v33
	v_add_f32_e32 v20, v2, v3
	v_pk_mul_f32 v[2:3], v[26:27], v[178:179]
	v_mul_f32_e32 v4, 0x41800000, v4
	v_add_f32_e32 v21, v2, v3
	v_mul_f32_e32 v2, 0x41800000, v32
	v_mul_f32_e32 v3, 0x41800000, v9
	v_med3_f32 v9, v2, s57, v207
	v_med3_f32 v3, v3, s57, v207
	v_mov_b32_e32 v2, v167
	v_cvt_pk_fp8_f32 v2, v9, v3
	v_mul_f32_e32 v3, 0x41800000, v5
	v_med3_f32 v4, v4, s57, v207
	v_med3_f32 v3, v3, s57, v207
	v_cvt_pk_fp8_f32 v2, v4, v3 op_sel:[0,0,1]
	v_mul_f32_e32 v3, 0x41800000, v22
	v_mul_f32_e32 v4, 0x41800000, v23
	v_med3_f32 v9, v3, s57, v207
	v_med3_f32 v4, v4, s57, v207
	v_mov_b32_e32 v3, v167
	v_cvt_pk_fp8_f32 v3, v9, v4
	v_mul_f32_e32 v5, 0x41800000, v20
	v_mul_f32_e32 v4, 0x41800000, v21
	v_med3_f32 v5, v5, s57, v207
	v_med3_f32 v4, v4, s57, v207
	v_cvt_pk_fp8_f32 v3, v5, v4 op_sel:[0,0,1]
	v_lshl_add_u64 v[4:5], s[20:21], 0, v[18:19]
	v_lshl_add_u64 v[18:19], v[4:5], 0, v[6:7]
	v_pk_mul_f32 v[24:25], v[98:99], s[28:29] op_sel_hi:[1,0]
	global_store_dwordx2 v[18:19], v[2:3], off
	s_nop 0
	v_pk_mul_f32 v[20:21], v[102:103], s[28:29] op_sel_hi:[1,0]
	v_pk_mul_f32 v[16:17], v[104:105], s[28:29] op_sel_hi:[1,0]
	v_pk_mul_f32 v[22:23], v[100:101], s[28:29] op_sel_hi:[1,0]
	s_waitcnt vmcnt(11)
	v_mov_b64_e32 v[2:3], v[218:219]
	v_mov_b64_e32 v[4:5], v[220:221]
	v_lshlrev_b32_e32 v9, 16, v2
	v_mul_f32_e32 v9, 0xbfb8aa3b, v9
	v_exp_f32_e32 v9, v9
	v_and_b32_e32 v2, 0xffff0000, v2
	v_mul_f32_e32 v2, 0xbfb8aa3b, v2
	v_exp_f32_e32 v2, v2
	v_add_f32_e32 v9, 1.0, v9
	v_add_f32_e32 v2, 1.0, v2
	v_lshlrev_b32_e32 v27, 16, v3
	v_mul_f32_e32 v27, 0xbfb8aa3b, v27
	v_rcp_f32_e32 v179, v9
	v_exp_f32_e32 v27, v27
	s_nop 0
	v_add_f32_e32 v27, 1.0, v27
	v_and_b32_e32 v3, 0xffff0000, v3
	v_mul_f32_e32 v3, 0xbfb8aa3b, v3
	v_rcp_f32_e32 v9, v2
	v_exp_f32_e32 v3, v3
	s_nop 0
	v_add_f32_e32 v3, 1.0, v3
	v_rcp_f32_e32 v31, v27
	v_lshlrev_b32_e32 v27, 16, v4
	v_mul_f32_e32 v27, 0xbfb8aa3b, v27
	v_exp_f32_e32 v27, v27
	s_nop 0
	v_add_f32_e32 v27, 1.0, v27
	v_and_b32_e32 v4, 0xffff0000, v4
	v_mul_f32_e32 v4, 0xbfb8aa3b, v4
	v_exp_f32_e32 v4, v4
	v_rcp_f32_e32 v30, v3
	v_add_f32_e32 v4, 1.0, v4
	v_rcp_f32_e32 v32, v27
	v_lshlrev_b32_e32 v27, 16, v5
	v_mul_f32_e32 v27, 0xbfb8aa3b, v27
	v_exp_f32_e32 v27, v27
	s_nop 0
	v_add_f32_e32 v26, 1.0, v27
	v_rcp_f32_e32 v33, v4
	v_and_b32_e32 v4, 0xffff0000, v5
	v_mul_f32_e32 v4, 0xbfb8aa3b, v4
	v_exp_f32_e32 v4, v4
	s_nop 0
	v_add_f32_e32 v4, 1.0, v4
	v_rcp_f32_e32 v98, v26
	v_mov_b32_e32 v29, v20
	v_rcp_f32_e32 v99, v4
	s_waitcnt vmcnt(10)
	v_mov_b64_e32 v[14:15], v[240:241]
	v_add_u32_e32 v250, 160, v8
	v_lshl_add_u32 v251, v250, 11, v6
	v_mad_u32_u24 v250, v250, s56, v12
	global_load_dwordx4 v[218:221], v250, s[18:19] offset:256 nt
	global_load_dwordx2 v[240:241], v251, s[16:17] offset:128 nt
	v_cvt_pk_f32_fp8_e32 v[2:3], v14
	v_cvt_pk_f32_fp8_sdwa v[4:5], v14 src0_sel:WORD_1
	v_cvt_pk_f32_fp8_e32 v[26:27], v15
	v_cvt_pk_f32_fp8_sdwa v[14:15], v15 src0_sel:WORD_1
	v_mov_b32_e32 v28, v2
	v_pk_mul_f32 v[28:29], v[28:29], v[178:179]
	v_mov_b32_e32 v20, v3
	v_mov_b32_e32 v179, v9
	v_pk_mul_f32 v[2:3], v[20:21], v[178:179]
	v_mov_b32_e32 v179, v31
	v_add_f32_e32 v9, v2, v3
	v_mov_b32_e32 v2, v4
	v_mov_b32_e32 v3, v16
	v_pk_mul_f32 v[2:3], v[2:3], v[178:179]
	v_mov_b32_e32 v16, v5
	v_mov_b32_e32 v179, v30
	v_add_f32_e32 v4, v2, v3
	v_pk_mul_f32 v[2:3], v[16:17], v[178:179]
	v_mov_b32_e32 v179, v32
	v_add_f32_e32 v5, v2, v3
	v_mov_b32_e32 v2, v26
	v_mov_b32_e32 v3, v24
	v_pk_mul_f32 v[2:3], v[2:3], v[178:179]
	v_mov_b32_e32 v24, v27
	v_mov_b32_e32 v179, v33
	v_add_f32_e32 v16, v2, v3
	v_pk_mul_f32 v[2:3], v[24:25], v[178:179]
	v_mov_b32_e32 v179, v98
	v_add_f32_e32 v17, v2, v3
	v_mov_b32_e32 v2, v14
	v_mov_b32_e32 v3, v22
	v_pk_mul_f32 v[2:3], v[2:3], v[178:179]
	v_mov_b32_e32 v22, v15
	v_mov_b32_e32 v179, v99
	v_add_f32_e32 v28, v28, v29
	v_add_f32_e32 v14, v2, v3
	v_pk_mul_f32 v[2:3], v[22:23], v[178:179]
	v_mul_f32_e32 v4, 0x41800000, v4
	v_add_f32_e32 v15, v2, v3
	v_mul_f32_e32 v2, 0x41800000, v28
	v_mul_f32_e32 v3, 0x41800000, v9
	v_med3_f32 v9, v2, s57, v207
	v_med3_f32 v3, v3, s57, v207
	v_mov_b32_e32 v2, v167
	v_cvt_pk_fp8_f32 v2, v9, v3
	v_mul_f32_e32 v3, 0x41800000, v5
	v_med3_f32 v4, v4, s57, v207
	v_med3_f32 v3, v3, s57, v207
	v_cvt_pk_fp8_f32 v2, v4, v3 op_sel:[0,0,1]
	v_mul_f32_e32 v3, 0x41800000, v16
	v_mul_f32_e32 v4, 0x41800000, v17
	v_med3_f32 v9, v3, s57, v207
	v_med3_f32 v4, v4, s57, v207
	v_mov_b32_e32 v3, v167
	v_cvt_pk_fp8_f32 v3, v9, v4
	v_mul_f32_e32 v5, 0x41800000, v14
	v_mul_f32_e32 v4, 0x41800000, v15
	v_med3_f32 v5, v5, s57, v207
	v_med3_f32 v4, v4, s57, v207
	v_cvt_pk_fp8_f32 v3, v5, v4 op_sel:[0,0,1]
	v_add_u32_e32 v16, 0x80, v8
	v_ashrrev_i32_e32 v17, 31, v16
	v_pk_mul_f32 v[28:29], v[90:91], s[28:29] op_sel_hi:[1,0]
	global_store_dwordx2 v[18:19], v[2:3], off offset:128
	v_mad_i64_i32 v[2:3], s[0:1], v16, s56, v[10:11]
	v_lshl_add_u64 v[14:15], v[2:3], 0, v[12:13]
	v_lshlrev_b64 v[18:19], 11, v[16:17]
	v_lshl_add_u64 v[16:17], s[16:17], 0, v[18:19]
	v_lshl_add_u64 v[16:17], v[16:17], 0, v[6:7]
	v_pk_mul_f32 v[26:27], v[92:93], s[28:29] op_sel_hi:[1,0]
	v_pk_mul_f32 v[24:25], v[94:95], s[28:29] op_sel_hi:[1,0]
	v_pk_mul_f32 v[22:23], v[96:97], s[28:29] op_sel_hi:[1,0]
	s_waitcnt vmcnt(11)
	v_mov_b64_e32 v[2:3], v[222:223]
	v_mov_b64_e32 v[4:5], v[224:225]
	v_lshlrev_b32_e32 v9, 16, v2
	v_mul_f32_e32 v9, 0xbfb8aa3b, v9
	v_exp_f32_e32 v9, v9
	v_and_b32_e32 v2, 0xffff0000, v2
	v_mul_f32_e32 v2, 0xbfb8aa3b, v2
	v_exp_f32_e32 v2, v2
	v_add_f32_e32 v9, 1.0, v9
	v_add_f32_e32 v2, 1.0, v2
	v_lshlrev_b32_e32 v31, 16, v3
	v_mul_f32_e32 v31, 0xbfb8aa3b, v31
	v_rcp_f32_e32 v179, v9
	v_exp_f32_e32 v31, v31
	s_nop 0
	v_add_f32_e32 v31, 1.0, v31
	v_and_b32_e32 v3, 0xffff0000, v3
	v_mul_f32_e32 v3, 0xbfb8aa3b, v3
	v_rcp_f32_e32 v9, v2
	v_exp_f32_e32 v3, v3
	s_nop 0
	v_add_f32_e32 v3, 1.0, v3
	v_rcp_f32_e32 v91, v31
	v_lshlrev_b32_e32 v31, 16, v4
	v_mul_f32_e32 v31, 0xbfb8aa3b, v31
	v_exp_f32_e32 v31, v31
	s_nop 0
	v_add_f32_e32 v31, 1.0, v31
	v_and_b32_e32 v4, 0xffff0000, v4
	v_mul_f32_e32 v4, 0xbfb8aa3b, v4
	v_exp_f32_e32 v4, v4
	v_rcp_f32_e32 v90, v3
	v_add_f32_e32 v4, 1.0, v4
	v_rcp_f32_e32 v92, v31
	v_lshlrev_b32_e32 v31, 16, v5
	v_mul_f32_e32 v31, 0xbfb8aa3b, v31
	v_exp_f32_e32 v31, v31
	s_nop 0
	v_add_f32_e32 v30, 1.0, v31
	v_rcp_f32_e32 v93, v4
	v_and_b32_e32 v4, 0xffff0000, v5
	v_mul_f32_e32 v4, 0xbfb8aa3b, v4
	v_exp_f32_e32 v4, v4
	s_nop 0
	v_add_f32_e32 v4, 1.0, v4
	v_rcp_f32_e32 v94, v30
	v_mov_b32_e32 v33, v24
	v_rcp_f32_e32 v95, v4
	s_waitcnt vmcnt(10)
	v_mov_b64_e32 v[20:21], v[242:243]
	v_add_u32_e32 v250, 176, v8
	v_lshl_add_u32 v251, v250, 11, v6
	v_mad_u32_u24 v250, v250, s56, v12
	global_load_dwordx4 v[222:225], v250, s[18:19] nt
	global_load_dwordx2 v[242:243], v251, s[16:17] nt
	v_cvt_pk_f32_fp8_e32 v[2:3], v20
	v_cvt_pk_f32_fp8_sdwa v[4:5], v20 src0_sel:WORD_1
	v_cvt_pk_f32_fp8_e32 v[30:31], v21
	v_cvt_pk_f32_fp8_sdwa v[20:21], v21 src0_sel:WORD_1
	v_mov_b32_e32 v32, v2
	v_pk_mul_f32 v[32:33], v[32:33], v[178:179]
	v_mov_b32_e32 v24, v3
	v_mov_b32_e32 v179, v9
	v_pk_mul_f32 v[2:3], v[24:25], v[178:179]
	v_mov_b32_e32 v179, v91
	v_add_f32_e32 v9, v2, v3
	v_mov_b32_e32 v2, v4
	v_mov_b32_e32 v3, v22
	v_pk_mul_f32 v[2:3], v[2:3], v[178:179]
	v_mov_b32_e32 v22, v5
	v_mov_b32_e32 v179, v90
	v_add_f32_e32 v4, v2, v3
	v_pk_mul_f32 v[2:3], v[22:23], v[178:179]
	v_mov_b32_e32 v179, v92
	v_add_f32_e32 v5, v2, v3
	v_mov_b32_e32 v2, v30
	v_mov_b32_e32 v3, v28
	v_pk_mul_f32 v[2:3], v[2:3], v[178:179]
	v_mov_b32_e32 v28, v31
	v_mov_b32_e32 v179, v93
	v_add_f32_e32 v22, v2, v3
	v_pk_mul_f32 v[2:3], v[28:29], v[178:179]
	v_mov_b32_e32 v179, v94
	v_add_f32_e32 v23, v2, v3
	v_mov_b32_e32 v2, v20
	v_mov_b32_e32 v3, v26
	v_pk_mul_f32 v[2:3], v[2:3], v[178:179]
	v_mov_b32_e32 v26, v21
	v_mov_b32_e32 v179, v95
	v_add_f32_e32 v32, v32, v33
	v_add_f32_e32 v20, v2, v3
	v_pk_mul_f32 v[2:3], v[26:27], v[178:179]
	v_mul_f32_e32 v4, 0x41800000, v4
	v_add_f32_e32 v21, v2, v3
	v_mul_f32_e32 v2, 0x41800000, v32
	v_mul_f32_e32 v3, 0x41800000, v9
	v_med3_f32 v9, v2, s57, v207
	v_med3_f32 v3, v3, s57, v207
	v_mov_b32_e32 v2, v167
	v_cvt_pk_fp8_f32 v2, v9, v3
	v_mul_f32_e32 v3, 0x41800000, v5
	v_med3_f32 v4, v4, s57, v207
	v_med3_f32 v3, v3, s57, v207
	v_cvt_pk_fp8_f32 v2, v4, v3 op_sel:[0,0,1]
	v_mul_f32_e32 v3, 0x41800000, v22
	v_mul_f32_e32 v4, 0x41800000, v23
	v_med3_f32 v9, v3, s57, v207
	v_med3_f32 v4, v4, s57, v207
	v_mov_b32_e32 v3, v167
	v_cvt_pk_fp8_f32 v3, v9, v4
	v_mul_f32_e32 v5, 0x41800000, v20
	v_mul_f32_e32 v4, 0x41800000, v21
	v_med3_f32 v5, v5, s57, v207
	v_med3_f32 v4, v4, s57, v207
	v_cvt_pk_fp8_f32 v3, v5, v4 op_sel:[0,0,1]
	v_lshl_add_u64 v[4:5], s[20:21], 0, v[18:19]
	v_lshl_add_u64 v[18:19], v[4:5], 0, v[6:7]
	v_pk_mul_f32 v[24:25], v[82:83], s[28:29] op_sel_hi:[1,0]
	global_store_dwordx2 v[18:19], v[2:3], off
	s_nop 0
	v_pk_mul_f32 v[20:21], v[86:87], s[28:29] op_sel_hi:[1,0]
	v_pk_mul_f32 v[16:17], v[88:89], s[28:29] op_sel_hi:[1,0]
	v_pk_mul_f32 v[22:23], v[84:85], s[28:29] op_sel_hi:[1,0]
	s_waitcnt vmcnt(11)
	v_mov_b64_e32 v[2:3], v[226:227]
	v_mov_b64_e32 v[4:5], v[228:229]
	v_lshlrev_b32_e32 v9, 16, v2
	v_mul_f32_e32 v9, 0xbfb8aa3b, v9
	v_exp_f32_e32 v9, v9
	v_and_b32_e32 v2, 0xffff0000, v2
	v_mul_f32_e32 v2, 0xbfb8aa3b, v2
	v_exp_f32_e32 v2, v2
	v_add_f32_e32 v9, 1.0, v9
	v_add_f32_e32 v2, 1.0, v2
	v_lshlrev_b32_e32 v27, 16, v3
	v_mul_f32_e32 v27, 0xbfb8aa3b, v27
	v_rcp_f32_e32 v179, v9
	v_exp_f32_e32 v27, v27
	s_nop 0
	v_add_f32_e32 v27, 1.0, v27
	v_and_b32_e32 v3, 0xffff0000, v3
	v_mul_f32_e32 v3, 0xbfb8aa3b, v3
	v_rcp_f32_e32 v9, v2
	v_exp_f32_e32 v3, v3
	s_nop 0
	v_add_f32_e32 v3, 1.0, v3
	v_rcp_f32_e32 v31, v27
	v_lshlrev_b32_e32 v27, 16, v4
	v_mul_f32_e32 v27, 0xbfb8aa3b, v27
	v_exp_f32_e32 v27, v27
	s_nop 0
	v_add_f32_e32 v27, 1.0, v27
	v_and_b32_e32 v4, 0xffff0000, v4
	v_mul_f32_e32 v4, 0xbfb8aa3b, v4
	v_exp_f32_e32 v4, v4
	v_rcp_f32_e32 v30, v3
	v_add_f32_e32 v4, 1.0, v4
	v_rcp_f32_e32 v32, v27
	v_lshlrev_b32_e32 v27, 16, v5
	v_mul_f32_e32 v27, 0xbfb8aa3b, v27
	v_exp_f32_e32 v27, v27
	s_nop 0
	v_add_f32_e32 v26, 1.0, v27
	v_rcp_f32_e32 v33, v4
	v_and_b32_e32 v4, 0xffff0000, v5
	v_mul_f32_e32 v4, 0xbfb8aa3b, v4
	v_exp_f32_e32 v4, v4
	s_nop 0
	v_add_f32_e32 v4, 1.0, v4
	v_rcp_f32_e32 v82, v26
	v_mov_b32_e32 v29, v20
	v_rcp_f32_e32 v83, v4
	s_waitcnt vmcnt(10)
	v_mov_b64_e32 v[14:15], v[244:245]
	v_add_u32_e32 v250, 176, v8
	v_lshl_add_u32 v251, v250, 11, v6
	v_mad_u32_u24 v250, v250, s56, v12
	global_load_dwordx4 v[226:229], v250, s[18:19] offset:256 nt
	global_load_dwordx2 v[244:245], v251, s[16:17] offset:128 nt
	v_cvt_pk_f32_fp8_e32 v[2:3], v14
	v_cvt_pk_f32_fp8_sdwa v[4:5], v14 src0_sel:WORD_1
	v_cvt_pk_f32_fp8_e32 v[26:27], v15
	v_cvt_pk_f32_fp8_sdwa v[14:15], v15 src0_sel:WORD_1
	v_mov_b32_e32 v28, v2
	v_pk_mul_f32 v[28:29], v[28:29], v[178:179]
	v_mov_b32_e32 v20, v3
	v_mov_b32_e32 v179, v9
	v_pk_mul_f32 v[2:3], v[20:21], v[178:179]
	v_mov_b32_e32 v179, v31
	v_add_f32_e32 v9, v2, v3
	v_mov_b32_e32 v2, v4
	v_mov_b32_e32 v3, v16
	v_pk_mul_f32 v[2:3], v[2:3], v[178:179]
	v_mov_b32_e32 v16, v5
	v_mov_b32_e32 v179, v30
	v_add_f32_e32 v4, v2, v3
	v_pk_mul_f32 v[2:3], v[16:17], v[178:179]
	v_mov_b32_e32 v179, v32
	v_add_f32_e32 v5, v2, v3
	v_mov_b32_e32 v2, v26
	v_mov_b32_e32 v3, v24
	v_pk_mul_f32 v[2:3], v[2:3], v[178:179]
	v_mov_b32_e32 v24, v27
	v_mov_b32_e32 v179, v33
	v_add_f32_e32 v16, v2, v3
	v_pk_mul_f32 v[2:3], v[24:25], v[178:179]
	v_mov_b32_e32 v179, v82
	v_add_f32_e32 v17, v2, v3
	v_mov_b32_e32 v2, v14
	v_mov_b32_e32 v3, v22
	v_pk_mul_f32 v[2:3], v[2:3], v[178:179]
	v_mov_b32_e32 v22, v15
	v_mov_b32_e32 v179, v83
	v_add_f32_e32 v28, v28, v29
	v_add_f32_e32 v14, v2, v3
	v_pk_mul_f32 v[2:3], v[22:23], v[178:179]
	v_mul_f32_e32 v4, 0x41800000, v4
	v_add_f32_e32 v15, v2, v3
	v_mul_f32_e32 v2, 0x41800000, v28
	v_mul_f32_e32 v3, 0x41800000, v9
	v_med3_f32 v9, v2, s57, v207
	v_med3_f32 v3, v3, s57, v207
	v_mov_b32_e32 v2, v167
	v_cvt_pk_fp8_f32 v2, v9, v3
	v_mul_f32_e32 v3, 0x41800000, v5
	v_med3_f32 v4, v4, s57, v207
	v_med3_f32 v3, v3, s57, v207
	v_cvt_pk_fp8_f32 v2, v4, v3 op_sel:[0,0,1]
	v_mul_f32_e32 v3, 0x41800000, v16
	v_mul_f32_e32 v4, 0x41800000, v17
	v_med3_f32 v9, v3, s57, v207
	v_med3_f32 v4, v4, s57, v207
	v_mov_b32_e32 v3, v167
	v_cvt_pk_fp8_f32 v3, v9, v4
	v_mul_f32_e32 v5, 0x41800000, v14
	v_mul_f32_e32 v4, 0x41800000, v15
	v_med3_f32 v5, v5, s57, v207
	v_med3_f32 v4, v4, s57, v207
	v_cvt_pk_fp8_f32 v3, v5, v4 op_sel:[0,0,1]
	v_add_u32_e32 v16, 0x90, v8
	v_ashrrev_i32_e32 v17, 31, v16
	v_pk_mul_f32 v[28:29], v[74:75], s[28:29] op_sel_hi:[1,0]
	global_store_dwordx2 v[18:19], v[2:3], off offset:128
	v_mad_i64_i32 v[2:3], s[0:1], v16, s56, v[10:11]
	v_lshl_add_u64 v[14:15], v[2:3], 0, v[12:13]
	v_lshlrev_b64 v[18:19], 11, v[16:17]
	v_lshl_add_u64 v[16:17], s[16:17], 0, v[18:19]
	v_lshl_add_u64 v[16:17], v[16:17], 0, v[6:7]
	v_pk_mul_f32 v[26:27], v[76:77], s[28:29] op_sel_hi:[1,0]
	v_pk_mul_f32 v[24:25], v[78:79], s[28:29] op_sel_hi:[1,0]
	v_pk_mul_f32 v[22:23], v[80:81], s[28:29] op_sel_hi:[1,0]
	s_waitcnt vmcnt(11)
	v_mov_b64_e32 v[2:3], v[230:231]
	v_mov_b64_e32 v[4:5], v[232:233]
	v_lshlrev_b32_e32 v9, 16, v2
	v_mul_f32_e32 v9, 0xbfb8aa3b, v9
	v_exp_f32_e32 v9, v9
	v_and_b32_e32 v2, 0xffff0000, v2
	v_mul_f32_e32 v2, 0xbfb8aa3b, v2
	v_exp_f32_e32 v2, v2
	v_add_f32_e32 v9, 1.0, v9
	v_add_f32_e32 v2, 1.0, v2
	v_lshlrev_b32_e32 v31, 16, v3
	v_mul_f32_e32 v31, 0xbfb8aa3b, v31
	v_rcp_f32_e32 v179, v9
	v_exp_f32_e32 v31, v31
	s_nop 0
	v_add_f32_e32 v31, 1.0, v31
	v_and_b32_e32 v3, 0xffff0000, v3
	v_mul_f32_e32 v3, 0xbfb8aa3b, v3
	v_rcp_f32_e32 v9, v2
	v_exp_f32_e32 v3, v3
	s_nop 0
	v_add_f32_e32 v3, 1.0, v3
	v_rcp_f32_e32 v75, v31
	v_lshlrev_b32_e32 v31, 16, v4
	v_mul_f32_e32 v31, 0xbfb8aa3b, v31
	v_exp_f32_e32 v31, v31
	s_nop 0
	v_add_f32_e32 v31, 1.0, v31
	v_and_b32_e32 v4, 0xffff0000, v4
	v_mul_f32_e32 v4, 0xbfb8aa3b, v4
	v_exp_f32_e32 v4, v4
	v_rcp_f32_e32 v74, v3
	v_add_f32_e32 v4, 1.0, v4
	v_rcp_f32_e32 v76, v31
	v_lshlrev_b32_e32 v31, 16, v5
	v_mul_f32_e32 v31, 0xbfb8aa3b, v31
	v_exp_f32_e32 v31, v31
	s_nop 0
	v_add_f32_e32 v30, 1.0, v31
	v_rcp_f32_e32 v77, v4
	v_and_b32_e32 v4, 0xffff0000, v5
	v_mul_f32_e32 v4, 0xbfb8aa3b, v4
	v_exp_f32_e32 v4, v4
	s_nop 0
	v_add_f32_e32 v4, 1.0, v4
	v_rcp_f32_e32 v78, v30
	v_mov_b32_e32 v33, v24
	v_rcp_f32_e32 v79, v4
	s_waitcnt vmcnt(10)
	v_mov_b64_e32 v[20:21], v[246:247]
	v_cvt_pk_f32_fp8_e32 v[2:3], v20
	v_cvt_pk_f32_fp8_sdwa v[4:5], v20 src0_sel:WORD_1
	v_cvt_pk_f32_fp8_e32 v[30:31], v21
	v_cvt_pk_f32_fp8_sdwa v[20:21], v21 src0_sel:WORD_1
	v_mov_b32_e32 v32, v2
	v_pk_mul_f32 v[32:33], v[32:33], v[178:179]
	v_mov_b32_e32 v24, v3
	v_mov_b32_e32 v179, v9
	v_pk_mul_f32 v[2:3], v[24:25], v[178:179]
	v_mov_b32_e32 v179, v75
	v_add_f32_e32 v9, v2, v3
	v_mov_b32_e32 v2, v4
	v_mov_b32_e32 v3, v22
	v_pk_mul_f32 v[2:3], v[2:3], v[178:179]
	v_mov_b32_e32 v22, v5
	v_mov_b32_e32 v179, v74
	v_add_f32_e32 v4, v2, v3
	v_pk_mul_f32 v[2:3], v[22:23], v[178:179]
	v_mov_b32_e32 v179, v76
	v_add_f32_e32 v5, v2, v3
	v_mov_b32_e32 v2, v30
	v_mov_b32_e32 v3, v28
	v_pk_mul_f32 v[2:3], v[2:3], v[178:179]
	v_mov_b32_e32 v28, v31
	v_mov_b32_e32 v179, v77
	v_add_f32_e32 v22, v2, v3
	v_pk_mul_f32 v[2:3], v[28:29], v[178:179]
	v_mov_b32_e32 v179, v78
	v_add_f32_e32 v23, v2, v3
	v_mov_b32_e32 v2, v20
	v_mov_b32_e32 v3, v26
	v_pk_mul_f32 v[2:3], v[2:3], v[178:179]
	v_mov_b32_e32 v26, v21
	v_mov_b32_e32 v179, v79
	v_add_f32_e32 v32, v32, v33
	v_add_f32_e32 v20, v2, v3
	v_pk_mul_f32 v[2:3], v[26:27], v[178:179]
	v_mul_f32_e32 v4, 0x41800000, v4
	v_add_f32_e32 v21, v2, v3
	v_mul_f32_e32 v2, 0x41800000, v32
	v_mul_f32_e32 v3, 0x41800000, v9
	v_med3_f32 v9, v2, s57, v207
	v_med3_f32 v3, v3, s57, v207
	v_mov_b32_e32 v2, v167
	v_cvt_pk_fp8_f32 v2, v9, v3
	v_mul_f32_e32 v3, 0x41800000, v5
	v_med3_f32 v4, v4, s57, v207
	v_med3_f32 v3, v3, s57, v207
	v_cvt_pk_fp8_f32 v2, v4, v3 op_sel:[0,0,1]
	v_mul_f32_e32 v3, 0x41800000, v22
	v_mul_f32_e32 v4, 0x41800000, v23
	v_med3_f32 v9, v3, s57, v207
	v_med3_f32 v4, v4, s57, v207
	v_mov_b32_e32 v3, v167
	v_cvt_pk_fp8_f32 v3, v9, v4
	v_mul_f32_e32 v5, 0x41800000, v20
	v_mul_f32_e32 v4, 0x41800000, v21
	v_med3_f32 v5, v5, s57, v207
	v_med3_f32 v4, v4, s57, v207
	v_cvt_pk_fp8_f32 v3, v5, v4 op_sel:[0,0,1]
	v_lshl_add_u64 v[4:5], s[20:21], 0, v[18:19]
	v_lshl_add_u64 v[18:19], v[4:5], 0, v[6:7]
	v_pk_mul_f32 v[24:25], v[66:67], s[28:29] op_sel_hi:[1,0]
	global_store_dwordx2 v[18:19], v[2:3], off
	s_nop 0
	v_pk_mul_f32 v[20:21], v[70:71], s[28:29] op_sel_hi:[1,0]
	v_pk_mul_f32 v[16:17], v[72:73], s[28:29] op_sel_hi:[1,0]
	v_pk_mul_f32 v[22:23], v[68:69], s[28:29] op_sel_hi:[1,0]
	s_waitcnt vmcnt(9)
	v_mov_b64_e32 v[2:3], v[234:235]
	v_mov_b64_e32 v[4:5], v[236:237]
	v_lshlrev_b32_e32 v9, 16, v2
	v_mul_f32_e32 v9, 0xbfb8aa3b, v9
	v_exp_f32_e32 v9, v9
	v_and_b32_e32 v2, 0xffff0000, v2
	v_mul_f32_e32 v2, 0xbfb8aa3b, v2
	v_exp_f32_e32 v2, v2
	v_add_f32_e32 v9, 1.0, v9
	v_add_f32_e32 v2, 1.0, v2
	v_lshlrev_b32_e32 v27, 16, v3
	v_mul_f32_e32 v27, 0xbfb8aa3b, v27
	v_rcp_f32_e32 v179, v9
	v_exp_f32_e32 v27, v27
	s_nop 0
	v_add_f32_e32 v27, 1.0, v27
	v_and_b32_e32 v3, 0xffff0000, v3
	v_mul_f32_e32 v3, 0xbfb8aa3b, v3
	v_rcp_f32_e32 v9, v2
	v_exp_f32_e32 v3, v3
	s_nop 0
	v_add_f32_e32 v3, 1.0, v3
	v_rcp_f32_e32 v31, v27
	v_lshlrev_b32_e32 v27, 16, v4
	v_mul_f32_e32 v27, 0xbfb8aa3b, v27
	v_exp_f32_e32 v27, v27
	s_nop 0
	v_add_f32_e32 v27, 1.0, v27
	v_and_b32_e32 v4, 0xffff0000, v4
	v_mul_f32_e32 v4, 0xbfb8aa3b, v4
	v_exp_f32_e32 v4, v4
	v_rcp_f32_e32 v30, v3
	v_add_f32_e32 v4, 1.0, v4
	v_rcp_f32_e32 v32, v27
	v_lshlrev_b32_e32 v27, 16, v5
	v_mul_f32_e32 v27, 0xbfb8aa3b, v27
	v_exp_f32_e32 v27, v27
	s_nop 0
	v_add_f32_e32 v26, 1.0, v27
	v_rcp_f32_e32 v33, v4
	v_and_b32_e32 v4, 0xffff0000, v5
	v_mul_f32_e32 v4, 0xbfb8aa3b, v4
	v_exp_f32_e32 v4, v4
	s_nop 0
	v_add_f32_e32 v4, 1.0, v4
	v_rcp_f32_e32 v66, v26
	v_mov_b32_e32 v29, v20
	v_rcp_f32_e32 v67, v4
	s_waitcnt vmcnt(8)
	v_mov_b64_e32 v[14:15], v[248:249]
	v_cvt_pk_f32_fp8_e32 v[2:3], v14
	v_cvt_pk_f32_fp8_sdwa v[4:5], v14 src0_sel:WORD_1
	v_cvt_pk_f32_fp8_e32 v[26:27], v15
	v_cvt_pk_f32_fp8_sdwa v[14:15], v15 src0_sel:WORD_1
	v_mov_b32_e32 v28, v2
	v_pk_mul_f32 v[28:29], v[28:29], v[178:179]
	v_mov_b32_e32 v20, v3
	v_mov_b32_e32 v179, v9
	v_pk_mul_f32 v[2:3], v[20:21], v[178:179]
	v_mov_b32_e32 v179, v31
	v_add_f32_e32 v9, v2, v3
	v_mov_b32_e32 v2, v4
	v_mov_b32_e32 v3, v16
	v_pk_mul_f32 v[2:3], v[2:3], v[178:179]
	v_mov_b32_e32 v16, v5
	v_mov_b32_e32 v179, v30
	v_add_f32_e32 v4, v2, v3
	v_pk_mul_f32 v[2:3], v[16:17], v[178:179]
	v_mov_b32_e32 v179, v32
	v_add_f32_e32 v5, v2, v3
	v_mov_b32_e32 v2, v26
	v_mov_b32_e32 v3, v24
	v_pk_mul_f32 v[2:3], v[2:3], v[178:179]
	v_mov_b32_e32 v24, v27
	v_mov_b32_e32 v179, v33
	v_add_f32_e32 v16, v2, v3
	v_pk_mul_f32 v[2:3], v[24:25], v[178:179]
	v_mov_b32_e32 v179, v66
	v_add_f32_e32 v17, v2, v3
	v_mov_b32_e32 v2, v14
	v_mov_b32_e32 v3, v22
	v_pk_mul_f32 v[2:3], v[2:3], v[178:179]
	v_mov_b32_e32 v22, v15
	v_mov_b32_e32 v179, v67
	v_add_f32_e32 v28, v28, v29
	v_add_f32_e32 v14, v2, v3
	v_pk_mul_f32 v[2:3], v[22:23], v[178:179]
	v_mul_f32_e32 v4, 0x41800000, v4
	v_add_f32_e32 v15, v2, v3
	v_mul_f32_e32 v2, 0x41800000, v28
	v_mul_f32_e32 v3, 0x41800000, v9
	v_med3_f32 v9, v2, s57, v207
	v_med3_f32 v3, v3, s57, v207
	v_mov_b32_e32 v2, v167
	v_cvt_pk_fp8_f32 v2, v9, v3
	v_mul_f32_e32 v3, 0x41800000, v5
	v_med3_f32 v4, v4, s57, v207
	v_med3_f32 v3, v3, s57, v207
	v_cvt_pk_fp8_f32 v2, v4, v3 op_sel:[0,0,1]
	v_mul_f32_e32 v3, 0x41800000, v16
	v_mul_f32_e32 v4, 0x41800000, v17
	v_med3_f32 v9, v3, s57, v207
	v_med3_f32 v4, v4, s57, v207
	v_mov_b32_e32 v3, v167
	v_cvt_pk_fp8_f32 v3, v9, v4
	v_mul_f32_e32 v5, 0x41800000, v14
	v_mul_f32_e32 v4, 0x41800000, v15
	v_med3_f32 v5, v5, s57, v207
	v_med3_f32 v4, v4, s57, v207
	v_cvt_pk_fp8_f32 v3, v5, v4 op_sel:[0,0,1]
	v_add_u32_e32 v16, 0xa0, v8
	v_ashrrev_i32_e32 v17, 31, v16
	v_pk_mul_f32 v[28:29], v[58:59], s[28:29] op_sel_hi:[1,0]
	global_store_dwordx2 v[18:19], v[2:3], off offset:128
	v_mad_i64_i32 v[2:3], s[0:1], v16, s56, v[10:11]
	v_lshl_add_u64 v[14:15], v[2:3], 0, v[12:13]
	v_lshlrev_b64 v[18:19], 11, v[16:17]
	v_lshl_add_u64 v[16:17], s[16:17], 0, v[18:19]
	v_lshl_add_u64 v[16:17], v[16:17], 0, v[6:7]
	v_pk_mul_f32 v[26:27], v[60:61], s[28:29] op_sel_hi:[1,0]
	v_pk_mul_f32 v[24:25], v[62:63], s[28:29] op_sel_hi:[1,0]
	v_pk_mul_f32 v[22:23], v[64:65], s[28:29] op_sel_hi:[1,0]
	s_waitcnt vmcnt(7)
	v_mov_b64_e32 v[2:3], v[214:215]
	v_mov_b64_e32 v[4:5], v[216:217]
	v_lshlrev_b32_e32 v9, 16, v2
	v_mul_f32_e32 v9, 0xbfb8aa3b, v9
	v_exp_f32_e32 v9, v9
	v_and_b32_e32 v2, 0xffff0000, v2
	v_mul_f32_e32 v2, 0xbfb8aa3b, v2
	v_exp_f32_e32 v2, v2
	v_add_f32_e32 v9, 1.0, v9
	v_add_f32_e32 v2, 1.0, v2
	v_lshlrev_b32_e32 v31, 16, v3
	v_mul_f32_e32 v31, 0xbfb8aa3b, v31
	v_rcp_f32_e32 v179, v9
	v_exp_f32_e32 v31, v31
	s_nop 0
	v_add_f32_e32 v31, 1.0, v31
	v_and_b32_e32 v3, 0xffff0000, v3
	v_mul_f32_e32 v3, 0xbfb8aa3b, v3
	v_rcp_f32_e32 v9, v2
	v_exp_f32_e32 v3, v3
	s_nop 0
	v_add_f32_e32 v3, 1.0, v3
	v_rcp_f32_e32 v59, v31
	v_lshlrev_b32_e32 v31, 16, v4
	v_mul_f32_e32 v31, 0xbfb8aa3b, v31
	v_exp_f32_e32 v31, v31
	s_nop 0
	v_add_f32_e32 v31, 1.0, v31
	v_and_b32_e32 v4, 0xffff0000, v4
	v_mul_f32_e32 v4, 0xbfb8aa3b, v4
	v_exp_f32_e32 v4, v4
	v_rcp_f32_e32 v58, v3
	v_add_f32_e32 v4, 1.0, v4
	v_rcp_f32_e32 v60, v31
	v_lshlrev_b32_e32 v31, 16, v5
	v_mul_f32_e32 v31, 0xbfb8aa3b, v31
	v_exp_f32_e32 v31, v31
	s_nop 0
	v_add_f32_e32 v30, 1.0, v31
	v_rcp_f32_e32 v61, v4
	v_and_b32_e32 v4, 0xffff0000, v5
	v_mul_f32_e32 v4, 0xbfb8aa3b, v4
	v_exp_f32_e32 v4, v4
	s_nop 0
	v_add_f32_e32 v4, 1.0, v4
	v_rcp_f32_e32 v62, v30
	v_mov_b32_e32 v33, v24
	v_rcp_f32_e32 v63, v4
	s_waitcnt vmcnt(6)
	v_mov_b64_e32 v[20:21], v[238:239]
	v_cvt_pk_f32_fp8_e32 v[2:3], v20
	v_cvt_pk_f32_fp8_sdwa v[4:5], v20 src0_sel:WORD_1
	v_cvt_pk_f32_fp8_e32 v[30:31], v21
	v_cvt_pk_f32_fp8_sdwa v[20:21], v21 src0_sel:WORD_1
	v_mov_b32_e32 v32, v2
	v_pk_mul_f32 v[32:33], v[32:33], v[178:179]
	v_mov_b32_e32 v24, v3
	v_mov_b32_e32 v179, v9
	v_pk_mul_f32 v[2:3], v[24:25], v[178:179]
	v_mov_b32_e32 v179, v59
	v_add_f32_e32 v9, v2, v3
	v_mov_b32_e32 v2, v4
	v_mov_b32_e32 v3, v22
	v_pk_mul_f32 v[2:3], v[2:3], v[178:179]
	v_mov_b32_e32 v22, v5
	v_mov_b32_e32 v179, v58
	v_add_f32_e32 v4, v2, v3
	v_pk_mul_f32 v[2:3], v[22:23], v[178:179]
	v_mov_b32_e32 v179, v60
	v_add_f32_e32 v5, v2, v3
	v_mov_b32_e32 v2, v30
	v_mov_b32_e32 v3, v28
	v_pk_mul_f32 v[2:3], v[2:3], v[178:179]
	v_mov_b32_e32 v28, v31
	v_mov_b32_e32 v179, v61
	v_add_f32_e32 v22, v2, v3
	v_pk_mul_f32 v[2:3], v[28:29], v[178:179]
	v_mov_b32_e32 v179, v62
	v_add_f32_e32 v23, v2, v3
	v_mov_b32_e32 v2, v20
	v_mov_b32_e32 v3, v26
	v_pk_mul_f32 v[2:3], v[2:3], v[178:179]
	v_mov_b32_e32 v26, v21
	v_mov_b32_e32 v179, v63
	v_add_f32_e32 v32, v32, v33
	v_add_f32_e32 v20, v2, v3
	v_pk_mul_f32 v[2:3], v[26:27], v[178:179]
	v_mul_f32_e32 v4, 0x41800000, v4
	v_add_f32_e32 v21, v2, v3
	v_mul_f32_e32 v2, 0x41800000, v32
	v_mul_f32_e32 v3, 0x41800000, v9
	v_med3_f32 v9, v2, s57, v207
	v_med3_f32 v3, v3, s57, v207
	v_mov_b32_e32 v2, v167
	v_cvt_pk_fp8_f32 v2, v9, v3
	v_mul_f32_e32 v3, 0x41800000, v5
	v_med3_f32 v4, v4, s57, v207
	v_med3_f32 v3, v3, s57, v207
	v_cvt_pk_fp8_f32 v2, v4, v3 op_sel:[0,0,1]
	v_mul_f32_e32 v3, 0x41800000, v22
	v_mul_f32_e32 v4, 0x41800000, v23
	v_med3_f32 v9, v3, s57, v207
	v_med3_f32 v4, v4, s57, v207
	v_mov_b32_e32 v3, v167
	v_cvt_pk_fp8_f32 v3, v9, v4
	v_mul_f32_e32 v5, 0x41800000, v20
	v_mul_f32_e32 v4, 0x41800000, v21
	v_med3_f32 v5, v5, s57, v207
	v_med3_f32 v4, v4, s57, v207
	v_cvt_pk_fp8_f32 v3, v5, v4 op_sel:[0,0,1]
	v_lshl_add_u64 v[4:5], s[20:21], 0, v[18:19]
	v_lshl_add_u64 v[18:19], v[4:5], 0, v[6:7]
	v_pk_mul_f32 v[24:25], v[50:51], s[28:29] op_sel_hi:[1,0]
	global_store_dwordx2 v[18:19], v[2:3], off
	s_nop 0
	v_pk_mul_f32 v[20:21], v[54:55], s[28:29] op_sel_hi:[1,0]
	v_pk_mul_f32 v[16:17], v[56:57], s[28:29] op_sel_hi:[1,0]
	v_pk_mul_f32 v[22:23], v[52:53], s[28:29] op_sel_hi:[1,0]
	s_waitcnt vmcnt(5)
	v_mov_b64_e32 v[2:3], v[218:219]
	v_mov_b64_e32 v[4:5], v[220:221]
	v_lshlrev_b32_e32 v9, 16, v2
	v_mul_f32_e32 v9, 0xbfb8aa3b, v9
	v_exp_f32_e32 v9, v9
	v_and_b32_e32 v2, 0xffff0000, v2
	v_mul_f32_e32 v2, 0xbfb8aa3b, v2
	v_exp_f32_e32 v2, v2
	v_add_f32_e32 v9, 1.0, v9
	v_add_f32_e32 v2, 1.0, v2
	v_lshlrev_b32_e32 v27, 16, v3
	v_mul_f32_e32 v27, 0xbfb8aa3b, v27
	v_rcp_f32_e32 v179, v9
	v_exp_f32_e32 v27, v27
	s_nop 0
	v_add_f32_e32 v27, 1.0, v27
	v_and_b32_e32 v3, 0xffff0000, v3
	v_mul_f32_e32 v3, 0xbfb8aa3b, v3
	v_rcp_f32_e32 v9, v2
	v_exp_f32_e32 v3, v3
	s_nop 0
	v_add_f32_e32 v3, 1.0, v3
	v_rcp_f32_e32 v31, v27
	v_lshlrev_b32_e32 v27, 16, v4
	v_mul_f32_e32 v27, 0xbfb8aa3b, v27
	v_exp_f32_e32 v27, v27
	s_nop 0
	v_add_f32_e32 v27, 1.0, v27
	v_and_b32_e32 v4, 0xffff0000, v4
	v_mul_f32_e32 v4, 0xbfb8aa3b, v4
	v_exp_f32_e32 v4, v4
	v_rcp_f32_e32 v30, v3
	v_add_f32_e32 v4, 1.0, v4
	v_rcp_f32_e32 v32, v27
	v_lshlrev_b32_e32 v27, 16, v5
	v_mul_f32_e32 v27, 0xbfb8aa3b, v27
	v_exp_f32_e32 v27, v27
	s_nop 0
	v_add_f32_e32 v26, 1.0, v27
	v_rcp_f32_e32 v33, v4
	v_and_b32_e32 v4, 0xffff0000, v5
	v_mul_f32_e32 v4, 0xbfb8aa3b, v4
	v_exp_f32_e32 v4, v4
	s_nop 0
	v_add_f32_e32 v4, 1.0, v4
	v_rcp_f32_e32 v50, v26
	v_mov_b32_e32 v29, v20
	v_rcp_f32_e32 v51, v4
	s_waitcnt vmcnt(4)
	v_mov_b64_e32 v[14:15], v[240:241]
	v_cvt_pk_f32_fp8_e32 v[2:3], v14
	v_cvt_pk_f32_fp8_sdwa v[4:5], v14 src0_sel:WORD_1
	v_cvt_pk_f32_fp8_e32 v[26:27], v15
	v_cvt_pk_f32_fp8_sdwa v[14:15], v15 src0_sel:WORD_1
	v_mov_b32_e32 v28, v2
	v_pk_mul_f32 v[28:29], v[28:29], v[178:179]
	v_mov_b32_e32 v20, v3
	v_mov_b32_e32 v179, v9
	v_pk_mul_f32 v[2:3], v[20:21], v[178:179]
	v_mov_b32_e32 v179, v31
	v_add_f32_e32 v9, v2, v3
	v_mov_b32_e32 v2, v4
	v_mov_b32_e32 v3, v16
	v_pk_mul_f32 v[2:3], v[2:3], v[178:179]
	v_mov_b32_e32 v16, v5
	v_mov_b32_e32 v179, v30
	v_add_f32_e32 v4, v2, v3
	v_pk_mul_f32 v[2:3], v[16:17], v[178:179]
	v_mov_b32_e32 v179, v32
	v_add_f32_e32 v5, v2, v3
	v_mov_b32_e32 v2, v26
	v_mov_b32_e32 v3, v24
	v_pk_mul_f32 v[2:3], v[2:3], v[178:179]
	v_mov_b32_e32 v24, v27
	v_mov_b32_e32 v179, v33
	v_add_f32_e32 v16, v2, v3
	v_pk_mul_f32 v[2:3], v[24:25], v[178:179]
	v_mov_b32_e32 v179, v50
	v_add_f32_e32 v17, v2, v3
	v_mov_b32_e32 v2, v14
	v_mov_b32_e32 v3, v22
	v_pk_mul_f32 v[2:3], v[2:3], v[178:179]
	v_mov_b32_e32 v22, v15
	v_mov_b32_e32 v179, v51
	v_add_f32_e32 v28, v28, v29
	v_add_f32_e32 v14, v2, v3
	v_pk_mul_f32 v[2:3], v[22:23], v[178:179]
	v_mul_f32_e32 v4, 0x41800000, v4
	v_add_f32_e32 v15, v2, v3
	v_mul_f32_e32 v2, 0x41800000, v28
	v_mul_f32_e32 v3, 0x41800000, v9
	v_med3_f32 v9, v2, s57, v207
	v_med3_f32 v3, v3, s57, v207
	v_mov_b32_e32 v2, v167
	v_cvt_pk_fp8_f32 v2, v9, v3
	v_mul_f32_e32 v3, 0x41800000, v5
	v_med3_f32 v4, v4, s57, v207
	v_med3_f32 v3, v3, s57, v207
	v_cvt_pk_fp8_f32 v2, v4, v3 op_sel:[0,0,1]
	v_mul_f32_e32 v3, 0x41800000, v16
	v_mul_f32_e32 v4, 0x41800000, v17
	v_med3_f32 v9, v3, s57, v207
	v_med3_f32 v4, v4, s57, v207
	v_mov_b32_e32 v3, v167
	v_cvt_pk_fp8_f32 v3, v9, v4
	v_mul_f32_e32 v5, 0x41800000, v14
	v_mul_f32_e32 v4, 0x41800000, v15
	v_med3_f32 v5, v5, s57, v207
	v_med3_f32 v4, v4, s57, v207
	v_cvt_pk_fp8_f32 v3, v5, v4 op_sel:[0,0,1]
	v_add_u32_e32 v14, 0xb0, v8
	v_ashrrev_i32_e32 v15, 31, v14
	v_pk_mul_f32 v[22:23], v[42:43], s[28:29] op_sel_hi:[1,0]
	global_store_dwordx2 v[18:19], v[2:3], off offset:128
	v_mad_i64_i32 v[2:3], s[0:1], v14, s56, v[10:11]
	v_lshl_add_u64 v[8:9], v[2:3], 0, v[12:13]
	v_lshlrev_b64 v[12:13], 11, v[14:15]
	v_lshl_add_u64 v[10:11], s[16:17], 0, v[12:13]
	v_lshl_add_u64 v[10:11], v[10:11], 0, v[6:7]
	v_pk_mul_f32 v[20:21], v[44:45], s[28:29] op_sel_hi:[1,0]
	s_waitcnt vmcnt(3)
	v_mov_b64_e32 v[2:3], v[222:223]
	v_mov_b64_e32 v[4:5], v[224:225]
	v_lshlrev_b32_e32 v16, 16, v2
	v_mul_f32_e32 v16, 0xbfb8aa3b, v16
	v_exp_f32_e32 v18, v16
	v_and_b32_e32 v2, 0xffff0000, v2
	v_mul_f32_e32 v2, 0xbfb8aa3b, v2
	v_exp_f32_e32 v2, v2
	v_add_f32_e32 v24, 1.0, v18
	v_add_f32_e32 v2, 1.0, v2
	v_pk_mul_f32 v[18:19], v[46:47], s[28:29] op_sel_hi:[1,0]
	v_pk_mul_f32 v[16:17], v[48:49], s[28:29] op_sel_hi:[1,0]
	v_lshlrev_b32_e32 v26, 16, v3
	v_mul_f32_e32 v26, 0xbfb8aa3b, v26
	v_rcp_f32_e32 v179, v24
	v_exp_f32_e32 v26, v26
	s_nop 0
	v_add_f32_e32 v26, 1.0, v26
	v_and_b32_e32 v3, 0xffff0000, v3
	v_mul_f32_e32 v3, 0xbfb8aa3b, v3
	v_exp_f32_e32 v3, v3
	v_rcp_f32_e32 v29, v2
	v_add_f32_e32 v3, 1.0, v3
	v_rcp_f32_e32 v28, v26
	v_lshlrev_b32_e32 v26, 16, v4
	v_mul_f32_e32 v26, 0xbfb8aa3b, v26
	v_exp_f32_e32 v26, v26
	s_nop 0
	v_add_f32_e32 v25, 1.0, v26
	v_and_b32_e32 v4, 0xffff0000, v4
	v_mul_f32_e32 v4, 0xbfb8aa3b, v4
	v_exp_f32_e32 v4, v4
	v_rcp_f32_e32 v31, v3
	v_add_f32_e32 v4, 1.0, v4
	v_rcp_f32_e32 v30, v25
	v_lshlrev_b32_e32 v25, 16, v5
	v_mul_f32_e32 v25, 0xbfb8aa3b, v25
	v_exp_f32_e32 v25, v25
	s_nop 0
	v_add_f32_e32 v24, 1.0, v25
	v_rcp_f32_e32 v32, v4
	v_and_b32_e32 v4, 0xffff0000, v5
	v_mul_f32_e32 v4, 0xbfb8aa3b, v4
	v_exp_f32_e32 v4, v4
	s_nop 0
	v_add_f32_e32 v4, 1.0, v4
	v_rcp_f32_e32 v33, v24
	v_mov_b32_e32 v27, v18
	v_rcp_f32_e32 v42, v4
	s_waitcnt vmcnt(2)
	v_mov_b64_e32 v[14:15], v[242:243]
	v_cvt_pk_f32_fp8_e32 v[2:3], v14
	v_cvt_pk_f32_fp8_sdwa v[4:5], v14 src0_sel:WORD_1
	v_cvt_pk_f32_fp8_e32 v[24:25], v15
	v_cvt_pk_f32_fp8_sdwa v[14:15], v15 src0_sel:WORD_1
	v_mov_b32_e32 v26, v2
	v_pk_mul_f32 v[26:27], v[26:27], v[178:179]
	v_mov_b32_e32 v18, v3
	v_mov_b32_e32 v179, v29
	v_pk_mul_f32 v[2:3], v[18:19], v[178:179]
	v_mov_b32_e32 v179, v28
	v_add_f32_e32 v18, v2, v3
	v_mov_b32_e32 v2, v4
	v_mov_b32_e32 v3, v16
	v_pk_mul_f32 v[2:3], v[2:3], v[178:179]
	v_mov_b32_e32 v16, v5
	v_mov_b32_e32 v179, v31
	v_add_f32_e32 v4, v2, v3
	v_pk_mul_f32 v[2:3], v[16:17], v[178:179]
	v_mov_b32_e32 v179, v30
	v_add_f32_e32 v5, v2, v3
	v_mov_b32_e32 v2, v24
	v_mov_b32_e32 v3, v22
	v_pk_mul_f32 v[2:3], v[2:3], v[178:179]
	v_mov_b32_e32 v22, v25
	v_mov_b32_e32 v179, v32
	v_add_f32_e32 v16, v2, v3
	v_pk_mul_f32 v[2:3], v[22:23], v[178:179]
	v_mov_b32_e32 v179, v33
	v_add_f32_e32 v17, v2, v3
	v_mov_b32_e32 v2, v14
	v_mov_b32_e32 v3, v20
	v_pk_mul_f32 v[2:3], v[2:3], v[178:179]
	v_mov_b32_e32 v20, v15
	v_mov_b32_e32 v179, v42
	v_add_f32_e32 v26, v26, v27
	v_add_f32_e32 v14, v2, v3
	v_pk_mul_f32 v[2:3], v[20:21], v[178:179]
	v_mul_f32_e32 v4, 0x41800000, v4
	v_add_f32_e32 v15, v2, v3
	v_mul_f32_e32 v2, 0x41800000, v26
	v_mul_f32_e32 v3, 0x41800000, v18
	v_med3_f32 v18, v2, s57, v207
	v_med3_f32 v3, v3, s57, v207
	v_mov_b32_e32 v2, v167
	v_cvt_pk_fp8_f32 v2, v18, v3
	v_mul_f32_e32 v3, 0x41800000, v5
	v_med3_f32 v4, v4, s57, v207
	v_med3_f32 v3, v3, s57, v207
	v_cvt_pk_fp8_f32 v2, v4, v3 op_sel:[0,0,1]
	v_mul_f32_e32 v3, 0x41800000, v16
	v_mul_f32_e32 v4, 0x41800000, v17
	v_mul_f32_e32 v5, 0x41800000, v14
	v_med3_f32 v14, v3, s57, v207
	v_med3_f32 v4, v4, s57, v207
	v_mov_b32_e32 v3, v167
	v_cvt_pk_fp8_f32 v3, v14, v4
	v_mul_f32_e32 v4, 0x41800000, v15
	v_med3_f32 v5, v5, s57, v207
	v_med3_f32 v4, v4, s57, v207
	v_cvt_pk_fp8_f32 v3, v5, v4 op_sel:[0,0,1]
	v_lshl_add_u64 v[4:5], s[20:21], 0, v[12:13]
	v_lshl_add_u64 v[6:7], v[4:5], 0, v[6:7]
	v_pk_mul_f32 v[16:17], v[34:35], s[28:29] op_sel_hi:[1,0]
	global_store_dwordx2 v[6:7], v[2:3], off
	s_nop 0
	v_pk_mul_f32 v[14:15], v[36:37], s[28:29] op_sel_hi:[1,0]
	s_waitcnt vmcnt(1)
	v_mov_b64_e32 v[2:3], v[226:227]
	v_mov_b64_e32 v[4:5], v[228:229]
	v_lshlrev_b32_e32 v10, 16, v2
	v_mul_f32_e32 v10, 0xbfb8aa3b, v10
	v_exp_f32_e32 v12, v10
	v_and_b32_e32 v2, 0xffff0000, v2
	v_mul_f32_e32 v2, 0xbfb8aa3b, v2
	v_exp_f32_e32 v2, v2
	v_add_f32_e32 v18, 1.0, v12
	v_add_f32_e32 v2, 1.0, v2
	v_pk_mul_f32 v[12:13], v[38:39], s[28:29] op_sel_hi:[1,0]
	v_pk_mul_f32 v[10:11], v[40:41], s[28:29] op_sel_hi:[1,0]
	v_lshlrev_b32_e32 v20, 16, v3
	v_mul_f32_e32 v20, 0xbfb8aa3b, v20
	v_rcp_f32_e32 v179, v18
	v_exp_f32_e32 v20, v20
	s_nop 0
	v_add_f32_e32 v20, 1.0, v20
	v_and_b32_e32 v3, 0xffff0000, v3
	v_mul_f32_e32 v3, 0xbfb8aa3b, v3
	v_exp_f32_e32 v3, v3
	v_rcp_f32_e32 v23, v2
	v_add_f32_e32 v3, 1.0, v3
	v_rcp_f32_e32 v22, v20
	v_lshlrev_b32_e32 v20, 16, v4
	v_mul_f32_e32 v20, 0xbfb8aa3b, v20
	v_exp_f32_e32 v20, v20
	s_nop 0
	v_add_f32_e32 v19, 1.0, v20
	v_and_b32_e32 v4, 0xffff0000, v4
	v_mul_f32_e32 v4, 0xbfb8aa3b, v4
	v_exp_f32_e32 v4, v4
	v_rcp_f32_e32 v25, v3
	v_add_f32_e32 v4, 1.0, v4
	v_rcp_f32_e32 v24, v19
	v_lshlrev_b32_e32 v19, 16, v5
	v_mul_f32_e32 v19, 0xbfb8aa3b, v19
	v_exp_f32_e32 v19, v19
	s_nop 0
	v_add_f32_e32 v18, 1.0, v19
	v_rcp_f32_e32 v26, v4
	v_and_b32_e32 v4, 0xffff0000, v5
	v_mul_f32_e32 v4, 0xbfb8aa3b, v4
	v_exp_f32_e32 v4, v4
	s_nop 0
	v_add_f32_e32 v4, 1.0, v4
	v_rcp_f32_e32 v27, v18
	v_mov_b32_e32 v21, v12
	v_rcp_f32_e32 v28, v4
	s_waitcnt vmcnt(0)
	v_mov_b64_e32 v[8:9], v[244:245]
	v_cvt_pk_f32_fp8_e32 v[2:3], v8
	v_cvt_pk_f32_fp8_sdwa v[4:5], v8 src0_sel:WORD_1
	v_cvt_pk_f32_fp8_e32 v[18:19], v9
	v_cvt_pk_f32_fp8_sdwa v[8:9], v9 src0_sel:WORD_1
	v_mov_b32_e32 v20, v2
	v_pk_mul_f32 v[20:21], v[20:21], v[178:179]
	v_mov_b32_e32 v12, v3
	v_mov_b32_e32 v179, v23
	v_pk_mul_f32 v[2:3], v[12:13], v[178:179]
	v_mov_b32_e32 v179, v22
	v_add_f32_e32 v12, v2, v3
	v_mov_b32_e32 v2, v4
	v_mov_b32_e32 v3, v10
	v_pk_mul_f32 v[2:3], v[2:3], v[178:179]
	v_mov_b32_e32 v10, v5
	v_mov_b32_e32 v179, v25
	v_add_f32_e32 v4, v2, v3
	v_pk_mul_f32 v[2:3], v[10:11], v[178:179]
	v_mov_b32_e32 v179, v24
	v_add_f32_e32 v5, v2, v3
	v_mov_b32_e32 v2, v18
	v_mov_b32_e32 v3, v16
	v_pk_mul_f32 v[2:3], v[2:3], v[178:179]
	v_mov_b32_e32 v16, v19
	v_mov_b32_e32 v179, v26
	v_add_f32_e32 v10, v2, v3
	v_pk_mul_f32 v[2:3], v[16:17], v[178:179]
	v_mov_b32_e32 v179, v27
	v_add_f32_e32 v11, v2, v3
	v_mov_b32_e32 v2, v8
	v_mov_b32_e32 v3, v14
	v_pk_mul_f32 v[2:3], v[2:3], v[178:179]
	v_mov_b32_e32 v14, v9
	v_mov_b32_e32 v179, v28
	v_add_f32_e32 v20, v20, v21
	v_add_f32_e32 v8, v2, v3
	v_pk_mul_f32 v[2:3], v[14:15], v[178:179]
	v_mul_f32_e32 v4, 0x41800000, v4
	v_add_f32_e32 v9, v2, v3
	v_mul_f32_e32 v2, 0x41800000, v20
	v_mul_f32_e32 v3, 0x41800000, v12
	v_med3_f32 v12, v2, s57, v207
	v_med3_f32 v3, v3, s57, v207
	v_mov_b32_e32 v2, v167
	v_cvt_pk_fp8_f32 v2, v12, v3
	v_mul_f32_e32 v3, 0x41800000, v5
	v_med3_f32 v4, v4, s57, v207
	v_med3_f32 v3, v3, s57, v207
	v_cvt_pk_fp8_f32 v2, v4, v3 op_sel:[0,0,1]
	v_mul_f32_e32 v3, 0x41800000, v10
	v_mul_f32_e32 v4, 0x41800000, v11
	v_mul_f32_e32 v5, 0x41800000, v8
	v_med3_f32 v8, v3, s57, v207
	v_med3_f32 v4, v4, s57, v207
	v_mov_b32_e32 v3, v167
	v_cvt_pk_fp8_f32 v3, v8, v4
	v_mul_f32_e32 v4, 0x41800000, v9
	v_med3_f32 v5, v5, s57, v207
	v_med3_f32 v4, v4, s57, v207
	v_cvt_pk_fp8_f32 v3, v5, v4 op_sel:[0,0,1]
	s_andn2_b64 vcc, exec, s[6:7]
	s_mov_b64 s[0:1], -1
	global_store_dwordx2 v[6:7], v[2:3], off offset:128
	s_cbranch_vccnz .LBB0_1050
	s_andn2_b64 vcc, exec, s[14:15]
	s_cbranch_vccnz .LBB0_1049
	s_barrier
	s_branch .LBB0_1049

.LBB0_1214:
	s_mov_b64 s[0:1], exec
	v_readlane_b32 s2, v254, 4
	v_readlane_b32 s3, v254, 5
	s_and_b64 s[2:3], s[0:1], s[2:3]
	s_mov_b64 exec, s[2:3]
	ds_write_b32 v144, v131
	s_or_b64 exec, exec, s[0:1]
	s_lshl_b32 s55, s54, 5
	s_add_i32 s12, s55, s33
	s_ashr_i32 s13, s12, 31
	s_lshl_b64 s[0:1], s[12:13], 13
	v_lshl_add_u64 v[2:3], v[134:135], 0, s[0:1]
	global_load_dwordx4 v[126:129], v[2:3], off nt
	global_load_dwordx4 v[122:125], v[2:3], off offset:1024 nt
	global_load_dwordx4 v[118:121], v[2:3], off offset:2048 nt
	global_load_dwordx4 v[114:117], v[2:3], off offset:3072 nt
	v_add_co_u32_e32 v2, vcc, 0x1000, v2
	s_or_b32 s10, s12, 1
	s_nop 0
	v_addc_co_u32_e32 v3, vcc, 0, v3, vcc
	global_load_dwordx4 v[110:113], v[2:3], off nt
	global_load_dwordx4 v[106:109], v[2:3], off offset:1024 nt
	global_load_dwordx4 v[102:105], v[2:3], off offset:2048 nt
	global_load_dwordx4 v[98:101], v[2:3], off offset:3072 nt
	s_or_b32 s4, s12, 2
	s_ashr_i32 s11, s10, 31
	s_ashr_i32 s5, s4, 31
	s_or_b32 s2, s12, 3
	s_lshl_b64 s[0:1], s[10:11], 13
	s_lshl_b64 s[14:15], s[4:5], 13
	s_ashr_i32 s3, s2, 31
	v_lshl_add_u64 v[4:5], v[134:135], 0, s[0:1]
	v_lshl_add_u64 v[6:7], v[134:135], 0, s[14:15]
	s_lshl_b64 s[16:17], s[2:3], 13
	global_load_dwordx4 v[94:97], v[4:5], off nt
	global_load_dwordx4 v[90:93], v[4:5], off offset:1024 nt
	global_load_dwordx4 v[86:89], v[4:5], off offset:2048 nt
	global_load_dwordx4 v[78:81], v[4:5], off offset:3072 nt
	global_load_dwordx4 v[62:65], v[6:7], off nt
	global_load_dwordx4 v[58:61], v[6:7], off offset:1024 nt
	global_load_dwordx4 v[54:57], v[6:7], off offset:2048 nt
	global_load_dwordx4 v[50:53], v[6:7], off offset:3072 nt
	v_add_co_u32_e64 v6, s[0:1], s42, v6
	v_lshl_add_u64 v[2:3], v[134:135], 0, s[16:17]
	s_nop 0
	v_addc_co_u32_e64 v7, s[0:1], 0, v7, s[0:1]
	v_add_co_u32_e32 v66, vcc, s42, v4
	global_load_dwordx4 v[30:33], v[2:3], off nt
	global_load_dwordx4 v[26:29], v[2:3], off offset:1024 nt
	global_load_dwordx4 v[22:25], v[2:3], off offset:2048 nt
	global_load_dwordx4 v[18:21], v[2:3], off offset:3072 nt
	v_add_co_u32_e64 v2, s[0:1], s42, v2
	v_addc_co_u32_e32 v67, vcc, 0, v5, vcc
	s_nop 0
	v_addc_co_u32_e64 v3, s[0:1], 0, v3, s[0:1]
	global_load_dwordx4 v[46:49], v[6:7], off nt
	global_load_dwordx4 v[42:45], v[6:7], off offset:1024 nt
	global_load_dwordx4 v[38:41], v[6:7], off offset:2048 nt
	global_load_dwordx4 v[34:37], v[6:7], off offset:3072 nt
	global_load_dwordx4 v[14:17], v[2:3], off nt
	global_load_dwordx4 v[10:13], v[2:3], off offset:1024 nt
	s_nop 0
	global_load_dwordx4 v[6:9], v[2:3], off offset:2048 nt
	s_nop 0
	global_load_dwordx4 v[2:5], v[2:3], off offset:3072 nt
	s_nop 0
	global_load_dwordx4 v[82:85], v[66:67], off nt
	global_load_dwordx4 v[74:77], v[66:67], off offset:1024 nt
	global_load_dwordx4 v[70:73], v[66:67], off offset:2048 nt
	s_nop 0
	global_load_dwordx4 v[66:69], v[66:67], off offset:3072 nt
	s_waitcnt vmcnt(31)
	v_mul_f32_e32 v130, v127, v127
	v_mul_f32_e32 v182, v129, v129
	s_waitcnt vmcnt(30)
	v_mul_f32_e32 v183, v123, v123
	v_mul_f32_e32 v184, v125, v125
	s_waitcnt vmcnt(29)
	v_mul_f32_e32 v185, v119, v119
	v_mul_f32_e32 v186, v121, v121
	v_fmac_f32_e32 v130, v126, v126
	v_fmac_f32_e32 v182, v128, v128
	v_fmac_f32_e32 v183, v122, v122
	v_fmac_f32_e32 v184, v124, v124
	s_waitcnt vmcnt(28)
	v_mul_f32_e32 v187, v115, v115
	v_mul_f32_e32 v188, v117, v117
	v_fmac_f32_e32 v185, v118, v118
	v_fmac_f32_e32 v186, v120, v120
	v_add_f32_e32 v130, v130, v182
	v_add_f32_e32 v182, v183, v184
	v_fmac_f32_e32 v187, v114, v114
	v_fmac_f32_e32 v188, v116, v116
	v_add_f32_e32 v183, v185, v186
	s_waitcnt vmcnt(27)
	v_mul_f32_e32 v185, v111, v111
	v_add_f32_e32 v130, v130, v182
	v_mul_f32_e32 v182, v113, v113
	v_add_f32_e32 v184, v187, v188
	v_add_f32_e32 v130, v130, v183
	v_fmac_f32_e32 v185, v110, v110
	v_fmac_f32_e32 v182, v112, v112
	v_add_f32_e32 v130, v130, v184
	v_add_f32_e32 v182, v185, v182
	v_add_f32_e32 v130, v130, v182
	s_waitcnt vmcnt(26)
	v_mul_f32_e32 v182, v107, v107
	v_mul_f32_e32 v183, v109, v109
	v_fmac_f32_e32 v182, v106, v106
	v_fmac_f32_e32 v183, v108, v108
	v_add_f32_e32 v182, v182, v183
	v_add_f32_e32 v130, v130, v182
	s_waitcnt vmcnt(25)
	v_mul_f32_e32 v182, v103, v103
	v_mul_f32_e32 v183, v105, v105
	v_fmac_f32_e32 v182, v102, v102
	v_fmac_f32_e32 v183, v104, v104
	v_add_f32_e32 v182, v182, v183
	v_add_f32_e32 v130, v130, v182
	s_waitcnt vmcnt(24)
	v_mul_f32_e32 v182, v99, v99
	v_mul_f32_e32 v183, v101, v101
	v_fmac_f32_e32 v182, v98, v98
	v_fmac_f32_e32 v183, v100, v100
	v_add_f32_e32 v182, v182, v183
	v_add_f32_e32 v130, v130, v182
	ds_bpermute_b32 v182, v1, v130
	s_waitcnt lgkmcnt(0)
	v_add_f32_e32 v130, v130, v182
	ds_bpermute_b32 v182, v138, v130
	s_waitcnt lgkmcnt(0)
	v_add_f32_e32 v130, v130, v182
	ds_bpermute_b32 v182, v139, v130
	s_waitcnt lgkmcnt(0)
	v_add_f32_e32 v130, v130, v182
	ds_bpermute_b32 v182, v140, v130
	s_waitcnt lgkmcnt(0)
	v_add_f32_e32 v130, v130, v182
	ds_bpermute_b32 v182, v141, v130
	s_waitcnt lgkmcnt(0)
	v_add_f32_e32 v130, v130, v182
	ds_bpermute_b32 v182, v142, v130
	s_waitcnt lgkmcnt(0)
	v_add_f32_e32 v130, v130, v182
	v_fmamk_f32 v130, v130, 0x3a000000, v175
	v_mul_f32_e32 v182, 0x4f800000, v130
	v_cmp_gt_f32_e32 vcc, s43, v130
	s_nop 1
	v_cndmask_b32_e32 v130, v130, v182, vcc
	v_sqrt_f32_e32 v182, v130
	s_nop 0
	v_add_u32_e32 v183, -1, v182
	v_add_u32_e32 v184, 1, v182
	v_fma_f32 v185, -v183, v182, v130
	v_fma_f32 v186, -v184, v182, v130
	v_cmp_ge_f32_e64 s[0:1], 0, v185
	s_nop 1
	v_cndmask_b32_e64 v182, v182, v183, s[0:1]
	v_cmp_lt_f32_e64 s[0:1], 0, v186
	s_nop 1
	v_cndmask_b32_e64 v182, v182, v184, s[0:1]
	v_mul_f32_e32 v183, 0x37800000, v182
	v_cndmask_b32_e32 v182, v182, v183, vcc
	v_cmp_class_f32_e32 vcc, v130, v176
	s_nop 1
	v_cndmask_b32_e32 v130, v182, v130, vcc
	v_div_scale_f32 v182, s[0:1], v130, v130, 1.0
	v_rcp_f32_e32 v183, v182
	v_div_scale_f32 v184, vcc, 1.0, v130, 1.0
	v_fma_f32 v185, -v182, v183, 1.0
	v_fmac_f32_e32 v183, v185, v183
	v_mul_f32_e32 v185, v184, v183
	v_fma_f32 v186, -v182, v185, v184
	v_fmac_f32_e32 v185, v186, v183
	v_fma_f32 v182, -v182, v185, v184
	v_div_fmas_f32 v182, v182, v183, v185
	v_div_fixup_f32 v130, v182, v130, 1.0
	s_and_saveexec_b64 s[0:1], s[6:7]
	s_add_i32 s14, s39, 0
	s_add_i32 s14, s14, 0x20c00
	v_mov_b32_e32 v182, s14
	ds_write_b32 v182, v130
	s_or_b64 exec, exec, s[0:1]
	ds_read_b128 v[182:185], v143
	ds_read_b128 v[186:189], v143 offset:8192
	v_pk_mul_f32 v[126:127], v[126:127], v[130:131] op_sel_hi:[1,0]
	ds_read_b128 v[190:193], v143 offset:1024
	ds_read_b128 v[198:201], v143 offset:9216
	v_pk_mul_f32 v[128:129], v[128:129], v[130:131] op_sel_hi:[1,0]
	v_pk_mul_f32 v[122:123], v[122:123], v[130:131] op_sel_hi:[1,0]
	s_waitcnt lgkmcnt(2)
	v_pk_fma_f32 v[126:127], v[126:127], v[182:183], v[186:187]
	v_mov_b32_e32 v182, 0
	v_med3_f32 v126, v126, s44, v181
	v_med3_f32 v127, v127, s44, v181
	v_cvt_pk_fp8_f32 v182, v126, v127
	v_pk_fma_f32 v[126:127], v[128:129], v[184:185], v[188:189]
	s_waitcnt lgkmcnt(0)
	v_pk_fma_f32 v[122:123], v[122:123], v[190:191], v[198:199]
	v_med3_f32 v126, v126, s44, v181
	v_med3_f32 v127, v127, s44, v181
	v_cvt_pk_fp8_f32 v182, v126, v127 op_sel:[0,0,1]
	v_med3_f32 v122, v122, s44, v181
	v_med3_f32 v123, v123, s44, v181
	v_mov_b32_e32 v195, 0
	v_cvt_pk_fp8_f32 v195, v122, v123
	s_lshl_b64 s[0:1], s[12:13], 11
	v_pk_mul_f32 v[124:125], v[124:125], v[130:131] op_sel_hi:[1,0]
	v_lshl_add_u64 v[126:127], v[136:137], 0, s[0:1]
	v_pk_fma_f32 v[122:123], v[124:125], v[192:193], v[200:201]
	global_store_dword v[126:127], v182, off
	v_med3_f32 v122, v122, s44, v181
	v_med3_f32 v123, v123, s44, v181
	v_cvt_pk_fp8_f32 v195, v122, v123 op_sel:[0,0,1]
	ds_read_b128 v[122:125], v143 offset:2048
	ds_read_b128 v[182:185], v143 offset:10240
	v_pk_mul_f32 v[128:129], v[120:121], v[130:131] op_sel_hi:[1,0]
	v_pk_mul_f32 v[190:191], v[118:119], v[130:131] op_sel_hi:[1,0]
	ds_read_b128 v[118:121], v143 offset:3072
	ds_read_b128 v[186:189], v143 offset:11264
	v_pk_mul_f32 v[114:115], v[114:115], v[130:131] op_sel_hi:[1,0]
	s_waitcnt lgkmcnt(2)
	v_pk_fma_f32 v[122:123], v[190:191], v[122:123], v[182:183]
	v_mov_b32_e32 v190, 0
	v_med3_f32 v122, v122, s44, v181
	v_med3_f32 v123, v123, s44, v181
	s_waitcnt lgkmcnt(0)
	v_pk_fma_f32 v[114:115], v[114:115], v[118:119], v[186:187]
	v_cvt_pk_fp8_f32 v190, v122, v123
	v_pk_fma_f32 v[122:123], v[128:129], v[124:125], v[184:185]
	v_med3_f32 v114, v114, s44, v181
	v_med3_f32 v115, v115, s44, v181
	v_mov_b32_e32 v184, 0
	v_cvt_pk_fp8_f32 v184, v114, v115
	v_pk_mul_f32 v[116:117], v[116:117], v[130:131] op_sel_hi:[1,0]
	v_med3_f32 v122, v122, s44, v181
	v_pk_fma_f32 v[114:115], v[116:117], v[120:121], v[188:189]
	v_med3_f32 v123, v123, s44, v181
	v_med3_f32 v114, v114, s44, v181
	v_med3_f32 v115, v115, s44, v181
	v_cvt_pk_fp8_f32 v190, v122, v123 op_sel:[0,0,1]
	v_cvt_pk_fp8_f32 v184, v114, v115 op_sel:[0,0,1]
	ds_read_b128 v[114:117], v143 offset:4096
	ds_read_b128 v[118:121], v143 offset:12288
	v_pk_mul_f32 v[128:129], v[112:113], v[130:131] op_sel_hi:[1,0]
	v_pk_mul_f32 v[182:183], v[110:111], v[130:131] op_sel_hi:[1,0]
	ds_read_b128 v[110:113], v143 offset:5120
	ds_read_b128 v[122:125], v143 offset:13312
	v_pk_mul_f32 v[106:107], v[106:107], v[130:131] op_sel_hi:[1,0]
	s_waitcnt lgkmcnt(2)
	v_pk_fma_f32 v[114:115], v[182:183], v[114:115], v[118:119]
	v_mov_b32_e32 v118, 0
	v_med3_f32 v114, v114, s44, v181
	s_waitcnt lgkmcnt(0)
	v_pk_fma_f32 v[106:107], v[106:107], v[110:111], v[122:123]
	v_mov_b32_e32 v122, 0
	v_med3_f32 v106, v106, s44, v181
	v_med3_f32 v107, v107, s44, v181
	v_cvt_pk_fp8_f32 v122, v106, v107
	s_waitcnt vmcnt(24)
	v_mul_f32_e32 v106, v95, v95
	v_mul_f32_e32 v107, v97, v97
	v_fmac_f32_e32 v106, v94, v94
	v_fmac_f32_e32 v107, v96, v96
	v_add_f32_e32 v106, v106, v107
	s_waitcnt vmcnt(23)
	v_mul_f32_e32 v107, v91, v91
	v_mul_f32_e32 v110, v93, v93
	v_fmac_f32_e32 v107, v90, v90
	v_fmac_f32_e32 v110, v92, v92
	v_add_f32_e32 v107, v107, v110
	v_add_f32_e32 v106, v106, v107
	s_waitcnt vmcnt(22)
	v_mul_f32_e32 v107, v87, v87
	v_mul_f32_e32 v110, v89, v89
	v_fmac_f32_e32 v107, v86, v86
	v_fmac_f32_e32 v110, v88, v88
	v_add_f32_e32 v107, v107, v110
	v_add_f32_e32 v106, v106, v107
	s_waitcnt vmcnt(21)
	v_mul_f32_e32 v107, v79, v79
	v_mul_f32_e32 v110, v81, v81
	v_fmac_f32_e32 v107, v78, v78
	v_fmac_f32_e32 v110, v80, v80
	v_add_f32_e32 v107, v107, v110
	v_add_f32_e32 v106, v106, v107
	s_waitcnt vmcnt(4)
	v_mul_f32_e32 v107, v83, v83
	v_mul_f32_e32 v110, v85, v85
	v_fmac_f32_e32 v107, v82, v82
	v_fmac_f32_e32 v110, v84, v84
	v_add_f32_e32 v107, v107, v110
	v_add_f32_e32 v106, v106, v107
	s_waitcnt vmcnt(3)
	v_mul_f32_e32 v107, v75, v75
	v_mul_f32_e32 v110, v77, v77
	v_fmac_f32_e32 v107, v74, v74
	v_fmac_f32_e32 v110, v76, v76
	v_add_f32_e32 v107, v107, v110
	v_add_f32_e32 v106, v106, v107
	s_waitcnt vmcnt(2)
	v_mul_f32_e32 v107, v71, v71
	v_mul_f32_e32 v110, v73, v73
	v_med3_f32 v115, v115, s44, v181
	v_fmac_f32_e32 v107, v70, v70
	v_fmac_f32_e32 v110, v72, v72
	v_cvt_pk_fp8_f32 v118, v114, v115
	v_add_f32_e32 v107, v107, v110
	v_add_f32_e32 v106, v106, v107
	s_waitcnt vmcnt(1)
	v_mul_f32_e32 v107, v67, v67
	v_mul_f32_e32 v110, v69, v69
	v_pk_fma_f32 v[114:115], v[128:129], v[116:117], v[120:121]
	v_fmac_f32_e32 v107, v66, v66
	v_fmac_f32_e32 v110, v68, v68
	v_med3_f32 v114, v114, s44, v181
	v_med3_f32 v115, v115, s44, v181
	v_add_f32_e32 v107, v107, v110
	v_cvt_pk_fp8_f32 v118, v114, v115 op_sel:[0,0,1]
	v_add_f32_e32 v114, v106, v107
	ds_bpermute_b32 v115, v1, v114
	v_pk_mul_f32 v[108:109], v[108:109], v[130:131] op_sel_hi:[1,0]
	global_store_dword v[126:127], v195, off offset:256
	global_store_dword v[126:127], v190, off offset:512
	global_store_dword v[126:127], v184, off offset:768
	global_store_dword v[126:127], v118, off offset:1024
	v_pk_fma_f32 v[108:109], v[108:109], v[112:113], v[124:125]
	v_pk_mul_f32 v[120:121], v[102:103], v[130:131] op_sel_hi:[1,0]
	v_med3_f32 v108, v108, s44, v181
	v_med3_f32 v109, v109, s44, v181
	s_waitcnt lgkmcnt(0)
	v_add_f32_e32 v123, v114, v115
	v_cvt_pk_fp8_f32 v122, v108, v109 op_sel:[0,0,1]
	ds_read_b128 v[106:109], v143 offset:6144
	ds_read_b128 v[110:113], v143 offset:14336
	ds_bpermute_b32 v124, v138, v123
	v_pk_mul_f32 v[118:119], v[104:105], v[130:131] op_sel_hi:[1,0]
	ds_read_b128 v[102:105], v143 offset:7168
	ds_read_b128 v[114:117], v143 offset:15360
	v_pk_mul_f32 v[98:99], v[98:99], v[130:131] op_sel_hi:[1,0]
	s_waitcnt lgkmcnt(3)
	v_pk_fma_f32 v[106:107], v[120:121], v[106:107], v[110:111]
	s_waitcnt lgkmcnt(2)
	v_add_f32_e32 v110, v123, v124
	ds_bpermute_b32 v111, v139, v110
	v_med3_f32 v106, v106, s44, v181
	v_med3_f32 v107, v107, s44, v181
	v_mov_b32_e32 v120, 0
	v_cvt_pk_fp8_f32 v120, v106, v107
	s_waitcnt lgkmcnt(0)
	v_add_f32_e32 v110, v110, v111
	ds_bpermute_b32 v111, v140, v110
	v_pk_fma_f32 v[106:107], v[118:119], v[108:109], v[112:113]
	v_pk_fma_f32 v[98:99], v[98:99], v[102:103], v[114:115]
	v_med3_f32 v106, v106, s44, v181
	v_med3_f32 v107, v107, s44, v181
	v_cvt_pk_fp8_f32 v120, v106, v107 op_sel:[0,0,1]
	s_waitcnt lgkmcnt(0)
	v_add_f32_e32 v106, v110, v111
	ds_bpermute_b32 v107, v141, v106
	v_pk_mul_f32 v[100:101], v[100:101], v[130:131] op_sel_hi:[1,0]
	v_med3_f32 v98, v98, s44, v181
	v_pk_fma_f32 v[100:101], v[100:101], v[104:105], v[116:117]
	v_med3_f32 v99, v99, s44, v181
	s_waitcnt lgkmcnt(0)
	v_add_f32_e32 v102, v106, v107
	ds_bpermute_b32 v103, v142, v102
	v_mov_b32_e32 v104, 0
	v_cvt_pk_fp8_f32 v104, v98, v99
	v_med3_f32 v100, v100, s44, v181
	v_med3_f32 v101, v101, s44, v181
	s_waitcnt lgkmcnt(0)
	v_add_f32_e32 v98, v102, v103
	v_fmamk_f32 v98, v98, 0x3a000000, v175
	v_mul_f32_e32 v99, 0x4f800000, v98
	v_cmp_gt_f32_e32 vcc, s43, v98
	v_cvt_pk_fp8_f32 v104, v100, v101 op_sel:[0,0,1]
	global_store_dword v[126:127], v122, off offset:1280
	global_store_dword v[126:127], v120, off offset:1536
	global_store_dword v[126:127], v104, off offset:1792
	v_cndmask_b32_e32 v98, v98, v99, vcc
	v_sqrt_f32_e32 v99, v98
	s_nop 0
	v_add_u32_e32 v100, -1, v99
	v_fma_f32 v101, -v100, v99, v98
	v_cmp_ge_f32_e64 s[0:1], 0, v101
	v_add_u32_e32 v101, 1, v99
	s_nop 0
	v_cndmask_b32_e64 v100, v99, v100, s[0:1]
	v_fma_f32 v99, -v101, v99, v98
	v_cmp_lt_f32_e64 s[0:1], 0, v99
	s_nop 1
	v_cndmask_b32_e64 v99, v100, v101, s[0:1]
	v_mul_f32_e32 v100, 0x37800000, v99
	v_cndmask_b32_e32 v99, v99, v100, vcc
	v_cmp_class_f32_e32 vcc, v98, v176
	s_nop 1
	v_cndmask_b32_e32 v98, v99, v98, vcc
	v_div_scale_f32 v99, s[0:1], v98, v98, 1.0
	v_rcp_f32_e32 v100, v99
	s_nop 0
	v_fma_f32 v101, -v99, v100, 1.0
	v_fmac_f32_e32 v100, v101, v100
	v_div_scale_f32 v101, vcc, 1.0, v98, 1.0
	v_mul_f32_e32 v102, v101, v100
	v_fma_f32 v103, -v99, v102, v101
	v_fmac_f32_e32 v102, v103, v100
	v_fma_f32 v99, -v99, v102, v101
	v_div_fmas_f32 v99, v99, v100, v102
	v_div_fixup_f32 v98, v99, v98, 1.0
	s_and_saveexec_b64 s[0:1], s[6:7]
	s_add_i32 s12, s39, 0
	s_add_i32 s12, s12, 0x20c04
	v_mov_b32_e32 v99, s12
	ds_write_b32 v99, v98
	s_or_b64 exec, exec, s[0:1]
	ds_read_b128 v[100:103], v143
	ds_read_b128 v[104:107], v143 offset:8192
	v_pk_mul_f32 v[94:95], v[94:95], v[98:99] op_sel_hi:[1,0]
	v_pk_mul_f32 v[96:97], v[96:97], v[98:99] op_sel_hi:[1,0]
	v_mov_b32_e32 v99, 0
	ds_read_b128 v[108:111], v143 offset:1024
	ds_read_b128 v[112:115], v143 offset:9216
	s_waitcnt lgkmcnt(2)
	v_pk_fma_f32 v[94:95], v[94:95], v[100:101], v[104:105]
	s_lshl_b64 s[0:1], s[10:11], 11
	v_med3_f32 v94, v94, s44, v181
	v_med3_f32 v95, v95, s44, v181
	v_cvt_pk_fp8_f32 v99, v94, v95
	v_pk_fma_f32 v[94:95], v[96:97], v[102:103], v[106:107]
	s_nop 0
	v_med3_f32 v94, v94, s44, v181
	v_med3_f32 v95, v95, s44, v181
	v_cvt_pk_fp8_f32 v99, v94, v95 op_sel:[0,0,1]
	v_lshl_add_u64 v[94:95], v[136:137], 0, s[0:1]
	v_pk_mul_f32 v[90:91], v[90:91], v[98:99] op_sel_hi:[1,0]
	s_waitcnt lgkmcnt(0)
	v_pk_fma_f32 v[90:91], v[90:91], v[108:109], v[112:113]
	global_store_dword v[94:95], v99, off
	v_pk_mul_f32 v[92:93], v[92:93], v[98:99] op_sel_hi:[1,0]
	v_med3_f32 v90, v90, s44, v181
	v_med3_f32 v91, v91, s44, v181
	v_mov_b32_e32 v99, 0
	v_cvt_pk_fp8_f32 v99, v90, v91
	v_pk_fma_f32 v[90:91], v[92:93], v[110:111], v[114:115]
	s_nop 0
	v_med3_f32 v90, v90, s44, v181
	v_med3_f32 v91, v91, s44, v181
	v_cvt_pk_fp8_f32 v99, v90, v91 op_sel:[0,0,1]
	ds_read_b128 v[90:93], v143 offset:2048
	ds_read_b128 v[100:103], v143 offset:10240
	v_pk_mul_f32 v[96:97], v[88:89], v[98:99] op_sel_hi:[1,0]
	v_pk_mul_f32 v[108:109], v[86:87], v[98:99] op_sel_hi:[1,0]
	ds_read_b128 v[86:89], v143 offset:3072
	ds_read_b128 v[104:107], v143 offset:11264
	s_waitcnt lgkmcnt(2)
	v_pk_fma_f32 v[90:91], v[108:109], v[90:91], v[100:101]
	v_pk_mul_f32 v[78:79], v[78:79], v[98:99] op_sel_hi:[1,0]
	v_med3_f32 v90, v90, s44, v181
	v_med3_f32 v91, v91, s44, v181
	v_mov_b32_e32 v108, 0
	s_waitcnt lgkmcnt(0)
	v_pk_fma_f32 v[78:79], v[78:79], v[86:87], v[104:105]
	v_cvt_pk_fp8_f32 v108, v90, v91
	v_pk_fma_f32 v[90:91], v[96:97], v[92:93], v[102:103]
	v_med3_f32 v78, v78, s44, v181
	v_med3_f32 v79, v79, s44, v181
	v_mov_b32_e32 v102, 0
	v_cvt_pk_fp8_f32 v102, v78, v79
	v_pk_mul_f32 v[80:81], v[80:81], v[98:99] op_sel_hi:[1,0]
	v_med3_f32 v90, v90, s44, v181
	v_pk_fma_f32 v[78:79], v[80:81], v[88:89], v[106:107]
	v_med3_f32 v91, v91, s44, v181
	v_med3_f32 v78, v78, s44, v181
	v_med3_f32 v79, v79, s44, v181
	v_cvt_pk_fp8_f32 v102, v78, v79 op_sel:[0,0,1]
	ds_read_b128 v[78:81], v143 offset:4096
	ds_read_b128 v[86:89], v143 offset:12288
	v_cvt_pk_fp8_f32 v108, v90, v91 op_sel:[0,0,1]
	v_pk_mul_f32 v[96:97], v[84:85], v[98:99] op_sel_hi:[1,0]
	v_pk_mul_f32 v[100:101], v[82:83], v[98:99] op_sel_hi:[1,0]
	ds_read_b128 v[82:85], v143 offset:5120
	ds_read_b128 v[90:93], v143 offset:13312
	s_waitcnt lgkmcnt(2)
	v_pk_fma_f32 v[78:79], v[100:101], v[78:79], v[86:87]
	v_mov_b32_e32 v86, 0
	v_med3_f32 v78, v78, s44, v181
	v_med3_f32 v79, v79, s44, v181
	v_pk_mul_f32 v[74:75], v[74:75], v[98:99] op_sel_hi:[1,0]
	v_cvt_pk_fp8_f32 v86, v78, v79
	s_waitcnt lgkmcnt(0)
	v_pk_fma_f32 v[74:75], v[74:75], v[82:83], v[90:91]
	v_mov_b32_e32 v90, 0
	v_med3_f32 v74, v74, s44, v181
	v_med3_f32 v75, v75, s44, v181
	v_pk_fma_f32 v[78:79], v[96:97], v[80:81], v[88:89]
	v_cvt_pk_fp8_f32 v90, v74, v75
	v_mul_f32_e32 v74, v63, v63
	v_mul_f32_e32 v75, v65, v65
	v_med3_f32 v78, v78, s44, v181
	v_med3_f32 v79, v79, s44, v181
	v_fmac_f32_e32 v74, v62, v62
	v_fmac_f32_e32 v75, v64, v64
	v_cvt_pk_fp8_f32 v86, v78, v79 op_sel:[0,0,1]
	v_add_f32_e32 v74, v74, v75
	v_mul_f32_e32 v75, v59, v59
	v_mul_f32_e32 v78, v61, v61
	v_fmac_f32_e32 v75, v58, v58
	v_fmac_f32_e32 v78, v60, v60
	v_add_f32_e32 v75, v75, v78
	v_add_f32_e32 v74, v74, v75
	v_mul_f32_e32 v75, v55, v55
	v_mul_f32_e32 v78, v57, v57
	v_fmac_f32_e32 v75, v54, v54
	v_fmac_f32_e32 v78, v56, v56
	v_add_f32_e32 v75, v75, v78
	v_add_f32_e32 v74, v74, v75
	v_mul_f32_e32 v75, v51, v51
	v_mul_f32_e32 v78, v53, v53
	v_fmac_f32_e32 v75, v50, v50
	v_fmac_f32_e32 v78, v52, v52
	v_add_f32_e32 v75, v75, v78
	v_add_f32_e32 v74, v74, v75
	v_mul_f32_e32 v75, v47, v47
	v_mul_f32_e32 v78, v49, v49
	v_fmac_f32_e32 v75, v46, v46
	v_fmac_f32_e32 v78, v48, v48
	v_add_f32_e32 v75, v75, v78
	v_add_f32_e32 v74, v74, v75
	v_mul_f32_e32 v75, v43, v43
	v_mul_f32_e32 v78, v45, v45
	v_fmac_f32_e32 v75, v42, v42
	v_fmac_f32_e32 v78, v44, v44
	v_add_f32_e32 v75, v75, v78
	v_add_f32_e32 v74, v74, v75
	v_mul_f32_e32 v75, v39, v39
	v_mul_f32_e32 v78, v41, v41
	v_fmac_f32_e32 v75, v38, v38
	v_fmac_f32_e32 v78, v40, v40
	v_add_f32_e32 v75, v75, v78
	v_add_f32_e32 v74, v74, v75
	v_mul_f32_e32 v75, v35, v35
	v_mul_f32_e32 v78, v37, v37
	v_fmac_f32_e32 v75, v34, v34
	v_fmac_f32_e32 v78, v36, v36
	v_add_f32_e32 v75, v75, v78
	v_add_f32_e32 v82, v74, v75
	ds_bpermute_b32 v83, v1, v82
	v_pk_mul_f32 v[76:77], v[76:77], v[98:99] op_sel_hi:[1,0]
	global_store_dword v[94:95], v99, off offset:256
	global_store_dword v[94:95], v108, off offset:512
	global_store_dword v[94:95], v102, off offset:768
	global_store_dword v[94:95], v86, off offset:1024
	v_pk_fma_f32 v[76:77], v[76:77], v[84:85], v[92:93]
	v_pk_mul_f32 v[88:89], v[70:71], v[98:99] op_sel_hi:[1,0]
	v_med3_f32 v76, v76, s44, v181
	v_med3_f32 v77, v77, s44, v181
	s_waitcnt lgkmcnt(0)
	v_add_f32_e32 v91, v82, v83
	v_cvt_pk_fp8_f32 v90, v76, v77 op_sel:[0,0,1]
	ds_read_b128 v[74:77], v143 offset:6144
	ds_read_b128 v[78:81], v143 offset:14336
	ds_bpermute_b32 v92, v138, v91
	v_pk_mul_f32 v[86:87], v[72:73], v[98:99] op_sel_hi:[1,0]
	ds_read_b128 v[70:73], v143 offset:7168
	ds_read_b128 v[82:85], v143 offset:15360
	v_pk_mul_f32 v[66:67], v[66:67], v[98:99] op_sel_hi:[1,0]
	s_waitcnt lgkmcnt(3)
	v_pk_fma_f32 v[74:75], v[88:89], v[74:75], v[78:79]
	s_waitcnt lgkmcnt(2)
	v_add_f32_e32 v78, v91, v92
	ds_bpermute_b32 v79, v139, v78
	v_med3_f32 v74, v74, s44, v181
	v_med3_f32 v75, v75, s44, v181
	v_mov_b32_e32 v88, 0
	v_cvt_pk_fp8_f32 v88, v74, v75
	s_waitcnt lgkmcnt(0)
	v_add_f32_e32 v78, v78, v79
	ds_bpermute_b32 v79, v140, v78
	v_pk_fma_f32 v[74:75], v[86:87], v[76:77], v[80:81]
	v_pk_fma_f32 v[66:67], v[66:67], v[70:71], v[82:83]
	v_med3_f32 v74, v74, s44, v181
	v_med3_f32 v75, v75, s44, v181
	v_cvt_pk_fp8_f32 v88, v74, v75 op_sel:[0,0,1]
	s_waitcnt lgkmcnt(0)
	v_add_f32_e32 v74, v78, v79
	ds_bpermute_b32 v75, v141, v74
	v_pk_mul_f32 v[68:69], v[68:69], v[98:99] op_sel_hi:[1,0]
	v_med3_f32 v66, v66, s44, v181
	v_pk_fma_f32 v[68:69], v[68:69], v[72:73], v[84:85]
	v_med3_f32 v67, v67, s44, v181
	s_waitcnt lgkmcnt(0)
	v_add_f32_e32 v70, v74, v75
	ds_bpermute_b32 v71, v142, v70
	v_mov_b32_e32 v72, 0
	v_cvt_pk_fp8_f32 v72, v66, v67
	v_med3_f32 v68, v68, s44, v181
	v_med3_f32 v69, v69, s44, v181
	s_waitcnt lgkmcnt(0)
	v_add_f32_e32 v66, v70, v71
	v_fmamk_f32 v66, v66, 0x3a000000, v175
	v_mul_f32_e32 v67, 0x4f800000, v66
	v_cmp_gt_f32_e32 vcc, s43, v66
	v_cvt_pk_fp8_f32 v72, v68, v69 op_sel:[0,0,1]
	global_store_dword v[94:95], v90, off offset:1280
	global_store_dword v[94:95], v88, off offset:1536
	global_store_dword v[94:95], v72, off offset:1792
	v_cndmask_b32_e32 v66, v66, v67, vcc
	v_sqrt_f32_e32 v67, v66
	s_nop 0
	v_add_u32_e32 v68, -1, v67
	v_fma_f32 v69, -v68, v67, v66
	v_cmp_ge_f32_e64 s[0:1], 0, v69
	v_add_u32_e32 v69, 1, v67
	s_nop 0
	v_cndmask_b32_e64 v68, v67, v68, s[0:1]
	v_fma_f32 v67, -v69, v67, v66
	v_cmp_lt_f32_e64 s[0:1], 0, v67
	s_nop 1
	v_cndmask_b32_e64 v67, v68, v69, s[0:1]
	v_mul_f32_e32 v68, 0x37800000, v67
	v_cndmask_b32_e32 v67, v67, v68, vcc
	v_cmp_class_f32_e32 vcc, v66, v176
	s_nop 1
	v_cndmask_b32_e32 v66, v67, v66, vcc
	v_div_scale_f32 v67, s[0:1], v66, v66, 1.0
	v_rcp_f32_e32 v68, v67
	s_nop 0
	v_fma_f32 v69, -v67, v68, 1.0
	v_fmac_f32_e32 v68, v69, v68
	v_div_scale_f32 v69, vcc, 1.0, v66, 1.0
	v_mul_f32_e32 v70, v69, v68
	v_fma_f32 v71, -v67, v70, v69
	v_fmac_f32_e32 v70, v71, v68
	v_fma_f32 v67, -v67, v70, v69
	v_div_fmas_f32 v67, v67, v68, v70
	v_div_fixup_f32 v66, v67, v66, 1.0
	s_and_saveexec_b64 s[0:1], s[6:7]
	s_add_i32 s10, s39, 0
	s_add_i32 s10, s10, 0x20c08
	v_mov_b32_e32 v67, s10
	ds_write_b32 v67, v66
	s_or_b64 exec, exec, s[0:1]
	ds_read_b128 v[68:71], v143
	ds_read_b128 v[72:75], v143 offset:8192
	v_pk_mul_f32 v[62:63], v[62:63], v[66:67] op_sel_hi:[1,0]
	v_pk_mul_f32 v[64:65], v[64:65], v[66:67] op_sel_hi:[1,0]
	v_mov_b32_e32 v67, 0
	ds_read_b128 v[76:79], v143 offset:1024
	ds_read_b128 v[80:83], v143 offset:9216
	s_waitcnt lgkmcnt(2)
	v_pk_fma_f32 v[62:63], v[62:63], v[68:69], v[72:73]
	s_lshl_b64 s[0:1], s[4:5], 11
	v_med3_f32 v62, v62, s44, v181
	v_med3_f32 v63, v63, s44, v181
	v_cvt_pk_fp8_f32 v67, v62, v63
	v_pk_fma_f32 v[62:63], v[64:65], v[70:71], v[74:75]
	s_nop 0
	v_med3_f32 v62, v62, s44, v181
	v_med3_f32 v63, v63, s44, v181
	v_cvt_pk_fp8_f32 v67, v62, v63 op_sel:[0,0,1]
	v_lshl_add_u64 v[62:63], v[136:137], 0, s[0:1]
	v_pk_mul_f32 v[58:59], v[58:59], v[66:67] op_sel_hi:[1,0]
	s_waitcnt lgkmcnt(0)
	v_pk_fma_f32 v[58:59], v[58:59], v[76:77], v[80:81]
	global_store_dword v[62:63], v67, off
	v_pk_mul_f32 v[60:61], v[60:61], v[66:67] op_sel_hi:[1,0]
	v_med3_f32 v58, v58, s44, v181
	v_med3_f32 v59, v59, s44, v181
	v_mov_b32_e32 v67, 0
	v_cvt_pk_fp8_f32 v67, v58, v59
	v_pk_fma_f32 v[58:59], v[60:61], v[78:79], v[82:83]
	s_nop 0
	v_med3_f32 v58, v58, s44, v181
	v_med3_f32 v59, v59, s44, v181
	v_cvt_pk_fp8_f32 v67, v58, v59 op_sel:[0,0,1]
	ds_read_b128 v[58:61], v143 offset:2048
	ds_read_b128 v[68:71], v143 offset:10240
	v_pk_mul_f32 v[64:65], v[56:57], v[66:67] op_sel_hi:[1,0]
	v_pk_mul_f32 v[76:77], v[54:55], v[66:67] op_sel_hi:[1,0]
	ds_read_b128 v[54:57], v143 offset:3072
	ds_read_b128 v[72:75], v143 offset:11264
	s_waitcnt lgkmcnt(2)
	v_pk_fma_f32 v[58:59], v[76:77], v[58:59], v[68:69]
	v_pk_mul_f32 v[50:51], v[50:51], v[66:67] op_sel_hi:[1,0]
	v_med3_f32 v58, v58, s44, v181
	v_med3_f32 v59, v59, s44, v181
	v_mov_b32_e32 v76, 0
	s_waitcnt lgkmcnt(0)
	v_pk_fma_f32 v[50:51], v[50:51], v[54:55], v[72:73]
	v_cvt_pk_fp8_f32 v76, v58, v59
	v_pk_fma_f32 v[58:59], v[64:65], v[60:61], v[70:71]
	v_med3_f32 v50, v50, s44, v181
	v_med3_f32 v51, v51, s44, v181
	v_mov_b32_e32 v70, 0
	v_cvt_pk_fp8_f32 v70, v50, v51
	v_pk_mul_f32 v[52:53], v[52:53], v[66:67] op_sel_hi:[1,0]
	v_med3_f32 v58, v58, s44, v181
	v_pk_fma_f32 v[50:51], v[52:53], v[56:57], v[74:75]
	v_med3_f32 v59, v59, s44, v181
	v_med3_f32 v50, v50, s44, v181
	v_med3_f32 v51, v51, s44, v181
	v_cvt_pk_fp8_f32 v76, v58, v59 op_sel:[0,0,1]
	v_cvt_pk_fp8_f32 v70, v50, v51 op_sel:[0,0,1]
	ds_read_b128 v[50:53], v143 offset:4096
	ds_read_b128 v[54:57], v143 offset:12288
	v_pk_mul_f32 v[64:65], v[48:49], v[66:67] op_sel_hi:[1,0]
	v_pk_mul_f32 v[68:69], v[46:47], v[66:67] op_sel_hi:[1,0]
	ds_read_b128 v[46:49], v143 offset:5120
	ds_read_b128 v[58:61], v143 offset:13312
	v_pk_mul_f32 v[42:43], v[42:43], v[66:67] op_sel_hi:[1,0]
	s_waitcnt lgkmcnt(2)
	v_pk_fma_f32 v[50:51], v[68:69], v[50:51], v[54:55]
	v_mov_b32_e32 v54, 0
	v_med3_f32 v50, v50, s44, v181
	s_waitcnt lgkmcnt(0)
	v_pk_fma_f32 v[42:43], v[42:43], v[46:47], v[58:59]
	v_mov_b32_e32 v58, 0
	v_med3_f32 v42, v42, s44, v181
	v_med3_f32 v43, v43, s44, v181
	v_cvt_pk_fp8_f32 v58, v42, v43
	v_mul_f32_e32 v42, v31, v31
	v_mul_f32_e32 v43, v33, v33
	v_fmac_f32_e32 v42, v30, v30
	v_fmac_f32_e32 v43, v32, v32
	v_add_f32_e32 v42, v42, v43
	v_mul_f32_e32 v43, v27, v27
	v_mul_f32_e32 v46, v29, v29
	v_fmac_f32_e32 v43, v26, v26
	v_fmac_f32_e32 v46, v28, v28
	v_add_f32_e32 v43, v43, v46
	v_add_f32_e32 v42, v42, v43
	v_mul_f32_e32 v43, v23, v23
	v_mul_f32_e32 v46, v25, v25
	v_fmac_f32_e32 v43, v22, v22
	v_fmac_f32_e32 v46, v24, v24
	v_add_f32_e32 v43, v43, v46
	v_add_f32_e32 v42, v42, v43
	v_mul_f32_e32 v43, v19, v19
	v_mul_f32_e32 v46, v21, v21
	v_fmac_f32_e32 v43, v18, v18
	v_fmac_f32_e32 v46, v20, v20
	v_add_f32_e32 v43, v43, v46
	v_add_f32_e32 v42, v42, v43
	v_mul_f32_e32 v43, v15, v15
	v_mul_f32_e32 v46, v17, v17
	v_fmac_f32_e32 v43, v14, v14
	v_fmac_f32_e32 v46, v16, v16
	v_add_f32_e32 v43, v43, v46
	v_add_f32_e32 v42, v42, v43
	v_mul_f32_e32 v43, v11, v11
	v_mul_f32_e32 v46, v13, v13
	v_fmac_f32_e32 v43, v10, v10
	v_fmac_f32_e32 v46, v12, v12
	v_add_f32_e32 v43, v43, v46
	v_add_f32_e32 v42, v42, v43
	v_mul_f32_e32 v43, v7, v7
	v_mul_f32_e32 v46, v9, v9
	v_med3_f32 v51, v51, s44, v181
	v_fmac_f32_e32 v43, v6, v6
	v_fmac_f32_e32 v46, v8, v8
	v_cvt_pk_fp8_f32 v54, v50, v51
	v_add_f32_e32 v43, v43, v46
	v_add_f32_e32 v42, v42, v43
	v_mul_f32_e32 v43, v3, v3
	v_mul_f32_e32 v46, v5, v5
	v_pk_fma_f32 v[50:51], v[64:65], v[52:53], v[56:57]
	v_fmac_f32_e32 v43, v2, v2
	v_fmac_f32_e32 v46, v4, v4
	v_med3_f32 v50, v50, s44, v181
	v_med3_f32 v51, v51, s44, v181
	v_add_f32_e32 v43, v43, v46
	v_cvt_pk_fp8_f32 v54, v50, v51 op_sel:[0,0,1]
	v_add_f32_e32 v50, v42, v43
	ds_bpermute_b32 v51, v1, v50
	v_pk_mul_f32 v[44:45], v[44:45], v[66:67] op_sel_hi:[1,0]
	global_store_dword v[62:63], v67, off offset:256
	global_store_dword v[62:63], v76, off offset:512
	global_store_dword v[62:63], v70, off offset:768
	global_store_dword v[62:63], v54, off offset:1024
	v_pk_fma_f32 v[44:45], v[44:45], v[48:49], v[60:61]
	v_pk_mul_f32 v[56:57], v[38:39], v[66:67] op_sel_hi:[1,0]
	v_med3_f32 v44, v44, s44, v181
	v_med3_f32 v45, v45, s44, v181
	s_waitcnt lgkmcnt(0)
	v_add_f32_e32 v59, v50, v51
	v_cvt_pk_fp8_f32 v58, v44, v45 op_sel:[0,0,1]
	ds_read_b128 v[42:45], v143 offset:6144
	ds_read_b128 v[46:49], v143 offset:14336
	ds_bpermute_b32 v60, v138, v59
	v_pk_mul_f32 v[54:55], v[40:41], v[66:67] op_sel_hi:[1,0]
	ds_read_b128 v[38:41], v143 offset:7168
	ds_read_b128 v[50:53], v143 offset:15360
	v_pk_mul_f32 v[34:35], v[34:35], v[66:67] op_sel_hi:[1,0]
	s_waitcnt lgkmcnt(3)
	v_pk_fma_f32 v[42:43], v[56:57], v[42:43], v[46:47]
	s_waitcnt lgkmcnt(2)
	v_add_f32_e32 v46, v59, v60
	ds_bpermute_b32 v47, v139, v46
	v_med3_f32 v42, v42, s44, v181
	v_med3_f32 v43, v43, s44, v181
	v_mov_b32_e32 v56, 0
	v_cvt_pk_fp8_f32 v56, v42, v43
	s_waitcnt lgkmcnt(0)
	v_add_f32_e32 v46, v46, v47
	ds_bpermute_b32 v47, v140, v46
	v_pk_fma_f32 v[42:43], v[54:55], v[44:45], v[48:49]
	v_pk_fma_f32 v[34:35], v[34:35], v[38:39], v[50:51]
	v_med3_f32 v42, v42, s44, v181
	v_med3_f32 v43, v43, s44, v181
	v_cvt_pk_fp8_f32 v56, v42, v43 op_sel:[0,0,1]
	s_waitcnt lgkmcnt(0)
	v_add_f32_e32 v42, v46, v47
	ds_bpermute_b32 v43, v141, v42
	v_pk_mul_f32 v[36:37], v[36:37], v[66:67] op_sel_hi:[1,0]
	v_med3_f32 v34, v34, s44, v181
	v_pk_fma_f32 v[36:37], v[36:37], v[40:41], v[52:53]
	v_med3_f32 v35, v35, s44, v181
	s_waitcnt lgkmcnt(0)
	v_add_f32_e32 v38, v42, v43
	ds_bpermute_b32 v39, v142, v38
	v_mov_b32_e32 v40, 0
	v_cvt_pk_fp8_f32 v40, v34, v35
	v_med3_f32 v36, v36, s44, v181
	v_med3_f32 v37, v37, s44, v181
	s_waitcnt lgkmcnt(0)
	v_add_f32_e32 v34, v38, v39
	v_fmamk_f32 v34, v34, 0x3a000000, v175
	v_mul_f32_e32 v35, 0x4f800000, v34
	v_cmp_gt_f32_e32 vcc, s43, v34
	v_cvt_pk_fp8_f32 v40, v36, v37 op_sel:[0,0,1]
	global_store_dword v[62:63], v58, off offset:1280
	global_store_dword v[62:63], v56, off offset:1536
	global_store_dword v[62:63], v40, off offset:1792
	v_cndmask_b32_e32 v34, v34, v35, vcc
	v_sqrt_f32_e32 v35, v34
	s_nop 0
	v_add_u32_e32 v36, -1, v35
	v_fma_f32 v37, -v36, v35, v34
	v_cmp_ge_f32_e64 s[0:1], 0, v37
	v_add_u32_e32 v37, 1, v35
	s_nop 0
	v_cndmask_b32_e64 v36, v35, v36, s[0:1]
	v_fma_f32 v35, -v37, v35, v34
	v_cmp_lt_f32_e64 s[0:1], 0, v35
	s_nop 1
	v_cndmask_b32_e64 v35, v36, v37, s[0:1]
	v_mul_f32_e32 v36, 0x37800000, v35
	v_cndmask_b32_e32 v35, v35, v36, vcc
	v_cmp_class_f32_e32 vcc, v34, v176
	s_nop 1
	v_cndmask_b32_e32 v34, v35, v34, vcc
	v_div_scale_f32 v35, s[0:1], v34, v34, 1.0
	v_rcp_f32_e32 v36, v35
	s_nop 0
	v_fma_f32 v37, -v35, v36, 1.0
	v_fmac_f32_e32 v36, v37, v36
	v_div_scale_f32 v37, vcc, 1.0, v34, 1.0
	v_mul_f32_e32 v38, v37, v36
	v_fma_f32 v39, -v35, v38, v37
	v_fmac_f32_e32 v38, v39, v36
	v_fma_f32 v35, -v35, v38, v37
	v_div_fmas_f32 v35, v35, v36, v38
	v_div_fixup_f32 v34, v35, v34, 1.0
	s_and_saveexec_b64 s[0:1], s[6:7]
	s_add_i32 s4, s39, 0
	s_add_i32 s4, s4, 0x20c0c
	v_mov_b32_e32 v35, s4
	ds_write_b32 v35, v34
	s_or_b64 exec, exec, s[0:1]
	ds_read_b128 v[36:39], v143
	ds_read_b128 v[40:43], v143 offset:8192
	v_pk_mul_f32 v[52:53], v[30:31], v[34:35] op_sel_hi:[1,0]
	v_pk_mul_f32 v[50:51], v[32:33], v[34:35] op_sel_hi:[1,0]
	ds_read_b128 v[30:33], v143 offset:1024
	ds_read_b128 v[44:47], v143 offset:9216
	s_lshl_b64 s[0:1], s[2:3], 11
	s_waitcnt lgkmcnt(2)
	v_pk_fma_f32 v[36:37], v[52:53], v[36:37], v[40:41]
	v_mov_b32_e32 v52, 0
	v_med3_f32 v35, v36, s44, v181
	v_med3_f32 v36, v37, s44, v181
	v_cvt_pk_fp8_f32 v52, v35, v36
	v_pk_fma_f32 v[36:37], v[50:51], v[38:39], v[42:43]
	v_lshl_add_u64 v[48:49], v[136:137], 0, s[0:1]
	v_med3_f32 v35, v36, s44, v181
	v_pk_mul_f32 v[26:27], v[26:27], v[34:35] op_sel_hi:[1,0]
	v_med3_f32 v36, v37, s44, v181
	s_waitcnt lgkmcnt(0)
	v_pk_fma_f32 v[26:27], v[26:27], v[30:31], v[44:45]
	v_cvt_pk_fp8_f32 v52, v35, v36 op_sel:[0,0,1]
	v_pk_mul_f32 v[28:29], v[28:29], v[34:35] op_sel_hi:[1,0]
	v_med3_f32 v26, v26, s44, v181
	v_med3_f32 v27, v27, s44, v181
	v_mov_b32_e32 v35, 0
	v_cvt_pk_fp8_f32 v35, v26, v27
	v_pk_fma_f32 v[26:27], v[28:29], v[32:33], v[46:47]
	v_mov_b32_e32 v122, 0
	v_med3_f32 v26, v26, s44, v181
	v_med3_f32 v27, v27, s44, v181
	v_cvt_pk_fp8_f32 v35, v26, v27 op_sel:[0,0,1]
	ds_read_b128 v[26:29], v143 offset:2048
	ds_read_b128 v[30:33], v143 offset:10240
	s_mov_b32 s4, 0
	s_mov_b32 s5, 0
	v_pk_mul_f32 v[40:41], v[24:25], v[34:35] op_sel_hi:[1,0]
	v_pk_mul_f32 v[42:43], v[22:23], v[34:35] op_sel_hi:[1,0]
	ds_read_b128 v[22:25], v143 offset:3072
	ds_read_b128 v[36:39], v143 offset:11264
	s_waitcnt lgkmcnt(2)
	v_pk_fma_f32 v[26:27], v[42:43], v[26:27], v[30:31]
	v_pk_mul_f32 v[18:19], v[18:19], v[34:35] op_sel_hi:[1,0]
	v_med3_f32 v26, v26, s44, v181
	v_med3_f32 v27, v27, s44, v181
	v_mov_b32_e32 v30, 0
	s_waitcnt lgkmcnt(0)
	v_pk_fma_f32 v[18:19], v[18:19], v[22:23], v[36:37]
	v_cvt_pk_fp8_f32 v30, v26, v27
	v_med3_f32 v18, v18, s44, v181
	v_med3_f32 v19, v19, s44, v181
	v_mov_b32_e32 v22, 0
	v_cvt_pk_fp8_f32 v22, v18, v19
	v_pk_fma_f32 v[26:27], v[40:41], v[28:29], v[32:33]
	v_pk_mul_f32 v[20:21], v[20:21], v[34:35] op_sel_hi:[1,0]
	v_med3_f32 v26, v26, s44, v181
	v_med3_f32 v27, v27, s44, v181
	v_pk_fma_f32 v[18:19], v[20:21], v[24:25], v[38:39]
	v_cvt_pk_fp8_f32 v30, v26, v27 op_sel:[0,0,1]
	v_med3_f32 v18, v18, s44, v181
	v_med3_f32 v19, v19, s44, v181
	v_cvt_pk_fp8_f32 v22, v18, v19 op_sel:[0,0,1]
	global_store_dword v[48:49], v52, off
	global_store_dword v[48:49], v35, off offset:256
	global_store_dword v[48:49], v30, off offset:512
	global_store_dword v[48:49], v22, off offset:768
	ds_read_b128 v[18:21], v143 offset:4096
	ds_read_b128 v[22:25], v143 offset:12288
	v_pk_mul_f32 v[30:31], v[16:17], v[34:35] op_sel_hi:[1,0]
	v_pk_mul_f32 v[32:33], v[14:15], v[34:35] op_sel_hi:[1,0]
	ds_read_b128 v[14:17], v143 offset:5120
	ds_read_b128 v[26:29], v143 offset:13312
	v_pk_mul_f32 v[10:11], v[10:11], v[34:35] op_sel_hi:[1,0]
	s_waitcnt lgkmcnt(2)
	v_pk_fma_f32 v[18:19], v[32:33], v[18:19], v[22:23]
	v_mov_b32_e32 v32, 0
	v_med3_f32 v18, v18, s44, v181
	s_waitcnt lgkmcnt(0)
	v_pk_fma_f32 v[10:11], v[10:11], v[14:15], v[26:27]
	v_mov_b32_e32 v26, 0
	v_med3_f32 v10, v10, s44, v181
	v_med3_f32 v11, v11, s44, v181
	v_med3_f32 v19, v19, s44, v181
	v_cvt_pk_fp8_f32 v26, v10, v11
	v_cvt_pk_fp8_f32 v32, v18, v19
	v_pk_mul_f32 v[12:13], v[12:13], v[34:35] op_sel_hi:[1,0]
	v_pk_fma_f32 v[18:19], v[30:31], v[20:21], v[24:25]
	v_pk_fma_f32 v[10:11], v[12:13], v[16:17], v[28:29]
	v_med3_f32 v18, v18, s44, v181
	v_med3_f32 v10, v10, s44, v181
	v_med3_f32 v11, v11, s44, v181
	v_med3_f32 v19, v19, s44, v181
	v_cvt_pk_fp8_f32 v26, v10, v11 op_sel:[0,0,1]
	ds_read_b128 v[10:13], v143 offset:6144
	ds_read_b128 v[14:17], v143 offset:14336
	v_cvt_pk_fp8_f32 v32, v18, v19 op_sel:[0,0,1]
	v_pk_mul_f32 v[22:23], v[8:9], v[34:35] op_sel_hi:[1,0]
	v_pk_mul_f32 v[24:25], v[6:7], v[34:35] op_sel_hi:[1,0]
	ds_read_b128 v[6:9], v143 offset:7168
	ds_read_b128 v[18:21], v143 offset:15360
	s_waitcnt lgkmcnt(2)
	v_pk_fma_f32 v[10:11], v[24:25], v[10:11], v[14:15]
	v_pk_mul_f32 v[2:3], v[2:3], v[34:35] op_sel_hi:[1,0]
	v_med3_f32 v10, v10, s44, v181
	v_med3_f32 v11, v11, s44, v181
	v_mov_b32_e32 v14, 0
	s_waitcnt lgkmcnt(0)
	v_pk_fma_f32 v[2:3], v[2:3], v[6:7], v[18:19]
	v_cvt_pk_fp8_f32 v14, v10, v11
	v_med3_f32 v2, v2, s44, v181
	v_med3_f32 v3, v3, s44, v181
	v_mov_b32_e32 v6, 0
	v_cvt_pk_fp8_f32 v6, v2, v3
	v_pk_fma_f32 v[10:11], v[22:23], v[12:13], v[16:17]
	v_pk_mul_f32 v[4:5], v[4:5], v[34:35] op_sel_hi:[1,0]
	v_med3_f32 v10, v10, s44, v181
	v_med3_f32 v11, v11, s44, v181
	v_pk_fma_f32 v[2:3], v[4:5], v[8:9], v[20:21]
	v_cvt_pk_fp8_f32 v14, v10, v11 op_sel:[0,0,1]
	v_med3_f32 v2, v2, s44, v181
	v_med3_f32 v3, v3, s44, v181
	v_cvt_pk_fp8_f32 v6, v2, v3 op_sel:[0,0,1]
	v_mov_b32_e32 v2, v0
	global_store_dword v[48:49], v32, off offset:1024
	global_store_dword v[48:49], v26, off offset:1280
	global_store_dword v[48:49], v14, off offset:1536
	global_store_dword v[48:49], v6, off offset:1792
	s_barrier
	v_mov_b32_e32 v123, v122
	v_lshrrev_b32_e32 v98, 6, v2
	v_lshlrev_b32_e32 v4, 4, v2
	v_add_u32_e32 v3, s55, v98
	v_and_b32_e32 v99, 0x3f0, v4
	v_lshl_or_b32 v86, v3, 13, v99
	v_lshlrev_b32_e32 v2, 7, v2
	v_and_b32_e32 v3, 0x1f0, v4
	v_and_or_b32 v100, v2, s45, v3
	v_add_u32_e32 v10, 0x10000, v86
	v_add_u32_e32 v18, 0x10000, v100
	v_add_u32_e32 v22, 0x20000, v86
	global_load_dwordx4 v[2:5], v100, s[30:31]
	global_load_dwordx4 v[6:9], v100, s[34:35]
	v_or_b32_e32 v46, 0x200, v100
	global_load_dwordx4 v[10:13], v10, s[48:49]
	s_nop 0
	global_load_dwordx4 v[14:17], v18, s[30:31]
	s_nop 0
	global_load_dwordx4 v[18:21], v18, s[34:35]
	v_add_u32_e32 v54, 0x10400, v86
	global_load_dwordx4 v[26:29], v22, s[48:49]
	v_add_u32_e32 v22, 0x20000, v100
	global_load_dwordx4 v[34:37], v22, s[30:31]
	global_load_dwordx4 v[42:45], v22, s[34:35]
	v_add_u32_e32 v22, 0x30000, v86
	global_load_dwordx4 v[50:53], v22, s[48:49]
	v_add_u32_e32 v22, 0x30000, v100
	global_load_dwordx4 v[58:61], v22, s[30:31]
	global_load_dwordx4 v[66:69], v22, s[34:35]
	s_nop 0
	global_load_dwordx4 v[22:25], v86, s[48:49]
	global_load_dwordx4 v[30:33], v86, s[48:49] offset:1024
	v_add_u32_e32 v70, 0x10200, v100
	v_add_u32_e32 v74, 0x20400, v86
	v_add_u32_e32 v82, 0x20200, v100
	v_add_u32_e32 v86, 0x30400, v86
	v_add_u32_e32 v94, 0x30200, v100
	global_load_dwordx4 v[38:41], v46, s[30:31]
	s_nop 0
	global_load_dwordx4 v[46:49], v46, s[34:35]
	v_lshlrev_b32_e32 v98, 13, v98
	global_load_dwordx4 v[54:57], v54, s[48:49]
	s_nop 0
	global_load_dwordx4 v[62:65], v70, s[30:31]
	s_nop 0
	global_load_dwordx4 v[70:73], v70, s[34:35]
	v_add_u32_e32 v130, 0x30600, v100
	global_load_dwordx4 v[74:77], v74, s[48:49]
	s_nop 0
	global_load_dwordx4 v[78:81], v82, s[30:31]
	s_nop 0
	global_load_dwordx4 v[82:85], v82, s[34:35]
	v_add3_u32 v182, s40, v98, v99
	global_load_dwordx4 v[86:89], v86, s[48:49]
	s_nop 0
	global_load_dwordx4 v[90:93], v94, s[30:31]
	s_nop 0
	global_load_dwordx4 v[94:97], v94, s[34:35]
	v_mov_b32_e32 v124, v122
	v_mov_b32_e32 v125, v122
	v_mov_b32_e32 v118, v122
	v_mov_b32_e32 v119, v122
	v_mov_b32_e32 v120, v122
	v_mov_b32_e32 v121, v122
	v_mov_b32_e32 v110, v122
	v_mov_b32_e32 v111, v122
	v_mov_b32_e32 v112, v122
	v_mov_b32_e32 v113, v122
	v_mov_b32_e32 v98, v122
	v_mov_b32_e32 v99, v122
	v_mov_b32_e32 v100, v122
	v_mov_b32_e32 v101, v122
	v_mov_b32_e32 v126, v122
	v_mov_b32_e32 v127, v122
	v_mov_b32_e32 v128, v122
	v_mov_b32_e32 v129, v122
	v_mov_b32_e32 v114, v122
	v_mov_b32_e32 v115, v122
	v_mov_b32_e32 v116, v122
	v_mov_b32_e32 v117, v122
	v_mov_b32_e32 v102, v122
	v_mov_b32_e32 v103, v122
	v_mov_b32_e32 v104, v122
	v_mov_b32_e32 v105, v122
	v_mov_b32_e32 v106, v122
	v_mov_b32_e32 v107, v122
	v_mov_b32_e32 v108, v122
	v_mov_b32_e32 v109, v122
	s_branch .LBB0_1226
